# P7: LayerNorm instances 2 and 4 no longer drain the previous row's stores before normalising (their gamma/beta are already resident); rest as previous
# baseline (speedup 1.0000x reference)
; __global__ void __launch_bounds__(NTHREADS, 2) hybrid_fwd(Args a) {
;     ...
;             for (int v = bid; v < 256; v += G) {
;                 u32x2 raw[2][8];
; #pragma unroll
;                 for (int q = 0; q < 2; ++q)
; #pragma unroll
;                     for (int j = 0; j < 8; ++j) raw[q][j] = __builtin_nontemporal_load((const u32x2*)(YB + (size_t)(v * 32 + wave + 8 * q) * DM + j * 256 + lane * 4));
;                 __syncthreads();
;                 if (tid < 16) hist[tid] = 0;
;                 __syncthreads();
;                 asm volatile("s_waitcnt vmcnt(0)" ::: "memory"); __syncthreads();
.LBB0_887:
	s_add_i32 s6, s22, s51
	s_ashr_i32 s7, s6, 31
	s_add_i32 s8, s6, 8
	s_lshl_b64 s[12:13], s[6:7], 12
	s_ashr_i32 s9, s8, 31
	v_lshl_add_u64 v[16:17], v[26:27], 0, s[12:13]
	s_lshl_b64 s[10:11], s[8:9], 12
	flat_load_dwordx2 v[58:59], v[16:17] nt
	flat_load_dwordx2 v[56:57], v[16:17] offset:512 nt
	flat_load_dwordx2 v[54:55], v[16:17] offset:1024 nt
	flat_load_dwordx2 v[52:53], v[16:17] offset:1536 nt
	flat_load_dwordx2 v[50:51], v[16:17] offset:2048 nt
	flat_load_dwordx2 v[48:49], v[16:17] offset:2560 nt
	flat_load_dwordx2 v[46:47], v[16:17] offset:3072 nt
	flat_load_dwordx2 v[44:45], v[16:17] offset:3584 nt
	v_lshl_add_u64 v[16:17], v[26:27], 0, s[10:11]
	flat_load_dwordx2 v[42:43], v[16:17] nt
	flat_load_dwordx2 v[40:41], v[16:17] offset:512 nt
	flat_load_dwordx2 v[38:39], v[16:17] offset:1024 nt
	flat_load_dwordx2 v[36:37], v[16:17] offset:1536 nt
	flat_load_dwordx2 v[22:23], v[16:17] offset:2048 nt
	flat_load_dwordx2 v[20:21], v[16:17] offset:2560 nt
	flat_load_dwordx2 v[18:19], v[16:17] offset:3072 nt
	s_nop 0
	flat_load_dwordx2 v[16:17], v[16:17] offset:3584 nt
	s_waitcnt vmcnt(0) lgkmcnt(0)
	s_barrier
	s_and_saveexec_b64 s[14:15], s[0:1]
	ds_write_b32 v156, v193
	s_or_b64 exec, exec, s[14:15]
	s_waitcnt lgkmcnt(0)
	s_barrier
	s_waitcnt vmcnt(0)
	s_add_i32 s38, s6, 16
	s_barrier
	s_mov_b64 s[14:15], s[34:35]
	v_lshlrev_b32_e32 v192, 2, v24
	s_mov_b64 s[16:17], s[36:37]
	v_lshl_add_u64 v[94:95], s[14:15], 0, v[192:193]
	v_lshlrev_b32_e32 v66, 16, v58
	v_lshl_add_u64 v[96:97], s[16:17], 0, v[192:193]
	s_nop 0
	v_and_b32_e32 v67, 0xffff0000, v58
	v_lshlrev_b32_e32 v64, 16, v59
	v_and_b32_e32 v65, 0xffff0000, v59
	v_add_f32_e32 v35, v66, v67
	v_add_f32_e32 v58, v64, v65
	v_lshlrev_b32_e32 v74, 16, v56
	v_and_b32_e32 v75, 0xffff0000, v56
	v_lshlrev_b32_e32 v72, 16, v57
	v_and_b32_e32 v73, 0xffff0000, v57
	v_add_f32_e32 v35, v35, v58
	v_add_f32_e32 v56, v74, v75
	v_add_f32_e32 v57, v72, v73
	v_lshlrev_b32_e32 v68, 16, v54
	v_and_b32_e32 v69, 0xffff0000, v54
	v_lshlrev_b32_e32 v70, 16, v55
	v_and_b32_e32 v71, 0xffff0000, v55
	v_add_f32_e32 v35, 0, v35
	v_add_f32_e32 v56, v56, v57
	v_add_f32_e32 v54, v68, v69
	v_add_f32_e32 v55, v70, v71
	v_lshlrev_b32_e32 v60, 16, v52
	v_and_b32_e32 v61, 0xffff0000, v52
	v_lshlrev_b32_e32 v62, 16, v53
	v_and_b32_e32 v63, 0xffff0000, v53
	v_add_f32_e32 v35, v35, v56
	v_add_f32_e32 v54, v54, v55
	v_add_f32_e32 v52, v60, v61
	v_add_f32_e32 v53, v62, v63
	v_add_f32_e32 v35, v35, v54
	v_add_f32_e32 v52, v52, v53
	v_lshlrev_b32_e32 v56, 16, v50
	v_and_b32_e32 v57, 0xffff0000, v50
	v_lshlrev_b32_e32 v58, 16, v51
	v_and_b32_e32 v59, 0xffff0000, v51
	v_add_f32_e32 v35, v35, v52
	v_add_f32_e32 v50, v56, v57
	v_add_f32_e32 v51, v58, v59
	v_lshlrev_b32_e32 v52, 16, v48
	v_and_b32_e32 v53, 0xffff0000, v48
	v_lshlrev_b32_e32 v54, 16, v49
	v_and_b32_e32 v55, 0xffff0000, v49
	v_add_f32_e32 v50, v50, v51
	v_add_f32_e32 v48, v52, v53
	v_add_f32_e32 v49, v54, v55
	v_add_f32_e32 v35, v35, v50
	v_add_f32_e32 v48, v48, v49
	v_add_f32_e32 v35, v35, v48
	v_lshlrev_b32_e32 v48, 16, v46
	v_and_b32_e32 v49, 0xffff0000, v46
	v_lshlrev_b32_e32 v50, 16, v47
	v_and_b32_e32 v51, 0xffff0000, v47
	v_add_f32_e32 v46, v48, v49
	v_add_f32_e32 v47, v50, v51
	v_add_f32_e32 v46, v46, v47
	v_add_f32_e32 v35, v35, v46
	v_lshlrev_b32_e32 v46, 16, v44
	v_and_b32_e32 v47, 0xffff0000, v44
	v_lshlrev_b32_e32 v44, 16, v45
	v_and_b32_e32 v45, 0xffff0000, v45
	v_add_f32_e32 v76, v46, v47
	v_add_f32_e32 v77, v44, v45
	v_add_f32_e32 v76, v76, v77
	v_add_f32_e32 v35, v35, v76
	s_lshl_b64 s[14:15], s[6:7], 11
	s_nop 0
	v_add_f32_dpp v35, v35, v35 quad_perm:[1,0,3,2] row_mask:0xf bank_mask:0xf bound_ctrl:1
	s_nop 1
	v_add_f32_dpp v35, v35, v35 quad_perm:[2,3,0,1] row_mask:0xf bank_mask:0xf bound_ctrl:1
	s_nop 1
	v_add_f32_dpp v35, v35, v35 row_ror:4 row_mask:0xf bank_mask:0xf bound_ctrl:1
	s_nop 1
	v_add_f32_dpp v35, v35, v35 row_ror:8 row_mask:0xf bank_mask:0xf bound_ctrl:1
	v_mov_b32_e32 v76, v35
	s_nop 1
	v_permlane16_swap_b32_e32 v35, v76
	v_add_f32_e32 v35, v35, v76
	v_mov_b32_e32 v76, v35
	s_nop 1
	v_permlane32_swap_b32_e32 v35, v76
	v_add_f32_e32 v35, v35, v76
	v_fmac_f32_e32 v65, 0xba000000, v35
	v_fmac_f32_e32 v67, 0xba000000, v35
	v_fmac_f32_e32 v64, 0xba000000, v35
	v_fmac_f32_e32 v66, 0xba000000, v35
	v_mul_f32_e32 v76, v67, v67
	v_mul_f32_e32 v77, v65, v65
	v_fmac_f32_e32 v76, v66, v66
	v_fmac_f32_e32 v77, v64, v64
	v_fmac_f32_e32 v73, 0xba000000, v35
	v_fmac_f32_e32 v75, 0xba000000, v35
	v_add_f32_e32 v76, v76, v77
	v_fmac_f32_e32 v72, 0xba000000, v35
	v_fmac_f32_e32 v74, 0xba000000, v35
	v_mul_f32_e32 v77, v75, v75
	v_mul_f32_e32 v78, v73, v73
	v_fmac_f32_e32 v77, v74, v74
	v_fmac_f32_e32 v78, v72, v72
	v_add_f32_e32 v77, v77, v78
	v_fmac_f32_e32 v71, 0xba000000, v35
	v_fmac_f32_e32 v69, 0xba000000, v35
	v_add_f32_e32 v76, v76, v77
	v_fmac_f32_e32 v70, 0xba000000, v35
	v_fmac_f32_e32 v68, 0xba000000, v35
	v_mul_f32_e32 v77, v69, v69
	v_mul_f32_e32 v78, v71, v71
	v_fmac_f32_e32 v77, v68, v68
	v_fmac_f32_e32 v78, v70, v70
	v_add_f32_e32 v77, v77, v78
	v_fmac_f32_e32 v63, 0xba000000, v35
	v_fmac_f32_e32 v61, 0xba000000, v35
	v_add_f32_e32 v76, v76, v77
	v_fmac_f32_e32 v62, 0xba000000, v35
	v_fmac_f32_e32 v60, 0xba000000, v35
	v_mul_f32_e32 v77, v61, v61
	v_mul_f32_e32 v78, v63, v63
	v_fmac_f32_e32 v77, v60, v60
	v_fmac_f32_e32 v78, v62, v62
	v_add_f32_e32 v77, v77, v78
	v_fmac_f32_e32 v59, 0xba000000, v35
	v_fmac_f32_e32 v57, 0xba000000, v35
	v_add_f32_e32 v76, v76, v77
	v_fmac_f32_e32 v58, 0xba000000, v35
	v_fmac_f32_e32 v56, 0xba000000, v35
	v_mul_f32_e32 v77, v57, v57
	v_mul_f32_e32 v78, v59, v59
	v_fmac_f32_e32 v77, v56, v56
	v_fmac_f32_e32 v78, v58, v58
	v_add_f32_e32 v77, v77, v78
	v_fmac_f32_e32 v55, 0xba000000, v35
	v_fmac_f32_e32 v53, 0xba000000, v35
	v_add_f32_e32 v76, v76, v77
	v_fmac_f32_e32 v54, 0xba000000, v35
	v_fmac_f32_e32 v52, 0xba000000, v35
	v_mul_f32_e32 v77, v53, v53
	v_mul_f32_e32 v78, v55, v55
	v_fmac_f32_e32 v77, v52, v52
	v_fmac_f32_e32 v78, v54, v54
	v_add_f32_e32 v77, v77, v78
	v_fmac_f32_e32 v51, 0xba000000, v35
	v_fmac_f32_e32 v49, 0xba000000, v35
	v_add_f32_e32 v76, v76, v77
	v_fmac_f32_e32 v50, 0xba000000, v35
	v_fmac_f32_e32 v48, 0xba000000, v35
	v_mul_f32_e32 v77, v49, v49
	v_mul_f32_e32 v78, v51, v51
	v_fmac_f32_e32 v77, v48, v48
	v_fmac_f32_e32 v78, v50, v50
	v_add_f32_e32 v77, v77, v78
	v_fmac_f32_e32 v45, 0xba000000, v35
	v_fmac_f32_e32 v47, 0xba000000, v35
	v_add_f32_e32 v76, v76, v77
	v_fmac_f32_e32 v44, 0xba000000, v35
	v_fmac_f32_e32 v46, 0xba000000, v35
	v_mul_f32_e32 v35, v47, v47
	v_mul_f32_e32 v77, v45, v45
	v_fmac_f32_e32 v35, v46, v46
	v_fmac_f32_e32 v77, v44, v44
	v_add_f32_e32 v35, v35, v77
	v_add_f32_e32 v35, v76, v35
	v_lshl_add_u64 v[78:79], v[30:31], 0, s[14:15]
	s_nop 0
	v_add_f32_dpp v35, v35, v35 quad_perm:[1,0,3,2] row_mask:0xf bank_mask:0xf bound_ctrl:1
	s_nop 1
	v_add_f32_dpp v35, v35, v35 quad_perm:[2,3,0,1] row_mask:0xf bank_mask:0xf bound_ctrl:1
	s_nop 1
	v_add_f32_dpp v35, v35, v35 row_ror:4 row_mask:0xf bank_mask:0xf bound_ctrl:1
	s_nop 1
	v_add_f32_dpp v35, v35, v35 row_ror:8 row_mask:0xf bank_mask:0xf bound_ctrl:1
	v_mov_b32_e32 v76, v35
	s_nop 1
	v_permlane16_swap_b32_e32 v35, v76
	v_add_f32_e32 v35, v35, v76
	v_mov_b32_e32 v76, v35
	s_nop 1
	v_permlane32_swap_b32_e32 v35, v76
	v_add_f32_e32 v35, v35, v76
	v_fmamk_f32 v35, v35, 0x3a000000, v207
	v_rsq_f32_e32 v84, v35
	v_lshl_add_u64 v[76:77], v[28:29], 0, s[12:13]
	v_pk_mul_f32 v[66:67], v[84:85], v[66:67] op_sel_hi:[0,1]
	v_pk_mul_f32 v[90:91], v[84:85], v[64:65] op_sel_hi:[0,1]
	s_waitcnt vmcnt(0) lgkmcnt(0)
	v_pk_fma_f32 v[64:65], v[158:159], v[66:67], v[198:199]
	v_mov_b32_e32 v85, 0
	v_med3_f32 v35, v64, s69, v208
	v_med3_f32 v66, v65, s69, v208
	v_cvt_pk_fp8_f32 v85, v35, v66
	v_pk_fma_f32 v[66:67], v[160:161], v[90:91], v[200:201]
	s_nop 0
	v_med3_f32 v35, v66, s69, v208
	v_med3_f32 v80, v67, s69, v208
	v_cvt_pk_fp8_f32 v85, v35, v80 op_sel:[0,0,1]
	v_cvt_pk_bf16_f32 v80, v64, v65
	v_cvt_pk_bf16_f32 v81, v66, v67
	global_store_dwordx2 v[76:77], v[80:81], off nt
	global_store_dword v[78:79], v85, off nt
	s_nop 0
	s_nop 0
	v_pk_mul_f32 v[74:75], v[84:85], v[74:75] op_sel_hi:[0,1]
	v_pk_mul_f32 v[90:91], v[84:85], v[72:73] op_sel_hi:[0,1]
	v_mov_b32_e32 v85, 0
	s_nop 0
	v_pk_fma_f32 v[72:73], v[162:163], v[74:75], v[202:203]
	s_nop 0
	v_med3_f32 v35, v72, s69, v208
	v_med3_f32 v74, v73, s69, v208
	v_cvt_pk_fp8_f32 v85, v35, v74
	v_pk_fma_f32 v[74:75], v[164:165], v[90:91], v[204:205]
	s_nop 0
	v_med3_f32 v35, v74, s69, v208
	v_med3_f32 v80, v75, s69, v208
	v_cvt_pk_fp8_f32 v85, v35, v80 op_sel:[0,0,1]
	v_cvt_pk_bf16_f32 v80, v72, v73
	v_cvt_pk_bf16_f32 v81, v74, v75
	global_store_dwordx2 v[76:77], v[80:81], off offset:512 nt
	global_store_dword v[78:79], v85, off offset:256 nt
	s_nop 0
	v_pk_mul_f32 v[68:69], v[84:85], v[68:69] op_sel_hi:[0,1]
	v_mov_b32_e32 v35, 0
	v_pk_mul_f32 v[70:71], v[84:85], v[70:71] op_sel_hi:[0,1]
	v_pk_mul_f32 v[60:61], v[84:85], v[60:61] op_sel_hi:[0,1]
	v_pk_mul_f32 v[62:63], v[84:85], v[62:63] op_sel_hi:[0,1]
	v_pk_mul_f32 v[56:57], v[84:85], v[56:57] op_sel_hi:[0,1]
	v_pk_mul_f32 v[58:59], v[84:85], v[58:59] op_sel_hi:[0,1]
	v_pk_mul_f32 v[52:53], v[84:85], v[52:53] op_sel_hi:[0,1]
	v_pk_mul_f32 v[54:55], v[84:85], v[54:55] op_sel_hi:[0,1]
	v_pk_mul_f32 v[48:49], v[84:85], v[48:49] op_sel_hi:[0,1]
	v_pk_mul_f32 v[50:51], v[84:85], v[50:51] op_sel_hi:[0,1]
	v_pk_mul_f32 v[46:47], v[84:85], v[46:47] op_sel_hi:[0,1]
	v_pk_mul_f32 v[44:45], v[84:85], v[44:45] op_sel_hi:[0,1]
	s_nop 0
	v_pk_fma_f32 v[82:83], v[166:167], v[68:69], v[216:217]
	s_nop 0
	v_med3_f32 v68, v82, s69, v208
	v_med3_f32 v69, v83, s69, v208
	v_cvt_pk_fp8_f32 v35, v68, v69
	v_pk_fma_f32 v[80:81], v[168:169], v[70:71], v[218:219]
	v_add_co_u32_e32 v90, vcc, s33, v94
	v_med3_f32 v68, v80, s69, v208
	v_med3_f32 v69, v81, s69, v208
	v_cvt_pk_fp8_f32 v35, v68, v69 op_sel:[0,0,1]
	v_cvt_pk_bf16_f32 v68, v82, v83
	v_cvt_pk_bf16_f32 v69, v80, v81
	global_store_dwordx2 v[76:77], v[68:69], off offset:1024 nt
	global_store_dword v[78:79], v35, off offset:512 nt
	s_nop 0
	s_nop 0
	v_addc_co_u32_e32 v91, vcc, 0, v95, vcc
	v_mov_b32_e32 v35, 0
	v_add_co_u32_e32 v96, vcc, s33, v96
	s_nop 0
	v_pk_fma_f32 v[94:95], v[170:171], v[60:61], v[220:221]
	s_nop 0
	v_med3_f32 v60, v94, s69, v208
	v_med3_f32 v61, v95, s69, v208
	v_cvt_pk_fp8_f32 v35, v60, v61
	v_pk_fma_f32 v[92:93], v[172:173], v[62:63], v[222:223]
	v_addc_co_u32_e32 v97, vcc, 0, v97, vcc
	v_med3_f32 v60, v92, s69, v208
	v_med3_f32 v61, v93, s69, v208
	v_cvt_pk_fp8_f32 v35, v60, v61 op_sel:[0,0,1]
	v_cvt_pk_bf16_f32 v60, v94, v95
	v_cvt_pk_bf16_f32 v61, v92, v93
	global_store_dwordx2 v[76:77], v[60:61], off offset:1536 nt
	global_store_dword v[78:79], v35, off offset:768 nt
	s_nop 0
	s_nop 0
	v_mov_b32_e32 v35, 0
	s_nop 0
	v_pk_fma_f32 v[114:115], v[174:175], v[56:57], v[224:225]
	s_nop 0
	v_med3_f32 v56, v114, s69, v208
	v_med3_f32 v57, v115, s69, v208
	v_cvt_pk_fp8_f32 v35, v56, v57
	v_pk_fma_f32 v[112:113], v[176:177], v[58:59], v[226:227]
	s_nop 0
	v_med3_f32 v56, v112, s69, v208
	v_med3_f32 v57, v113, s69, v208
	v_cvt_pk_fp8_f32 v35, v56, v57 op_sel:[0,0,1]
	v_cvt_pk_bf16_f32 v56, v114, v115
	v_cvt_pk_bf16_f32 v57, v112, v113
	global_store_dwordx2 v[76:77], v[56:57], off offset:2048 nt
	global_store_dword v[78:79], v35, off offset:1024 nt
	s_nop 0
	s_nop 0
	v_mov_b32_e32 v35, 0
	s_nop 0
	v_pk_fma_f32 v[118:119], v[178:179], v[52:53], v[228:229]
	s_nop 0
	v_med3_f32 v52, v118, s69, v208
	v_med3_f32 v53, v119, s69, v208
	v_cvt_pk_fp8_f32 v35, v52, v53
	v_pk_fma_f32 v[116:117], v[180:181], v[54:55], v[230:231]
	s_nop 0
	v_med3_f32 v52, v116, s69, v208
	v_med3_f32 v53, v117, s69, v208
	v_cvt_pk_fp8_f32 v35, v52, v53 op_sel:[0,0,1]
	v_cvt_pk_bf16_f32 v52, v118, v119
	v_cvt_pk_bf16_f32 v53, v116, v117
	global_store_dwordx2 v[76:77], v[52:53], off offset:2560 nt
	global_store_dword v[78:79], v35, off offset:1280 nt
	s_nop 0
	s_nop 0
	v_mov_b32_e32 v35, 0
	s_nop 0
	v_pk_fma_f32 v[122:123], v[182:183], v[48:49], v[232:233]
	s_nop 0
	v_med3_f32 v48, v122, s69, v208
	v_med3_f32 v49, v123, s69, v208
	v_cvt_pk_fp8_f32 v35, v48, v49
	v_pk_fma_f32 v[120:121], v[184:185], v[50:51], v[234:235]
	s_nop 0
	v_med3_f32 v48, v120, s69, v208
	v_med3_f32 v49, v121, s69, v208
	v_cvt_pk_fp8_f32 v35, v48, v49 op_sel:[0,0,1]
	v_cvt_pk_bf16_f32 v48, v122, v123
	v_cvt_pk_bf16_f32 v49, v120, v121
	global_store_dwordx2 v[76:77], v[48:49], off offset:3072 nt
	global_store_dword v[78:79], v35, off offset:1536 nt
	s_nop 0
	s_nop 0
	v_mov_b32_e32 v35, 0
	s_nop 0
	v_pk_fma_f32 v[124:125], v[186:187], v[46:47], v[246:247]
	s_nop 0
	v_med3_f32 v46, v124, s69, v208
	v_med3_f32 v47, v125, s69, v208
	v_mov_b32_e32 v48, 0
	v_cvt_pk_fp8_f32 v48, v46, v47
	v_pk_fma_f32 v[126:127], v[188:189], v[44:45], v[248:249]
	s_nop 0
	v_med3_f32 v44, v126, s69, v208
	v_med3_f32 v45, v127, s69, v208
	v_cvt_pk_fp8_f32 v48, v44, v45 op_sel:[0,0,1]
	v_cvt_pk_bf16_f32 v44, v124, v125
	v_cvt_pk_bf16_f32 v45, v126, v127
	global_store_dwordx2 v[76:77], v[44:45], off offset:3584 nt
	global_store_dword v[78:79], v48, off offset:1792 nt
	v_lshlrev_b32_e32 v84, 16, v42
	v_and_b32_e32 v85, 0xffff0000, v42
	v_lshlrev_b32_e32 v78, 16, v43
	v_and_b32_e32 v79, 0xffff0000, v43
	v_add_f32_e32 v42, v84, v85
	v_add_f32_e32 v43, v78, v79
	v_lshlrev_b32_e32 v76, 16, v40
	v_and_b32_e32 v77, 0xffff0000, v40
	v_lshlrev_b32_e32 v70, 16, v41
	v_and_b32_e32 v71, 0xffff0000, v41
	v_add_f32_e32 v42, v42, v43
	v_add_f32_e32 v40, v76, v77
	v_add_f32_e32 v41, v70, v71
	v_lshlrev_b32_e32 v62, 16, v38
	v_and_b32_e32 v63, 0xffff0000, v38
	v_lshlrev_b32_e32 v68, 16, v39
	v_and_b32_e32 v69, 0xffff0000, v39
	v_add_f32_e32 v42, 0, v42
	v_add_f32_e32 v40, v40, v41
	v_add_f32_e32 v38, v62, v63
	v_add_f32_e32 v39, v68, v69
	v_lshlrev_b32_e32 v58, 16, v36
	v_and_b32_e32 v59, 0xffff0000, v36
	v_lshlrev_b32_e32 v60, 16, v37
	v_and_b32_e32 v61, 0xffff0000, v37
	v_add_f32_e32 v40, v42, v40
	v_add_f32_e32 v38, v38, v39
	v_add_f32_e32 v36, v58, v59
	v_add_f32_e32 v37, v60, v61
	v_lshlrev_b32_e32 v50, 16, v22
	v_and_b32_e32 v51, 0xffff0000, v22
	v_lshlrev_b32_e32 v52, 16, v23
	v_and_b32_e32 v53, 0xffff0000, v23
	v_add_f32_e32 v38, v40, v38
	v_add_f32_e32 v36, v36, v37
	v_add_f32_e32 v22, v50, v51
	v_add_f32_e32 v23, v52, v53
	v_lshlrev_b32_e32 v46, 16, v20
	v_and_b32_e32 v47, 0xffff0000, v20
	v_lshlrev_b32_e32 v48, 16, v21
	v_and_b32_e32 v49, 0xffff0000, v21
	v_add_f32_e32 v36, v38, v36
	v_add_f32_e32 v22, v22, v23
	v_add_f32_e32 v20, v46, v47
	v_add_f32_e32 v21, v48, v49
	v_lshlrev_b32_e32 v40, 16, v18
	v_and_b32_e32 v41, 0xffff0000, v18
	v_lshlrev_b32_e32 v42, 16, v19
	v_and_b32_e32 v43, 0xffff0000, v19
	v_add_f32_e32 v22, v36, v22
	v_add_f32_e32 v20, v20, v21
	v_add_f32_e32 v18, v40, v41
	v_add_f32_e32 v19, v42, v43
	v_lshlrev_b32_e32 v38, 16, v16
	v_and_b32_e32 v39, 0xffff0000, v16
	v_lshlrev_b32_e32 v36, 16, v17
	v_and_b32_e32 v37, 0xffff0000, v17
	v_add_f32_e32 v20, v22, v20
	v_add_f32_e32 v18, v18, v19
	v_add_f32_e32 v16, v38, v39
	v_add_f32_e32 v17, v36, v37
	v_add_f32_e32 v18, v20, v18
	v_add_f32_e32 v16, v16, v17
	v_add_f32_e32 v16, v18, v16
	s_mov_b64 s[12:13], s[34:35]
	s_mov_b64 s[14:15], s[36:37]
	v_add_f32_dpp v16, v16, v16 quad_perm:[1,0,3,2] row_mask:0xf bank_mask:0xf bound_ctrl:1
	v_lshl_add_u64 v[100:101], s[12:13], 0, v[192:193]
	v_lshl_add_u64 v[56:57], v[28:29], 0, s[10:11]
	v_add_f32_dpp v16, v16, v16 quad_perm:[2,3,0,1] row_mask:0xf bank_mask:0xf bound_ctrl:1
	v_lshl_add_u64 v[86:87], s[14:15], 0, v[192:193]
	s_lshl_b64 s[8:9], s[8:9], 11
	v_add_f32_dpp v16, v16, v16 row_ror:4 row_mask:0xf bank_mask:0xf bound_ctrl:1
	v_lshl_add_u64 v[54:55], v[30:31], 0, s[8:9]
	s_nop 0
	v_add_f32_dpp v16, v16, v16 row_ror:8 row_mask:0xf bank_mask:0xf bound_ctrl:1
	v_mov_b32_e32 v17, v16
	s_nop 1
	v_permlane16_swap_b32_e32 v16, v17
	v_add_f32_e32 v16, v16, v17
	v_mov_b32_e32 v17, v16
	s_nop 1
	v_permlane32_swap_b32_e32 v16, v17
	v_add_f32_e32 v16, v16, v17
	v_fmac_f32_e32 v79, 0xba000000, v16
	v_fmac_f32_e32 v85, 0xba000000, v16
	v_fmac_f32_e32 v78, 0xba000000, v16
	v_fmac_f32_e32 v84, 0xba000000, v16
	v_mul_f32_e32 v17, v85, v85
	v_mul_f32_e32 v18, v79, v79
	v_fmac_f32_e32 v17, v84, v84
	v_fmac_f32_e32 v18, v78, v78
	v_fmac_f32_e32 v71, 0xba000000, v16
	v_fmac_f32_e32 v77, 0xba000000, v16
	v_add_f32_e32 v17, v17, v18
	v_fmac_f32_e32 v70, 0xba000000, v16
	v_fmac_f32_e32 v76, 0xba000000, v16
	v_mul_f32_e32 v18, v77, v77
	v_mul_f32_e32 v19, v71, v71
	v_fmac_f32_e32 v18, v76, v76
	v_fmac_f32_e32 v19, v70, v70
	v_add_f32_e32 v18, v18, v19
	v_fmac_f32_e32 v69, 0xba000000, v16
	v_fmac_f32_e32 v63, 0xba000000, v16
	v_add_f32_e32 v17, v17, v18
	v_fmac_f32_e32 v68, 0xba000000, v16
	v_fmac_f32_e32 v62, 0xba000000, v16
	v_mul_f32_e32 v18, v63, v63
	v_mul_f32_e32 v19, v69, v69
	v_fmac_f32_e32 v18, v62, v62
	v_fmac_f32_e32 v19, v68, v68
	v_add_f32_e32 v18, v18, v19
	v_fmac_f32_e32 v61, 0xba000000, v16
	v_fmac_f32_e32 v59, 0xba000000, v16
	v_add_f32_e32 v17, v17, v18
	v_fmac_f32_e32 v60, 0xba000000, v16
	v_fmac_f32_e32 v58, 0xba000000, v16
	v_mul_f32_e32 v18, v59, v59
	v_mul_f32_e32 v19, v61, v61
	v_fmac_f32_e32 v18, v58, v58
	v_fmac_f32_e32 v19, v60, v60
	v_add_f32_e32 v18, v18, v19
	v_fmac_f32_e32 v53, 0xba000000, v16
	v_fmac_f32_e32 v51, 0xba000000, v16
	v_add_f32_e32 v17, v17, v18
	v_fmac_f32_e32 v52, 0xba000000, v16
	v_fmac_f32_e32 v50, 0xba000000, v16
	v_mul_f32_e32 v18, v51, v51
	v_mul_f32_e32 v19, v53, v53
	v_fmac_f32_e32 v18, v50, v50
	v_fmac_f32_e32 v19, v52, v52
	v_add_f32_e32 v18, v18, v19
	v_fmac_f32_e32 v49, 0xba000000, v16
	v_fmac_f32_e32 v47, 0xba000000, v16
	v_add_f32_e32 v17, v17, v18
	v_fmac_f32_e32 v48, 0xba000000, v16
	v_fmac_f32_e32 v46, 0xba000000, v16
	v_mul_f32_e32 v18, v47, v47
	v_mul_f32_e32 v19, v49, v49
	v_fmac_f32_e32 v18, v46, v46
	v_fmac_f32_e32 v19, v48, v48
	v_add_f32_e32 v18, v18, v19
	v_fmac_f32_e32 v43, 0xba000000, v16
	v_fmac_f32_e32 v41, 0xba000000, v16
	v_add_f32_e32 v17, v17, v18
	v_fmac_f32_e32 v42, 0xba000000, v16
	v_fmac_f32_e32 v40, 0xba000000, v16
	v_mul_f32_e32 v18, v41, v41
	v_mul_f32_e32 v19, v43, v43
	v_fmac_f32_e32 v18, v40, v40
	v_fmac_f32_e32 v19, v42, v42
	v_add_f32_e32 v18, v18, v19
	v_fmac_f32_e32 v37, 0xba000000, v16
	v_fmac_f32_e32 v39, 0xba000000, v16
	v_add_f32_e32 v17, v17, v18
	v_fmac_f32_e32 v36, 0xba000000, v16
	v_fmac_f32_e32 v38, 0xba000000, v16
	v_mul_f32_e32 v16, v39, v39
	v_mul_f32_e32 v18, v37, v37
	v_fmac_f32_e32 v16, v38, v38
	v_fmac_f32_e32 v18, v36, v36
	v_add_f32_e32 v16, v16, v18
	v_add_f32_e32 v16, v17, v16
	s_nop 1
	v_add_f32_dpp v16, v16, v16 quad_perm:[1,0,3,2] row_mask:0xf bank_mask:0xf bound_ctrl:1
	s_nop 1
	v_add_f32_dpp v16, v16, v16 quad_perm:[2,3,0,1] row_mask:0xf bank_mask:0xf bound_ctrl:1
	s_nop 1
	v_add_f32_dpp v16, v16, v16 row_ror:4 row_mask:0xf bank_mask:0xf bound_ctrl:1
	s_nop 1
	v_add_f32_dpp v16, v16, v16 row_ror:8 row_mask:0xf bank_mask:0xf bound_ctrl:1
	v_mov_b32_e32 v17, v16
	s_nop 1
	v_permlane16_swap_b32_e32 v16, v17
	v_add_f32_e32 v16, v16, v17
	v_mov_b32_e32 v17, v16
	s_nop 1
	v_permlane32_swap_b32_e32 v16, v17
	v_add_f32_e32 v16, v16, v17
	v_fmamk_f32 v16, v16, 0x3a000000, v207
	v_rsq_f32_e32 v44, v16
	s_nop 0
	v_pk_mul_f32 v[84:85], v[44:45], v[84:85] op_sel_hi:[0,1]
	v_pk_mul_f32 v[78:79], v[44:45], v[78:79] op_sel_hi:[0,1]
	v_pk_mul_f32 v[76:77], v[44:45], v[76:77] op_sel_hi:[0,1]
	v_pk_mul_f32 v[70:71], v[44:45], v[70:71] op_sel_hi:[0,1]
	v_pk_mul_f32 v[62:63], v[44:45], v[62:63] op_sel_hi:[0,1]
	v_pk_mul_f32 v[68:69], v[44:45], v[68:69] op_sel_hi:[0,1]
	v_pk_mul_f32 v[58:59], v[44:45], v[58:59] op_sel_hi:[0,1]
	v_pk_mul_f32 v[60:61], v[44:45], v[60:61] op_sel_hi:[0,1]
	v_pk_mul_f32 v[50:51], v[44:45], v[50:51] op_sel_hi:[0,1]
	v_pk_mul_f32 v[52:53], v[44:45], v[52:53] op_sel_hi:[0,1]
	v_mov_b32_e32 v45, 0
	s_waitcnt lgkmcnt(0)
	v_pk_fma_f32 v[128:129], v[160:161], v[78:79], v[200:201]
	v_pk_fma_f32 v[130:131], v[158:159], v[84:85], v[198:199]
	v_mov_b32_e32 v20, 0
	v_cvt_pk_bf16_f32 v16, v130, v131
	v_cvt_pk_bf16_f32 v17, v128, v129
	global_store_dwordx2 v[56:57], v[16:17], off nt
	v_med3_f32 v16, v130, s69, v208
	v_med3_f32 v17, v131, s69, v208
	v_cvt_pk_fp8_f32 v20, v16, v17
	v_med3_f32 v18, v128, s69, v208
	v_med3_f32 v19, v129, s69, v208
	v_cvt_pk_fp8_f32 v20, v18, v19 op_sel:[0,0,1]
	global_store_dword v[54:55], v20, off nt
	s_nop 0
	s_nop 0
	s_nop 0
	v_pk_fma_f32 v[104:105], v[164:165], v[70:71], v[204:205]
	v_pk_fma_f32 v[106:107], v[162:163], v[76:77], v[202:203]
	v_mov_b32_e32 v20, 0
	v_cvt_pk_bf16_f32 v16, v106, v107
	v_cvt_pk_bf16_f32 v17, v104, v105
	global_store_dwordx2 v[56:57], v[16:17], off offset:512 nt
	v_med3_f32 v16, v106, s69, v208
	v_med3_f32 v17, v107, s69, v208
	v_cvt_pk_fp8_f32 v20, v16, v17
	v_med3_f32 v18, v104, s69, v208
	v_med3_f32 v19, v105, s69, v208
	v_cvt_pk_fp8_f32 v20, v18, v19 op_sel:[0,0,1]
	global_store_dword v[54:55], v20, off offset:256 nt
	s_nop 0
	s_nop 0
	s_nop 0
	v_pk_fma_f32 v[96:97], v[168:169], v[68:69], v[218:219]
	v_pk_fma_f32 v[98:99], v[166:167], v[62:63], v[216:217]
	v_mov_b32_e32 v20, 0
	v_cvt_pk_bf16_f32 v16, v98, v99
	v_cvt_pk_bf16_f32 v17, v96, v97
	global_store_dwordx2 v[56:57], v[16:17], off offset:1024 nt
	v_med3_f32 v16, v98, s69, v208
	v_med3_f32 v17, v99, s69, v208
	v_cvt_pk_fp8_f32 v20, v16, v17
	v_med3_f32 v18, v96, s69, v208
	v_med3_f32 v19, v97, s69, v208
	v_cvt_pk_fp8_f32 v20, v18, v19 op_sel:[0,0,1]
	global_store_dword v[54:55], v20, off offset:512 nt
	s_nop 0
	s_nop 0
	s_nop 0
	v_pk_fma_f32 v[88:89], v[172:173], v[60:61], v[222:223]
	v_pk_fma_f32 v[90:91], v[170:171], v[58:59], v[220:221]
	v_mov_b32_e32 v20, 0
	v_cvt_pk_bf16_f32 v16, v90, v91
	v_cvt_pk_bf16_f32 v17, v88, v89
	global_store_dwordx2 v[56:57], v[16:17], off offset:1536 nt
	v_med3_f32 v16, v90, s69, v208
	v_med3_f32 v17, v91, s69, v208
	v_cvt_pk_fp8_f32 v20, v16, v17
	v_med3_f32 v18, v88, s69, v208
	v_med3_f32 v19, v89, s69, v208
	v_add_co_u32_e32 v16, vcc, s33, v100
	v_cvt_pk_fp8_f32 v20, v18, v19 op_sel:[0,0,1]
	s_nop 0
	v_addc_co_u32_e32 v17, vcc, 0, v101, vcc
	v_add_co_u32_e32 v18, vcc, s33, v86
	global_store_dword v[54:55], v20, off offset:768 nt
	s_nop 0
	v_addc_co_u32_e32 v19, vcc, 0, v87, vcc
	s_nop 0
	s_nop 0
	v_pk_fma_f32 v[84:85], v[176:177], v[52:53], v[226:227]
	v_pk_fma_f32 v[86:87], v[174:175], v[50:51], v[224:225]
	v_med3_f32 v22, v84, s69, v208
	v_cvt_pk_bf16_f32 v20, v86, v87
	v_cvt_pk_bf16_f32 v21, v84, v85
	global_store_dwordx2 v[56:57], v[20:21], off offset:2048 nt
	v_med3_f32 v20, v86, s69, v208
	v_med3_f32 v21, v87, s69, v208
	v_cvt_pk_fp8_f32 v45, v20, v21
	v_med3_f32 v23, v85, s69, v208
; #define LAS __attribute__((address_space(3)))
; __global__ void __launch_bounds__(NTHREADS, 2) hybrid_fwd(Args a) {
;     ...
;                     if (qp == 0) {
; #pragma unroll
;                         for (int q = 0; q < 2; ++q)
; #pragma unroll
;                             for (int j = 0; j < 8; ++j) raw[q][j] = __builtin_nontemporal_load((const u32x2*)(YB + (size_t)(v * 32 + wave + 8 * (2 + q)) * DM + j * 256 + lane * 4));
;                         __builtin_amdgcn_sched_barrier(0);
;                     }
;                     f32x2 y2[8][4];
; #pragma unroll
;                     for (int j = 0; j < 8; ++j)
; #pragma unroll
;                         for (int c = 0; c < 4; ++c) y2[j][c] = (f32x2){ya[j][c], yb[j][c]};
;                     f32x2 acc2[16];
; #pragma unroll
;                     for (int e = 0; e < 16; ++e) acc2[e] = (f32x2){0.f, 0.f};
; #pragma unroll
;                     for (int j = 0; j < 8; ++j) {
; #pragma unroll
;                         for (int e = 0; e < 16; ++e) { const f32x4 w = *(const LAS f32x4*)(rwT + e * 2052 + j * 256 + lane * 4);
;                             acc2[e] += y2[j][0] * (f32x2){w[0], w[0]}; acc2[e] += y2[j][1] * (f32x2){w[1], w[1]};
;                             acc2[e] += y2[j][2] * (f32x2){w[2], w[2]}; acc2[e] += y2[j][3] * (f32x2){w[3], w[3]}; }
	v_cvt_pk_fp8_f32 v45, v22, v23 op_sel:[0,0,1]
	global_store_dword v[54:55], v45, off offset:1024 nt
	s_nop 0
	v_pk_mul_f32 v[46:47], v[44:45], v[46:47] op_sel_hi:[0,1]
	v_pk_mul_f32 v[48:49], v[44:45], v[48:49] op_sel_hi:[0,1]
	v_mov_b32_e32 v45, 0
	s_nop 0
	v_pk_fma_f32 v[76:77], v[180:181], v[48:49], v[230:231]
	v_pk_fma_f32 v[78:79], v[178:179], v[46:47], v[228:229]
	v_med3_f32 v22, v76, s69, v208
	v_cvt_pk_bf16_f32 v20, v78, v79
	v_cvt_pk_bf16_f32 v21, v76, v77
	global_store_dwordx2 v[56:57], v[20:21], off offset:2560 nt
	v_med3_f32 v20, v78, s69, v208
	v_med3_f32 v21, v79, s69, v208
	v_cvt_pk_fp8_f32 v45, v20, v21
	v_med3_f32 v23, v77, s69, v208
	v_cvt_pk_fp8_f32 v45, v22, v23 op_sel:[0,0,1]
	global_store_dword v[54:55], v45, off offset:1280 nt
	s_nop 0
	v_pk_mul_f32 v[40:41], v[44:45], v[40:41] op_sel_hi:[0,1]
	v_pk_mul_f32 v[42:43], v[44:45], v[42:43] op_sel_hi:[0,1]
	v_pk_mul_f32 v[38:39], v[44:45], v[38:39] op_sel_hi:[0,1]
	v_pk_mul_f32 v[36:37], v[44:45], v[36:37] op_sel_hi:[0,1]
	s_nop 0
	v_pk_fma_f32 v[68:69], v[184:185], v[42:43], v[234:235]
	v_pk_fma_f32 v[70:71], v[182:183], v[40:41], v[232:233]
	v_mov_b32_e32 v40, 0
	v_cvt_pk_bf16_f32 v20, v70, v71
	v_cvt_pk_bf16_f32 v21, v68, v69
	global_store_dwordx2 v[56:57], v[20:21], off offset:3072 nt
	v_med3_f32 v20, v70, s69, v208
	v_med3_f32 v21, v71, s69, v208
	v_cvt_pk_fp8_f32 v40, v20, v21
	v_med3_f32 v22, v68, s69, v208
	v_med3_f32 v23, v69, s69, v208
	v_cvt_pk_fp8_f32 v40, v22, v23 op_sel:[0,0,1]
	global_store_dword v[54:55], v40, off offset:1536 nt
	s_nop 0
	s_nop 0
	s_nop 0
	v_pk_fma_f32 v[60:61], v[188:189], v[36:37], v[248:249]
	v_pk_fma_f32 v[62:63], v[186:187], v[38:39], v[246:247]
	v_mov_b32_e32 v20, 0
	v_cvt_pk_bf16_f32 v16, v62, v63
	v_cvt_pk_bf16_f32 v17, v60, v61
	global_store_dwordx2 v[56:57], v[16:17], off offset:3584 nt
	v_med3_f32 v16, v62, s69, v208
	v_med3_f32 v17, v63, s69, v208
	v_cvt_pk_fp8_f32 v20, v16, v17
	v_med3_f32 v18, v60, s69, v208
	v_med3_f32 v19, v61, s69, v208
	v_cvt_pk_fp8_f32 v20, v18, v19 op_sel:[0,0,1]
	global_store_dword v[54:55], v20, off offset:1792 nt
	s_ashr_i32 s39, s38, 31
	s_add_i32 s40, s6, 24
	s_lshl_b64 s[44:45], s[38:39], 12
	s_ashr_i32 s41, s40, 31
	v_lshl_add_u64 v[16:17], v[26:27], 0, s[44:45]
	s_lshl_b64 s[42:43], s[40:41], 12
	flat_load_dwordx2 v[58:59], v[16:17] nt
	flat_load_dwordx2 v[56:57], v[16:17] offset:512 nt
	flat_load_dwordx2 v[54:55], v[16:17] offset:1024 nt
	flat_load_dwordx2 v[52:53], v[16:17] offset:1536 nt
	flat_load_dwordx2 v[50:51], v[16:17] offset:2048 nt
	flat_load_dwordx2 v[48:49], v[16:17] offset:2560 nt
	flat_load_dwordx2 v[46:47], v[16:17] offset:3072 nt
	flat_load_dwordx2 v[44:45], v[16:17] offset:3584 nt
	v_lshl_add_u64 v[16:17], v[26:27], 0, s[42:43]
	flat_load_dwordx2 v[42:43], v[16:17] nt
	flat_load_dwordx2 v[40:41], v[16:17] offset:512 nt
	flat_load_dwordx2 v[38:39], v[16:17] offset:1024 nt
	flat_load_dwordx2 v[36:37], v[16:17] offset:1536 nt
	flat_load_dwordx2 v[22:23], v[16:17] offset:2048 nt
	flat_load_dwordx2 v[20:21], v[16:17] offset:2560 nt
	flat_load_dwordx2 v[18:19], v[16:17] offset:3072 nt
	s_nop 0
	flat_load_dwordx2 v[16:17], v[16:17] offset:3584 nt
	v_add_u32_e32 v238, 0x10000, v25
	ds_read_b128 v[158:161], v25 offset:0
	ds_read_b128 v[162:165], v25 offset:8208
	ds_read_b128 v[166:169], v25 offset:16416
	ds_read_b128 v[170:173], v25 offset:24624
	ds_read_b128 v[174:177], v25 offset:32832
	ds_read_b128 v[178:181], v25 offset:41040
	ds_read_b128 v[182:185], v25 offset:49248
	ds_read_b128 v[186:189], v25 offset:57456
	v_mov_b32_e32 v100, v94
	v_mov_b32_e32 v101, v90
	v_mov_b32_e32 v90, v95
	v_mov_b32_e32 v102, v92
	v_mov_b32_e32 v103, v88
	v_mov_b32_e32 v88, v93
	v_mov_b32_e32 v92, v114
	v_mov_b32_e32 v93, v86
	v_mov_b32_e32 v86, v115
	v_mov_b32_e32 v94, v112
	v_mov_b32_e32 v95, v84
	v_mov_b32_e32 v84, v113
	ds_read_b128 v[198:201], v238 offset:128
	v_mov_b32_e32 v136, v64
	v_mov_b32_e32 v137, v130
	v_mov_b32_e32 v130, v65
	v_mov_b32_e32 v108, v82
	v_mov_b32_e32 v109, v98
	v_mov_b32_e32 v98, v83
	v_mov_b32_e32 v82, v116
	v_mov_b32_e32 v83, v76
	v_mov_b32_e32 v76, v117
	s_waitcnt lgkmcnt(8)
	v_pk_fma_f32 v[116:117], v[136:137], v[158:159], 0 op_sel_hi:[1,0,0]
	v_mov_b32_e32 v138, v66
	v_mov_b32_e32 v139, v128
	v_pk_fma_f32 v[112:113], v[158:159], v[130:131], v[116:117] op_sel:[1,0,0]
	v_mov_b32_e32 v128, v67
	v_pk_fma_f32 v[112:113], v[160:161], v[138:139], v[112:113] op_sel_hi:[0,1,1]
	v_mov_b32_e32 v114, v161
	v_pk_fma_f32 v[112:113], v[114:115], v[128:129], v[112:113] op_sel_hi:[0,1,1]
	ds_read_b128 v[202:205], v238 offset:8336
	v_mov_b32_e32 v110, v80
	v_mov_b32_e32 v111, v96
	v_mov_b32_e32 v96, v81
	v_mov_b32_e32 v80, v118
	v_mov_b32_e32 v81, v78
	v_mov_b32_e32 v78, v119
	s_waitcnt lgkmcnt(8)
	v_pk_fma_f32 v[118:119], v[136:137], v[162:163], 0 op_sel_hi:[1,0,0]
	v_mov_b32_e32 v134, v74
	v_pk_fma_f32 v[114:115], v[162:163], v[130:131], v[118:119] op_sel:[1,0,0]
	v_mov_b32_e32 v135, v104
	v_pk_fma_f32 v[114:115], v[164:165], v[138:139], v[114:115] op_sel_hi:[0,1,1]
	v_mov_b32_e32 v116, v165
	v_pk_fma_f32 v[152:153], v[116:117], v[128:129], v[114:115] op_sel_hi:[0,1,1]
	ds_read_b128 v[216:219], v238 offset:16544
	v_mov_b32_e32 v104, v75
	v_mov_b32_e32 v74, v120
	v_mov_b32_e32 v75, v68
	v_mov_b32_e32 v68, v121
	s_waitcnt lgkmcnt(8)
	v_pk_fma_f32 v[118:119], v[136:137], v[166:167], 0 op_sel_hi:[1,0,0]
	v_mov_b32_e32 v132, v72
	v_pk_fma_f32 v[114:115], v[166:167], v[130:131], v[118:119] op_sel:[1,0,0]
	v_mov_b32_e32 v133, v106
	v_pk_fma_f32 v[114:115], v[168:169], v[138:139], v[114:115] op_sel_hi:[0,1,1]
	v_mov_b32_e32 v116, v169
	v_pk_fma_f32 v[154:155], v[116:117], v[128:129], v[114:115] op_sel_hi:[0,1,1]
	ds_read_b128 v[220:223], v238 offset:24752
	v_mov_b32_e32 v106, v73
	v_mov_b32_e32 v72, v122
	v_mov_b32_e32 v73, v70
	v_mov_b32_e32 v70, v123
	s_waitcnt lgkmcnt(8)
; #define LAS __attribute__((address_space(3)))
; __global__ void __launch_bounds__(NTHREADS, 2) hybrid_fwd(Args a) {
;     ...
; #pragma unroll
;                     for (int j = 0; j < 8; ++j) {
; #pragma unroll
;                         for (int e = 0; e < 16; ++e) { const f32x4 w = *(const LAS f32x4*)(rwT + e * 2052 + j * 256 + lane * 4);
;                             acc2[e] += y2[j][0] * (f32x2){w[0], w[0]}; acc2[e] += y2[j][1] * (f32x2){w[1], w[1]};
;                             acc2[e] += y2[j][2] * (f32x2){w[2], w[2]}; acc2[e] += y2[j][3] * (f32x2){w[3], w[3]}; }
	v_pk_fma_f32 v[118:119], v[136:137], v[170:171], 0 op_sel_hi:[1,0,0]
	v_mov_b32_e32 v66, v124
	v_pk_fma_f32 v[114:115], v[170:171], v[130:131], v[118:119] op_sel:[1,0,0]
	v_mov_b32_e32 v67, v62
	v_pk_fma_f32 v[114:115], v[172:173], v[138:139], v[114:115] op_sel_hi:[0,1,1]
	v_mov_b32_e32 v116, v173
	v_pk_fma_f32 v[114:115], v[116:117], v[128:129], v[114:115] op_sel_hi:[0,1,1]
	ds_read_b128 v[224:227], v238 offset:32960
	v_mov_b32_e32 v62, v125
	v_mov_b32_e32 v64, v126
	v_mov_b32_e32 v65, v60
	v_mov_b32_e32 v60, v127
	s_waitcnt lgkmcnt(8)
	v_pk_fma_f32 v[120:121], v[136:137], v[174:175], 0 op_sel_hi:[1,0,0]
	s_nop 0
	v_pk_fma_f32 v[116:117], v[174:175], v[130:131], v[120:121] op_sel:[1,0,0]
	s_nop 0
	v_pk_fma_f32 v[116:117], v[176:177], v[138:139], v[116:117] op_sel_hi:[0,1,1]
	v_mov_b32_e32 v118, v177
	v_pk_fma_f32 v[116:117], v[118:119], v[128:129], v[116:117] op_sel_hi:[0,1,1]
	ds_read_b128 v[228:231], v238 offset:41168
	s_waitcnt lgkmcnt(8)
	v_pk_fma_f32 v[122:123], v[136:137], v[178:179], 0 op_sel_hi:[1,0,0]
	s_nop 0
	v_pk_fma_f32 v[118:119], v[178:179], v[130:131], v[122:123] op_sel:[1,0,0]
	s_nop 0
	v_pk_fma_f32 v[118:119], v[180:181], v[138:139], v[118:119] op_sel_hi:[0,1,1]
	v_mov_b32_e32 v120, v181
	v_pk_fma_f32 v[118:119], v[120:121], v[128:129], v[118:119] op_sel_hi:[0,1,1]
	ds_read_b128 v[232:235], v238 offset:49376
	s_waitcnt lgkmcnt(8)
	v_pk_fma_f32 v[124:125], v[136:137], v[182:183], 0 op_sel_hi:[1,0,0]
	s_nop 0
	v_pk_fma_f32 v[120:121], v[182:183], v[130:131], v[124:125] op_sel:[1,0,0]
	s_nop 0
	v_pk_fma_f32 v[120:121], v[184:185], v[138:139], v[120:121] op_sel_hi:[0,1,1]
	v_mov_b32_e32 v122, v185
	v_pk_fma_f32 v[120:121], v[122:123], v[128:129], v[120:121] op_sel_hi:[0,1,1]
	ds_read_b128 v[242:245], v238 offset:57584
	s_waitcnt lgkmcnt(8)
	v_pk_fma_f32 v[126:127], v[136:137], v[186:187], 0 op_sel_hi:[1,0,0]
	s_nop 0
	v_pk_fma_f32 v[122:123], v[186:187], v[130:131], v[126:127] op_sel:[1,0,0]
	s_nop 0
	v_pk_fma_f32 v[122:123], v[188:189], v[138:139], v[122:123] op_sel_hi:[0,1,1]
	v_mov_b32_e32 v124, v189
	v_pk_fma_f32 v[122:123], v[124:125], v[128:129], v[122:123] op_sel_hi:[0,1,1]
	ds_read_b128 v[246:249], v25 offset:1024
	s_waitcnt lgkmcnt(8)
	v_pk_fma_f32 v[140:141], v[136:137], v[198:199], 0 op_sel_hi:[1,0,0]
	s_nop 0
	v_pk_fma_f32 v[124:125], v[198:199], v[130:131], v[140:141] op_sel:[1,0,0]
	ds_read_b128 v[250:253], v25 offset:9232
	v_pk_fma_f32 v[124:125], v[200:201], v[138:139], v[124:125] op_sel_hi:[0,1,1]
	v_mov_b32_e32 v126, v201
	v_pk_fma_f32 v[124:125], v[126:127], v[128:129], v[124:125] op_sel_hi:[0,1,1]
	s_waitcnt lgkmcnt(8)
	v_pk_fma_f32 v[126:127], v[136:137], v[202:203], 0 op_sel_hi:[1,0,0]
	s_nop 0
	v_pk_fma_f32 v[126:127], v[202:203], v[130:131], v[126:127] op_sel:[1,0,0]
	v_mov_b32_e32 v140, v205
	v_pk_fma_f32 v[126:127], v[204:205], v[138:139], v[126:127] op_sel_hi:[0,1,1]
	v_pk_fma_f32 v[126:127], v[140:141], v[128:129], v[126:127] op_sel_hi:[0,1,1]
	ds_read_b128 v[158:161], v25 offset:17440
	s_waitcnt lgkmcnt(8)
	v_pk_fma_f32 v[144:145], v[136:137], v[216:217], 0 op_sel_hi:[1,0,0]
	s_nop 0
	v_pk_fma_f32 v[140:141], v[216:217], v[130:131], v[144:145] op_sel:[1,0,0]
	s_nop 0
	v_pk_fma_f32 v[140:141], v[218:219], v[138:139], v[140:141] op_sel_hi:[0,1,1]
	v_mov_b32_e32 v142, v219
	v_pk_fma_f32 v[140:141], v[142:143], v[128:129], v[140:141] op_sel_hi:[0,1,1]
	ds_read_b128 v[162:165], v25 offset:25648
	s_waitcnt lgkmcnt(8)
	v_pk_fma_f32 v[146:147], v[136:137], v[220:221], 0 op_sel_hi:[1,0,0]
	s_nop 0
	v_pk_fma_f32 v[142:143], v[220:221], v[130:131], v[146:147] op_sel:[1,0,0]
	s_nop 0
	v_pk_fma_f32 v[142:143], v[222:223], v[138:139], v[142:143] op_sel_hi:[0,1,1]
	v_mov_b32_e32 v144, v223
	v_pk_fma_f32 v[142:143], v[144:145], v[128:129], v[142:143] op_sel_hi:[0,1,1]
	ds_read_b128 v[166:169], v25 offset:33856
	s_waitcnt lgkmcnt(8)
	v_pk_fma_f32 v[148:149], v[136:137], v[224:225], 0 op_sel_hi:[1,0,0]
	s_nop 0
	v_pk_fma_f32 v[144:145], v[224:225], v[130:131], v[148:149] op_sel:[1,0,0]
	s_nop 0
	v_pk_fma_f32 v[144:145], v[226:227], v[138:139], v[144:145] op_sel_hi:[0,1,1]
	v_mov_b32_e32 v146, v227
	v_pk_fma_f32 v[144:145], v[146:147], v[128:129], v[144:145] op_sel_hi:[0,1,1]
	ds_read_b128 v[170:173], v25 offset:42064
	s_waitcnt lgkmcnt(8)
	v_pk_fma_f32 v[150:151], v[136:137], v[228:229], 0 op_sel_hi:[1,0,0]
	s_nop 0
	v_pk_fma_f32 v[146:147], v[228:229], v[130:131], v[150:151] op_sel:[1,0,0]
	s_nop 0
	v_pk_fma_f32 v[146:147], v[230:231], v[138:139], v[146:147] op_sel_hi:[0,1,1]
	v_mov_b32_e32 v148, v231
	v_pk_fma_f32 v[146:147], v[148:149], v[128:129], v[146:147] op_sel_hi:[0,1,1]
	ds_read_b128 v[174:177], v25 offset:50272
	s_waitcnt lgkmcnt(8)
	v_pk_fma_f32 v[194:195], v[136:137], v[232:233], 0 op_sel_hi:[1,0,0]
	s_nop 0
	v_pk_fma_f32 v[148:149], v[232:233], v[130:131], v[194:195] op_sel:[1,0,0]
	ds_read_b128 v[178:181], v25 offset:58480
	v_pk_fma_f32 v[148:149], v[234:235], v[138:139], v[148:149] op_sel_hi:[0,1,1]
	v_mov_b32_e32 v150, v235
	v_pk_fma_f32 v[148:149], v[150:151], v[128:129], v[148:149] op_sel_hi:[0,1,1]
	s_waitcnt lgkmcnt(8)
	v_pk_fma_f32 v[136:137], v[136:137], v[242:243], 0 op_sel_hi:[1,0,0]
	s_nop 0
	v_pk_fma_f32 v[130:131], v[242:243], v[130:131], v[136:137] op_sel:[1,0,0]
	v_mov_b32_e32 v136, v245
	v_pk_fma_f32 v[130:131], v[244:245], v[138:139], v[130:131] op_sel_hi:[0,1,1]
	v_pk_fma_f32 v[150:151], v[136:137], v[128:129], v[130:131] op_sel_hi:[0,1,1]
	ds_read_b128 v[182:185], v238 offset:1152
	s_waitcnt lgkmcnt(8)
; #define LAS __attribute__((address_space(3)))
; __global__ void __launch_bounds__(NTHREADS, 2) hybrid_fwd(Args a) {
;     ...
; #pragma unroll
;                     for (int j = 0; j < 8; ++j) {
; #pragma unroll
;                         for (int e = 0; e < 16; ++e) { const f32x4 w = *(const LAS f32x4*)(rwT + e * 2052 + j * 256 + lane * 4);
;                             acc2[e] += y2[j][0] * (f32x2){w[0], w[0]}; acc2[e] += y2[j][1] * (f32x2){w[1], w[1]};
;                             acc2[e] += y2[j][2] * (f32x2){w[2], w[2]}; acc2[e] += y2[j][3] * (f32x2){w[3], w[3]}; }
	v_pk_fma_f32 v[112:113], v[132:133], v[246:247], v[112:113] op_sel_hi:[1,0,1]
	s_nop 0
	v_pk_fma_f32 v[112:113], v[246:247], v[106:107], v[112:113] op_sel:[1,0,0]
	v_mov_b32_e32 v128, v249
	v_pk_fma_f32 v[112:113], v[248:249], v[134:135], v[112:113] op_sel_hi:[0,1,1]
	v_pk_fma_f32 v[112:113], v[128:129], v[104:105], v[112:113] op_sel_hi:[0,1,1]
	ds_read_b128 v[186:189], v238 offset:9360
	s_waitcnt lgkmcnt(8)
	v_pk_fma_f32 v[136:137], v[132:133], v[250:251], v[152:153] op_sel_hi:[1,0,1]
	s_nop 0
	v_pk_fma_f32 v[128:129], v[250:251], v[106:107], v[136:137] op_sel:[1,0,0]
	s_nop 0
	v_pk_fma_f32 v[128:129], v[252:253], v[134:135], v[128:129] op_sel_hi:[0,1,1]
	v_mov_b32_e32 v130, v253
	v_pk_fma_f32 v[152:153], v[130:131], v[104:105], v[128:129] op_sel_hi:[0,1,1]
	ds_read_b128 v[198:201], v238 offset:17568
	s_waitcnt lgkmcnt(8)
	v_pk_fma_f32 v[136:137], v[132:133], v[158:159], v[154:155] op_sel_hi:[1,0,1]
	s_nop 0
	v_pk_fma_f32 v[128:129], v[158:159], v[106:107], v[136:137] op_sel:[1,0,0]
	ds_read_b128 v[202:205], v238 offset:25776
	v_pk_fma_f32 v[128:129], v[160:161], v[134:135], v[128:129] op_sel_hi:[0,1,1]
	v_mov_b32_e32 v130, v161
	v_pk_fma_f32 v[128:129], v[130:131], v[104:105], v[128:129] op_sel_hi:[0,1,1]
	s_waitcnt lgkmcnt(8)
	v_pk_fma_f32 v[114:115], v[132:133], v[162:163], v[114:115] op_sel_hi:[1,0,1]
	s_nop 0
	v_pk_fma_f32 v[114:115], v[162:163], v[106:107], v[114:115] op_sel:[1,0,0]
	v_mov_b32_e32 v130, v165
	v_pk_fma_f32 v[114:115], v[164:165], v[134:135], v[114:115] op_sel_hi:[0,1,1]
	ds_read_b128 v[216:219], v238 offset:33984
	v_pk_fma_f32 v[114:115], v[130:131], v[104:105], v[114:115] op_sel_hi:[0,1,1]
	s_waitcnt lgkmcnt(8)
	v_pk_fma_f32 v[116:117], v[132:133], v[166:167], v[116:117] op_sel_hi:[1,0,1]
	s_nop 0
	v_pk_fma_f32 v[116:117], v[166:167], v[106:107], v[116:117] op_sel:[1,0,0]
	v_mov_b32_e32 v130, v169
	v_pk_fma_f32 v[116:117], v[168:169], v[134:135], v[116:117] op_sel_hi:[0,1,1]
	ds_read_b128 v[220:223], v238 offset:42192
	v_pk_fma_f32 v[116:117], v[130:131], v[104:105], v[116:117] op_sel_hi:[0,1,1]
	s_waitcnt lgkmcnt(8)
	v_pk_fma_f32 v[118:119], v[132:133], v[170:171], v[118:119] op_sel_hi:[1,0,1]
	s_nop 0
	v_pk_fma_f32 v[118:119], v[170:171], v[106:107], v[118:119] op_sel:[1,0,0]
	v_mov_b32_e32 v130, v173
	v_pk_fma_f32 v[118:119], v[172:173], v[134:135], v[118:119] op_sel_hi:[0,1,1]
	ds_read_b128 v[224:227], v238 offset:50400
	v_pk_fma_f32 v[118:119], v[130:131], v[104:105], v[118:119] op_sel_hi:[0,1,1]
	s_waitcnt lgkmcnt(8)
	v_pk_fma_f32 v[120:121], v[132:133], v[174:175], v[120:121] op_sel_hi:[1,0,1]
	s_nop 0
	v_pk_fma_f32 v[120:121], v[174:175], v[106:107], v[120:121] op_sel:[1,0,0]
	v_mov_b32_e32 v130, v177
	v_pk_fma_f32 v[120:121], v[176:177], v[134:135], v[120:121] op_sel_hi:[0,1,1]
	ds_read_b128 v[228:231], v238 offset:58608
	v_pk_fma_f32 v[120:121], v[130:131], v[104:105], v[120:121] op_sel_hi:[0,1,1]
	s_waitcnt lgkmcnt(8)
	v_pk_fma_f32 v[122:123], v[132:133], v[178:179], v[122:123] op_sel_hi:[1,0,1]
	s_nop 0
	v_pk_fma_f32 v[122:123], v[178:179], v[106:107], v[122:123] op_sel:[1,0,0]
	v_mov_b32_e32 v130, v181
	v_pk_fma_f32 v[122:123], v[180:181], v[134:135], v[122:123] op_sel_hi:[0,1,1]
	ds_read_b128 v[232:235], v25 offset:2048
	v_pk_fma_f32 v[122:123], v[130:131], v[104:105], v[122:123] op_sel_hi:[0,1,1]
	s_waitcnt lgkmcnt(8)
	v_pk_fma_f32 v[124:125], v[132:133], v[182:183], v[124:125] op_sel_hi:[1,0,1]
	s_nop 0
	v_pk_fma_f32 v[124:125], v[182:183], v[106:107], v[124:125] op_sel:[1,0,0]
	v_mov_b32_e32 v130, v185
	v_pk_fma_f32 v[124:125], v[184:185], v[134:135], v[124:125] op_sel_hi:[0,1,1]
	ds_read_b128 v[242:245], v25 offset:10256
	v_pk_fma_f32 v[124:125], v[130:131], v[104:105], v[124:125] op_sel_hi:[0,1,1]
	s_waitcnt lgkmcnt(8)
	v_pk_fma_f32 v[126:127], v[132:133], v[186:187], v[126:127] op_sel_hi:[1,0,1]
	s_nop 0
	v_pk_fma_f32 v[126:127], v[186:187], v[106:107], v[126:127] op_sel:[1,0,0]
	v_mov_b32_e32 v130, v189
	v_pk_fma_f32 v[126:127], v[188:189], v[134:135], v[126:127] op_sel_hi:[0,1,1]
	ds_read_b128 v[246:249], v25 offset:18464
	v_pk_fma_f32 v[126:127], v[130:131], v[104:105], v[126:127] op_sel_hi:[0,1,1]
	s_waitcnt lgkmcnt(8)
	v_pk_fma_f32 v[130:131], v[132:133], v[198:199], v[140:141] op_sel_hi:[1,0,1]
	s_nop 0
	v_pk_fma_f32 v[130:131], v[198:199], v[106:107], v[130:131] op_sel:[1,0,0]
	v_mov_b32_e32 v136, v201
	v_pk_fma_f32 v[130:131], v[200:201], v[134:135], v[130:131] op_sel_hi:[0,1,1]
	v_pk_fma_f32 v[130:131], v[136:137], v[104:105], v[130:131] op_sel_hi:[0,1,1]
	ds_read_b128 v[250:253], v25 offset:26672
	s_waitcnt lgkmcnt(8)
	v_pk_fma_f32 v[140:141], v[132:133], v[202:203], v[142:143] op_sel_hi:[1,0,1]
	s_nop 0
	v_pk_fma_f32 v[136:137], v[202:203], v[106:107], v[140:141] op_sel:[1,0,0]
	s_nop 0
	v_pk_fma_f32 v[136:137], v[204:205], v[134:135], v[136:137] op_sel_hi:[0,1,1]
	v_mov_b32_e32 v138, v205
	v_pk_fma_f32 v[136:137], v[138:139], v[104:105], v[136:137] op_sel_hi:[0,1,1]
	ds_read_b128 v[162:165], v25 offset:34880
	s_waitcnt lgkmcnt(8)
	v_pk_fma_f32 v[142:143], v[132:133], v[216:217], v[144:145] op_sel_hi:[1,0,1]
	s_nop 0
	v_pk_fma_f32 v[138:139], v[216:217], v[106:107], v[142:143] op_sel:[1,0,0]
	s_nop 0
	v_pk_fma_f32 v[138:139], v[218:219], v[134:135], v[138:139] op_sel_hi:[0,1,1]
	v_mov_b32_e32 v140, v219
	v_pk_fma_f32 v[138:139], v[140:141], v[104:105], v[138:139] op_sel_hi:[0,1,1]
	ds_read_b128 v[166:169], v25 offset:43088
	s_waitcnt lgkmcnt(8)
	v_pk_fma_f32 v[144:145], v[132:133], v[220:221], v[146:147] op_sel_hi:[1,0,1]
	s_nop 0
	v_pk_fma_f32 v[140:141], v[220:221], v[106:107], v[144:145] op_sel:[1,0,0]
	s_nop 0
	v_pk_fma_f32 v[140:141], v[222:223], v[134:135], v[140:141] op_sel_hi:[0,1,1]
	v_mov_b32_e32 v142, v223
	v_pk_fma_f32 v[140:141], v[142:143], v[104:105], v[140:141] op_sel_hi:[0,1,1]
	ds_read_b128 v[170:173], v25 offset:51296
	s_waitcnt lgkmcnt(8)
; #define LAS __attribute__((address_space(3)))
; __global__ void __launch_bounds__(NTHREADS, 2) hybrid_fwd(Args a) {
;     ...
; #pragma unroll
;                     for (int j = 0; j < 8; ++j) {
; #pragma unroll
;                         for (int e = 0; e < 16; ++e) { const f32x4 w = *(const LAS f32x4*)(rwT + e * 2052 + j * 256 + lane * 4);
;                             acc2[e] += y2[j][0] * (f32x2){w[0], w[0]}; acc2[e] += y2[j][1] * (f32x2){w[1], w[1]};
;                             acc2[e] += y2[j][2] * (f32x2){w[2], w[2]}; acc2[e] += y2[j][3] * (f32x2){w[3], w[3]}; }
	v_pk_fma_f32 v[146:147], v[132:133], v[224:225], v[148:149] op_sel_hi:[1,0,1]
	s_nop 0
	v_pk_fma_f32 v[142:143], v[224:225], v[106:107], v[146:147] op_sel:[1,0,0]
	s_nop 0
	v_pk_fma_f32 v[142:143], v[226:227], v[134:135], v[142:143] op_sel_hi:[0,1,1]
	v_mov_b32_e32 v144, v227
	v_pk_fma_f32 v[142:143], v[144:145], v[104:105], v[142:143] op_sel_hi:[0,1,1]
	ds_read_b128 v[174:177], v25 offset:59504
	s_waitcnt lgkmcnt(8)
	v_pk_fma_f32 v[132:133], v[132:133], v[228:229], v[150:151] op_sel_hi:[1,0,1]
	s_nop 0
	v_pk_fma_f32 v[106:107], v[228:229], v[106:107], v[132:133] op_sel:[1,0,0]
	v_mov_b32_e32 v132, v231
	v_pk_fma_f32 v[106:107], v[230:231], v[134:135], v[106:107] op_sel_hi:[0,1,1]
	v_pk_fma_f32 v[144:145], v[132:133], v[104:105], v[106:107] op_sel_hi:[0,1,1]
	ds_read_b128 v[178:181], v238 offset:2176
	ds_read_b128 v[182:185], v238 offset:10384
	s_waitcnt lgkmcnt(8)
	v_pk_fma_f32 v[112:113], v[108:109], v[232:233], v[112:113] op_sel_hi:[1,0,1]
	s_nop 0
	v_pk_fma_f32 v[104:105], v[232:233], v[98:99], v[112:113] op_sel:[1,0,0]
	v_mov_b32_e32 v112, v245
	v_pk_fma_f32 v[104:105], v[234:235], v[110:111], v[104:105] op_sel_hi:[0,1,1]
	v_mov_b32_e32 v106, v235
	v_pk_fma_f32 v[104:105], v[106:107], v[96:97], v[104:105] op_sel_hi:[0,1,1]
	v_pk_fma_f32 v[106:107], v[108:109], v[242:243], v[152:153] op_sel_hi:[1,0,1]
	s_nop 0
	v_pk_fma_f32 v[106:107], v[242:243], v[98:99], v[106:107] op_sel:[1,0,0]
	s_nop 0
	v_pk_fma_f32 v[106:107], v[244:245], v[110:111], v[106:107] op_sel_hi:[0,1,1]
	ds_read_b128 v[186:189], v238 offset:18592
	v_pk_fma_f32 v[146:147], v[112:113], v[96:97], v[106:107] op_sel_hi:[0,1,1]
	s_waitcnt lgkmcnt(8)
	v_pk_fma_f32 v[106:107], v[108:109], v[246:247], v[128:129] op_sel_hi:[1,0,1]
	s_nop 0
	v_pk_fma_f32 v[106:107], v[246:247], v[98:99], v[106:107] op_sel:[1,0,0]
	v_mov_b32_e32 v112, v249
	v_pk_fma_f32 v[106:107], v[248:249], v[110:111], v[106:107] op_sel_hi:[0,1,1]
	ds_read_b128 v[158:161], v238 offset:26800
	v_pk_fma_f32 v[106:107], v[112:113], v[96:97], v[106:107] op_sel_hi:[0,1,1]
	s_waitcnt lgkmcnt(8)
	v_pk_fma_f32 v[112:113], v[108:109], v[250:251], v[114:115] op_sel_hi:[1,0,1]
	s_nop 0
	v_pk_fma_f32 v[112:113], v[250:251], v[98:99], v[112:113] op_sel:[1,0,0]
	v_mov_b32_e32 v114, v253
	v_pk_fma_f32 v[112:113], v[252:253], v[110:111], v[112:113] op_sel_hi:[0,1,1]
	ds_read_b128 v[198:201], v238 offset:35008
	v_pk_fma_f32 v[112:113], v[114:115], v[96:97], v[112:113] op_sel_hi:[0,1,1]
	s_waitcnt lgkmcnt(8)
	v_pk_fma_f32 v[114:115], v[108:109], v[162:163], v[116:117] op_sel_hi:[1,0,1]
	s_nop 0
	v_pk_fma_f32 v[114:115], v[162:163], v[98:99], v[114:115] op_sel:[1,0,0]
	v_mov_b32_e32 v116, v165
	v_pk_fma_f32 v[114:115], v[164:165], v[110:111], v[114:115] op_sel_hi:[0,1,1]
	ds_read_b128 v[202:205], v238 offset:43216
	v_pk_fma_f32 v[114:115], v[116:117], v[96:97], v[114:115] op_sel_hi:[0,1,1]
	s_waitcnt lgkmcnt(8)
	v_pk_fma_f32 v[116:117], v[108:109], v[166:167], v[118:119] op_sel_hi:[1,0,1]
	s_nop 0
	v_pk_fma_f32 v[116:117], v[166:167], v[98:99], v[116:117] op_sel:[1,0,0]
	v_mov_b32_e32 v118, v169
	v_pk_fma_f32 v[116:117], v[168:169], v[110:111], v[116:117] op_sel_hi:[0,1,1]
	ds_read_b128 v[216:219], v238 offset:51424
	v_pk_fma_f32 v[116:117], v[118:119], v[96:97], v[116:117] op_sel_hi:[0,1,1]
	s_waitcnt lgkmcnt(8)
	v_pk_fma_f32 v[118:119], v[108:109], v[170:171], v[120:121] op_sel_hi:[1,0,1]
	s_nop 0
	v_pk_fma_f32 v[118:119], v[170:171], v[98:99], v[118:119] op_sel:[1,0,0]
	v_mov_b32_e32 v120, v173
	v_pk_fma_f32 v[118:119], v[172:173], v[110:111], v[118:119] op_sel_hi:[0,1,1]
	ds_read_b128 v[220:223], v238 offset:59632
	v_pk_fma_f32 v[118:119], v[120:121], v[96:97], v[118:119] op_sel_hi:[0,1,1]
	s_waitcnt lgkmcnt(8)
	v_pk_fma_f32 v[120:121], v[108:109], v[174:175], v[122:123] op_sel_hi:[1,0,1]
	s_nop 0
	v_pk_fma_f32 v[120:121], v[174:175], v[98:99], v[120:121] op_sel:[1,0,0]
	v_mov_b32_e32 v122, v177
	v_pk_fma_f32 v[120:121], v[176:177], v[110:111], v[120:121] op_sel_hi:[0,1,1]
	ds_read_b128 v[224:227], v25 offset:3072
	v_pk_fma_f32 v[120:121], v[122:123], v[96:97], v[120:121] op_sel_hi:[0,1,1]
	s_waitcnt lgkmcnt(8)
	v_pk_fma_f32 v[122:123], v[108:109], v[178:179], v[124:125] op_sel_hi:[1,0,1]
	s_nop 0
	v_pk_fma_f32 v[122:123], v[178:179], v[98:99], v[122:123] op_sel:[1,0,0]
	v_mov_b32_e32 v124, v181
	v_pk_fma_f32 v[122:123], v[180:181], v[110:111], v[122:123] op_sel_hi:[0,1,1]
	ds_read_b128 v[228:231], v25 offset:11280
	v_pk_fma_f32 v[122:123], v[124:125], v[96:97], v[122:123] op_sel_hi:[0,1,1]
	s_waitcnt lgkmcnt(8)
	v_pk_fma_f32 v[124:125], v[108:109], v[182:183], v[126:127] op_sel_hi:[1,0,1]
	s_nop 0
	v_pk_fma_f32 v[124:125], v[182:183], v[98:99], v[124:125] op_sel:[1,0,0]
	v_mov_b32_e32 v126, v185
	v_pk_fma_f32 v[124:125], v[184:185], v[110:111], v[124:125] op_sel_hi:[0,1,1]
	v_pk_fma_f32 v[124:125], v[126:127], v[96:97], v[124:125] op_sel_hi:[0,1,1]
	ds_read_b128 v[232:235], v25 offset:19488
	s_waitcnt lgkmcnt(8)
	v_pk_fma_f32 v[130:131], v[108:109], v[186:187], v[130:131] op_sel_hi:[1,0,1]
	s_nop 0
	v_pk_fma_f32 v[126:127], v[186:187], v[98:99], v[130:131] op_sel:[1,0,0]
	s_nop 0
	v_pk_fma_f32 v[126:127], v[188:189], v[110:111], v[126:127] op_sel_hi:[0,1,1]
	v_mov_b32_e32 v128, v189
	v_pk_fma_f32 v[126:127], v[128:129], v[96:97], v[126:127] op_sel_hi:[0,1,1]
	ds_read_b128 v[242:245], v25 offset:27696
	s_waitcnt lgkmcnt(8)
	v_pk_fma_f32 v[132:133], v[108:109], v[158:159], v[136:137] op_sel_hi:[1,0,1]
	s_nop 0
	v_pk_fma_f32 v[128:129], v[158:159], v[98:99], v[132:133] op_sel:[1,0,0]
	s_nop 0
	v_pk_fma_f32 v[128:129], v[160:161], v[110:111], v[128:129] op_sel_hi:[0,1,1]
	v_mov_b32_e32 v130, v161
	v_pk_fma_f32 v[128:129], v[130:131], v[96:97], v[128:129] op_sel_hi:[0,1,1]
	ds_read_b128 v[246:249], v25 offset:35904
	s_waitcnt lgkmcnt(8)
; #define LAS __attribute__((address_space(3)))
; __global__ void __launch_bounds__(NTHREADS, 2) hybrid_fwd(Args a) {
;     ...
; #pragma unroll
;                     for (int j = 0; j < 8; ++j) {
; #pragma unroll
;                         for (int e = 0; e < 16; ++e) { const f32x4 w = *(const LAS f32x4*)(rwT + e * 2052 + j * 256 + lane * 4);
;                             acc2[e] += y2[j][0] * (f32x2){w[0], w[0]}; acc2[e] += y2[j][1] * (f32x2){w[1], w[1]};
;                             acc2[e] += y2[j][2] * (f32x2){w[2], w[2]}; acc2[e] += y2[j][3] * (f32x2){w[3], w[3]}; }
	v_pk_fma_f32 v[134:135], v[108:109], v[198:199], v[138:139] op_sel_hi:[1,0,1]
	s_nop 0
	v_pk_fma_f32 v[130:131], v[198:199], v[98:99], v[134:135] op_sel:[1,0,0]
	s_nop 0
	v_pk_fma_f32 v[130:131], v[200:201], v[110:111], v[130:131] op_sel_hi:[0,1,1]
	v_mov_b32_e32 v132, v201
	v_pk_fma_f32 v[130:131], v[132:133], v[96:97], v[130:131] op_sel_hi:[0,1,1]
	ds_read_b128 v[250:253], v25 offset:44112
	s_waitcnt lgkmcnt(8)
	v_pk_fma_f32 v[136:137], v[108:109], v[202:203], v[140:141] op_sel_hi:[1,0,1]
	s_nop 0
	v_pk_fma_f32 v[132:133], v[202:203], v[98:99], v[136:137] op_sel:[1,0,0]
	s_nop 0
	v_pk_fma_f32 v[132:133], v[204:205], v[110:111], v[132:133] op_sel_hi:[0,1,1]
	v_mov_b32_e32 v134, v205
	v_pk_fma_f32 v[132:133], v[134:135], v[96:97], v[132:133] op_sel_hi:[0,1,1]
	ds_read_b128 v[162:165], v25 offset:52320
	s_waitcnt lgkmcnt(8)
	v_pk_fma_f32 v[138:139], v[108:109], v[216:217], v[142:143] op_sel_hi:[1,0,1]
	s_nop 0
	v_pk_fma_f32 v[134:135], v[216:217], v[98:99], v[138:139] op_sel:[1,0,0]
	s_nop 0
	v_pk_fma_f32 v[134:135], v[218:219], v[110:111], v[134:135] op_sel_hi:[0,1,1]
	v_mov_b32_e32 v136, v219
	v_pk_fma_f32 v[134:135], v[136:137], v[96:97], v[134:135] op_sel_hi:[0,1,1]
	ds_read_b128 v[166:169], v25 offset:60528
	s_waitcnt lgkmcnt(8)
	v_pk_fma_f32 v[108:109], v[108:109], v[220:221], v[144:145] op_sel_hi:[1,0,1]
	s_nop 0
	v_pk_fma_f32 v[98:99], v[220:221], v[98:99], v[108:109] op_sel:[1,0,0]
	v_mov_b32_e32 v108, v223
	v_pk_fma_f32 v[98:99], v[222:223], v[110:111], v[98:99] op_sel_hi:[0,1,1]
	v_pk_fma_f32 v[136:137], v[108:109], v[96:97], v[98:99] op_sel_hi:[0,1,1]
	ds_read_b128 v[170:173], v238 offset:3200
	ds_read_b128 v[174:177], v238 offset:11408
	s_waitcnt lgkmcnt(8)
	v_pk_fma_f32 v[104:105], v[100:101], v[224:225], v[104:105] op_sel_hi:[1,0,1]
	s_nop 0
	v_pk_fma_f32 v[96:97], v[224:225], v[90:91], v[104:105] op_sel:[1,0,0]
	v_mov_b32_e32 v104, v231
	v_pk_fma_f32 v[96:97], v[226:227], v[102:103], v[96:97] op_sel_hi:[0,1,1]
	v_mov_b32_e32 v98, v227
	v_pk_fma_f32 v[96:97], v[98:99], v[88:89], v[96:97] op_sel_hi:[0,1,1]
	v_pk_fma_f32 v[98:99], v[100:101], v[228:229], v[146:147] op_sel_hi:[1,0,1]
	s_nop 0
	v_pk_fma_f32 v[98:99], v[228:229], v[90:91], v[98:99] op_sel:[1,0,0]
	s_nop 0
	v_pk_fma_f32 v[98:99], v[230:231], v[102:103], v[98:99] op_sel_hi:[0,1,1]
	ds_read_b128 v[178:181], v238 offset:19616
	v_pk_fma_f32 v[138:139], v[104:105], v[88:89], v[98:99] op_sel_hi:[0,1,1]
	s_waitcnt lgkmcnt(8)
	v_pk_fma_f32 v[98:99], v[100:101], v[232:233], v[106:107] op_sel_hi:[1,0,1]
	s_nop 0
	v_pk_fma_f32 v[98:99], v[232:233], v[90:91], v[98:99] op_sel:[1,0,0]
	v_mov_b32_e32 v104, v235
	v_pk_fma_f32 v[98:99], v[234:235], v[102:103], v[98:99] op_sel_hi:[0,1,1]
	v_pk_fma_f32 v[98:99], v[104:105], v[88:89], v[98:99] op_sel_hi:[0,1,1]
	ds_read_b128 v[182:185], v238 offset:27824
	s_waitcnt lgkmcnt(8)
	v_pk_fma_f32 v[108:109], v[100:101], v[242:243], v[112:113] op_sel_hi:[1,0,1]
	s_nop 0
	v_pk_fma_f32 v[104:105], v[242:243], v[90:91], v[108:109] op_sel:[1,0,0]
	s_nop 0
	v_pk_fma_f32 v[104:105], v[244:245], v[102:103], v[104:105] op_sel_hi:[0,1,1]
	v_mov_b32_e32 v106, v245
	v_pk_fma_f32 v[104:105], v[106:107], v[88:89], v[104:105] op_sel_hi:[0,1,1]
	ds_read_b128 v[186:189], v238 offset:36032
	s_waitcnt lgkmcnt(8)
	v_pk_fma_f32 v[110:111], v[100:101], v[246:247], v[114:115] op_sel_hi:[1,0,1]
	s_nop 0
	v_pk_fma_f32 v[106:107], v[246:247], v[90:91], v[110:111] op_sel:[1,0,0]
	s_nop 0
	v_pk_fma_f32 v[106:107], v[248:249], v[102:103], v[106:107] op_sel_hi:[0,1,1]
	v_mov_b32_e32 v108, v249
	v_pk_fma_f32 v[106:107], v[108:109], v[88:89], v[106:107] op_sel_hi:[0,1,1]
	ds_read_b128 v[158:161], v238 offset:44240
	s_waitcnt lgkmcnt(8)
	v_pk_fma_f32 v[112:113], v[100:101], v[250:251], v[116:117] op_sel_hi:[1,0,1]
	s_nop 0
	v_pk_fma_f32 v[108:109], v[250:251], v[90:91], v[112:113] op_sel:[1,0,0]
	s_nop 0
	v_pk_fma_f32 v[108:109], v[252:253], v[102:103], v[108:109] op_sel_hi:[0,1,1]
	v_mov_b32_e32 v110, v253
	v_pk_fma_f32 v[108:109], v[110:111], v[88:89], v[108:109] op_sel_hi:[0,1,1]
	ds_read_b128 v[198:201], v238 offset:52448
	s_waitcnt lgkmcnt(8)
	v_pk_fma_f32 v[114:115], v[100:101], v[162:163], v[118:119] op_sel_hi:[1,0,1]
	s_nop 0
	v_pk_fma_f32 v[110:111], v[162:163], v[90:91], v[114:115] op_sel:[1,0,0]
	s_nop 0
	v_pk_fma_f32 v[110:111], v[164:165], v[102:103], v[110:111] op_sel_hi:[0,1,1]
	v_mov_b32_e32 v112, v165
	v_pk_fma_f32 v[110:111], v[112:113], v[88:89], v[110:111] op_sel_hi:[0,1,1]
	ds_read_b128 v[202:205], v238 offset:60656
	s_waitcnt lgkmcnt(8)
	v_pk_fma_f32 v[116:117], v[100:101], v[166:167], v[120:121] op_sel_hi:[1,0,1]
	s_nop 0
	v_pk_fma_f32 v[112:113], v[166:167], v[90:91], v[116:117] op_sel:[1,0,0]
	s_nop 0
	v_pk_fma_f32 v[112:113], v[168:169], v[102:103], v[112:113] op_sel_hi:[0,1,1]
	v_mov_b32_e32 v114, v169
	v_pk_fma_f32 v[112:113], v[114:115], v[88:89], v[112:113] op_sel_hi:[0,1,1]
	ds_read_b128 v[216:219], v25 offset:4096
	s_waitcnt lgkmcnt(8)
	v_pk_fma_f32 v[118:119], v[100:101], v[170:171], v[122:123] op_sel_hi:[1,0,1]
	s_nop 0
	v_pk_fma_f32 v[114:115], v[170:171], v[90:91], v[118:119] op_sel:[1,0,0]
	s_nop 0
	v_pk_fma_f32 v[114:115], v[172:173], v[102:103], v[114:115] op_sel_hi:[0,1,1]
	v_mov_b32_e32 v116, v173
	v_pk_fma_f32 v[114:115], v[116:117], v[88:89], v[114:115] op_sel_hi:[0,1,1]
	ds_read_b128 v[220:223], v25 offset:12304
	s_waitcnt lgkmcnt(8)
	v_pk_fma_f32 v[120:121], v[100:101], v[174:175], v[124:125] op_sel_hi:[1,0,1]
	s_nop 0
	v_pk_fma_f32 v[116:117], v[174:175], v[90:91], v[120:121] op_sel:[1,0,0]
	s_nop 0
	v_pk_fma_f32 v[116:117], v[176:177], v[102:103], v[116:117] op_sel_hi:[0,1,1]
	v_mov_b32_e32 v118, v177
	v_pk_fma_f32 v[116:117], v[118:119], v[88:89], v[116:117] op_sel_hi:[0,1,1]
	ds_read_b128 v[224:227], v25 offset:20512
	s_waitcnt lgkmcnt(8)
; #define LAS __attribute__((address_space(3)))
; __global__ void __launch_bounds__(NTHREADS, 2) hybrid_fwd(Args a) {
;     ...
; #pragma unroll
;                     for (int j = 0; j < 8; ++j) {
; #pragma unroll
;                         for (int e = 0; e < 16; ++e) { const f32x4 w = *(const LAS f32x4*)(rwT + e * 2052 + j * 256 + lane * 4);
;                             acc2[e] += y2[j][0] * (f32x2){w[0], w[0]}; acc2[e] += y2[j][1] * (f32x2){w[1], w[1]};
;                             acc2[e] += y2[j][2] * (f32x2){w[2], w[2]}; acc2[e] += y2[j][3] * (f32x2){w[3], w[3]}; }
	v_pk_fma_f32 v[122:123], v[100:101], v[178:179], v[126:127] op_sel_hi:[1,0,1]
	s_nop 0
	v_pk_fma_f32 v[118:119], v[178:179], v[90:91], v[122:123] op_sel:[1,0,0]
	s_nop 0
	v_pk_fma_f32 v[118:119], v[180:181], v[102:103], v[118:119] op_sel_hi:[0,1,1]
	v_mov_b32_e32 v120, v181
	v_pk_fma_f32 v[118:119], v[120:121], v[88:89], v[118:119] op_sel_hi:[0,1,1]
	ds_read_b128 v[228:231], v25 offset:28720
	s_waitcnt lgkmcnt(8)
	v_pk_fma_f32 v[124:125], v[100:101], v[182:183], v[128:129] op_sel_hi:[1,0,1]
	s_nop 0
	v_pk_fma_f32 v[120:121], v[182:183], v[90:91], v[124:125] op_sel:[1,0,0]
	s_nop 0
	v_pk_fma_f32 v[120:121], v[184:185], v[102:103], v[120:121] op_sel_hi:[0,1,1]
	v_mov_b32_e32 v122, v185
	v_pk_fma_f32 v[120:121], v[122:123], v[88:89], v[120:121] op_sel_hi:[0,1,1]
	ds_read_b128 v[232:235], v25 offset:36928
	s_waitcnt lgkmcnt(8)
	v_pk_fma_f32 v[126:127], v[100:101], v[186:187], v[130:131] op_sel_hi:[1,0,1]
	s_nop 0
	v_pk_fma_f32 v[122:123], v[186:187], v[90:91], v[126:127] op_sel:[1,0,0]
	s_nop 0
	v_pk_fma_f32 v[122:123], v[188:189], v[102:103], v[122:123] op_sel_hi:[0,1,1]
	v_mov_b32_e32 v124, v189
	v_pk_fma_f32 v[122:123], v[124:125], v[88:89], v[122:123] op_sel_hi:[0,1,1]
	ds_read_b128 v[242:245], v25 offset:45136
	s_waitcnt lgkmcnt(8)
	v_pk_fma_f32 v[128:129], v[100:101], v[158:159], v[132:133] op_sel_hi:[1,0,1]
	s_nop 0
	v_pk_fma_f32 v[124:125], v[158:159], v[90:91], v[128:129] op_sel:[1,0,0]
	s_nop 0
	v_pk_fma_f32 v[124:125], v[160:161], v[102:103], v[124:125] op_sel_hi:[0,1,1]
	v_mov_b32_e32 v126, v161
	v_pk_fma_f32 v[124:125], v[126:127], v[88:89], v[124:125] op_sel_hi:[0,1,1]
	ds_read_b128 v[246:249], v25 offset:53344
	s_waitcnt lgkmcnt(8)
	v_pk_fma_f32 v[130:131], v[100:101], v[198:199], v[134:135] op_sel_hi:[1,0,1]
	s_nop 0
	v_pk_fma_f32 v[126:127], v[198:199], v[90:91], v[130:131] op_sel:[1,0,0]
	s_nop 0
	v_pk_fma_f32 v[126:127], v[200:201], v[102:103], v[126:127] op_sel_hi:[0,1,1]
	v_mov_b32_e32 v128, v201
	v_pk_fma_f32 v[126:127], v[128:129], v[88:89], v[126:127] op_sel_hi:[0,1,1]
	ds_read_b128 v[250:253], v25 offset:61552
	s_waitcnt lgkmcnt(8)
	v_pk_fma_f32 v[100:101], v[100:101], v[202:203], v[136:137] op_sel_hi:[1,0,1]
	s_nop 0
	v_pk_fma_f32 v[90:91], v[202:203], v[90:91], v[100:101] op_sel:[1,0,0]
	v_mov_b32_e32 v100, v205
	v_pk_fma_f32 v[90:91], v[204:205], v[102:103], v[90:91] op_sel_hi:[0,1,1]
	v_pk_fma_f32 v[128:129], v[100:101], v[88:89], v[90:91] op_sel_hi:[0,1,1]
	ds_read_b128 v[162:165], v238 offset:4224
	ds_read_b128 v[166:169], v238 offset:12432
	s_waitcnt lgkmcnt(8)
	v_pk_fma_f32 v[96:97], v[92:93], v[216:217], v[96:97] op_sel_hi:[1,0,1]
	s_nop 0
	v_pk_fma_f32 v[88:89], v[216:217], v[86:87], v[96:97] op_sel:[1,0,0]
	v_mov_b32_e32 v96, v223
	v_pk_fma_f32 v[88:89], v[218:219], v[94:95], v[88:89] op_sel_hi:[0,1,1]
	v_mov_b32_e32 v90, v219
	v_pk_fma_f32 v[88:89], v[90:91], v[84:85], v[88:89] op_sel_hi:[0,1,1]
	v_pk_fma_f32 v[90:91], v[92:93], v[220:221], v[138:139] op_sel_hi:[1,0,1]
	s_nop 0
	v_pk_fma_f32 v[90:91], v[220:221], v[86:87], v[90:91] op_sel:[1,0,0]
	s_nop 0
	v_pk_fma_f32 v[90:91], v[222:223], v[94:95], v[90:91] op_sel_hi:[0,1,1]
	ds_read_b128 v[170:173], v238 offset:20640
	v_pk_fma_f32 v[130:131], v[96:97], v[84:85], v[90:91] op_sel_hi:[0,1,1]
	s_waitcnt lgkmcnt(8)
	v_pk_fma_f32 v[90:91], v[92:93], v[224:225], v[98:99] op_sel_hi:[1,0,1]
	s_nop 0
	v_pk_fma_f32 v[90:91], v[224:225], v[86:87], v[90:91] op_sel:[1,0,0]
	v_mov_b32_e32 v96, v227
	v_pk_fma_f32 v[90:91], v[226:227], v[94:95], v[90:91] op_sel_hi:[0,1,1]
	v_pk_fma_f32 v[90:91], v[96:97], v[84:85], v[90:91] op_sel_hi:[0,1,1]
	ds_read_b128 v[174:177], v238 offset:28848
	s_waitcnt lgkmcnt(8)
	v_pk_fma_f32 v[100:101], v[92:93], v[228:229], v[104:105] op_sel_hi:[1,0,1]
	s_nop 0
	v_pk_fma_f32 v[96:97], v[228:229], v[86:87], v[100:101] op_sel:[1,0,0]
	s_nop 0
	v_pk_fma_f32 v[96:97], v[230:231], v[94:95], v[96:97] op_sel_hi:[0,1,1]
	v_mov_b32_e32 v98, v231
	v_pk_fma_f32 v[96:97], v[98:99], v[84:85], v[96:97] op_sel_hi:[0,1,1]
	ds_read_b128 v[178:181], v238 offset:37056
	s_waitcnt lgkmcnt(8)
	v_pk_fma_f32 v[102:103], v[92:93], v[232:233], v[106:107] op_sel_hi:[1,0,1]
	s_nop 0
	v_pk_fma_f32 v[98:99], v[232:233], v[86:87], v[102:103] op_sel:[1,0,0]
	s_nop 0
	v_pk_fma_f32 v[98:99], v[234:235], v[94:95], v[98:99] op_sel_hi:[0,1,1]
	v_mov_b32_e32 v100, v235
	v_pk_fma_f32 v[98:99], v[100:101], v[84:85], v[98:99] op_sel_hi:[0,1,1]
	ds_read_b128 v[182:185], v238 offset:45264
	s_waitcnt lgkmcnt(8)
	v_pk_fma_f32 v[104:105], v[92:93], v[242:243], v[108:109] op_sel_hi:[1,0,1]
	s_nop 0
	v_pk_fma_f32 v[100:101], v[242:243], v[86:87], v[104:105] op_sel:[1,0,0]
	s_nop 0
	v_pk_fma_f32 v[100:101], v[244:245], v[94:95], v[100:101] op_sel_hi:[0,1,1]
	v_mov_b32_e32 v102, v245
	v_pk_fma_f32 v[100:101], v[102:103], v[84:85], v[100:101] op_sel_hi:[0,1,1]
	ds_read_b128 v[186:189], v238 offset:53472
	s_waitcnt lgkmcnt(8)
	v_pk_fma_f32 v[106:107], v[92:93], v[246:247], v[110:111] op_sel_hi:[1,0,1]
	s_nop 0
	v_pk_fma_f32 v[102:103], v[246:247], v[86:87], v[106:107] op_sel:[1,0,0]
	s_nop 0
	v_pk_fma_f32 v[102:103], v[248:249], v[94:95], v[102:103] op_sel_hi:[0,1,1]
	v_mov_b32_e32 v104, v249
	v_pk_fma_f32 v[102:103], v[104:105], v[84:85], v[102:103] op_sel_hi:[0,1,1]
	ds_read_b128 v[158:161], v238 offset:61680
	s_waitcnt lgkmcnt(8)
	v_pk_fma_f32 v[108:109], v[92:93], v[250:251], v[112:113] op_sel_hi:[1,0,1]
	s_nop 0
	v_pk_fma_f32 v[104:105], v[250:251], v[86:87], v[108:109] op_sel:[1,0,0]
	s_nop 0
	v_pk_fma_f32 v[104:105], v[252:253], v[94:95], v[104:105] op_sel_hi:[0,1,1]
	v_mov_b32_e32 v106, v253
	v_pk_fma_f32 v[104:105], v[106:107], v[84:85], v[104:105] op_sel_hi:[0,1,1]
	ds_read_b128 v[198:201], v25 offset:5120
	s_waitcnt lgkmcnt(8)
; #define LAS __attribute__((address_space(3)))
; __global__ void __launch_bounds__(NTHREADS, 2) hybrid_fwd(Args a) {
;     ...
; #pragma unroll
;                     for (int j = 0; j < 8; ++j) {
; #pragma unroll
;                         for (int e = 0; e < 16; ++e) { const f32x4 w = *(const LAS f32x4*)(rwT + e * 2052 + j * 256 + lane * 4);
;                             acc2[e] += y2[j][0] * (f32x2){w[0], w[0]}; acc2[e] += y2[j][1] * (f32x2){w[1], w[1]};
;                             acc2[e] += y2[j][2] * (f32x2){w[2], w[2]}; acc2[e] += y2[j][3] * (f32x2){w[3], w[3]}; }
	v_pk_fma_f32 v[110:111], v[92:93], v[162:163], v[114:115] op_sel_hi:[1,0,1]
	s_nop 0
	v_pk_fma_f32 v[106:107], v[162:163], v[86:87], v[110:111] op_sel:[1,0,0]
	s_nop 0
	v_pk_fma_f32 v[106:107], v[164:165], v[94:95], v[106:107] op_sel_hi:[0,1,1]
	v_mov_b32_e32 v108, v165
	v_pk_fma_f32 v[106:107], v[108:109], v[84:85], v[106:107] op_sel_hi:[0,1,1]
	ds_read_b128 v[202:205], v25 offset:13328
	s_waitcnt lgkmcnt(8)
	v_pk_fma_f32 v[112:113], v[92:93], v[166:167], v[116:117] op_sel_hi:[1,0,1]
	s_nop 0
	v_pk_fma_f32 v[108:109], v[166:167], v[86:87], v[112:113] op_sel:[1,0,0]
	s_nop 0
	v_pk_fma_f32 v[108:109], v[168:169], v[94:95], v[108:109] op_sel_hi:[0,1,1]
	v_mov_b32_e32 v110, v169
	v_pk_fma_f32 v[108:109], v[110:111], v[84:85], v[108:109] op_sel_hi:[0,1,1]
	ds_read_b128 v[216:219], v25 offset:21536
	s_waitcnt lgkmcnt(8)
	v_pk_fma_f32 v[114:115], v[92:93], v[170:171], v[118:119] op_sel_hi:[1,0,1]
	s_nop 0
	v_pk_fma_f32 v[110:111], v[170:171], v[86:87], v[114:115] op_sel:[1,0,0]
	s_nop 0
	v_pk_fma_f32 v[110:111], v[172:173], v[94:95], v[110:111] op_sel_hi:[0,1,1]
	v_mov_b32_e32 v112, v173
	v_pk_fma_f32 v[110:111], v[112:113], v[84:85], v[110:111] op_sel_hi:[0,1,1]
	ds_read_b128 v[220:223], v25 offset:29744
	s_waitcnt lgkmcnt(8)
	v_pk_fma_f32 v[116:117], v[92:93], v[174:175], v[120:121] op_sel_hi:[1,0,1]
	s_nop 0
	v_pk_fma_f32 v[112:113], v[174:175], v[86:87], v[116:117] op_sel:[1,0,0]
	s_nop 0
	v_pk_fma_f32 v[112:113], v[176:177], v[94:95], v[112:113] op_sel_hi:[0,1,1]
	v_mov_b32_e32 v114, v177
	v_pk_fma_f32 v[112:113], v[114:115], v[84:85], v[112:113] op_sel_hi:[0,1,1]
	ds_read_b128 v[224:227], v25 offset:37952
	s_waitcnt lgkmcnt(8)
	v_pk_fma_f32 v[118:119], v[92:93], v[178:179], v[122:123] op_sel_hi:[1,0,1]
	s_nop 0
	v_pk_fma_f32 v[114:115], v[178:179], v[86:87], v[118:119] op_sel:[1,0,0]
	s_nop 0
	v_pk_fma_f32 v[114:115], v[180:181], v[94:95], v[114:115] op_sel_hi:[0,1,1]
	v_mov_b32_e32 v116, v181
	v_pk_fma_f32 v[114:115], v[116:117], v[84:85], v[114:115] op_sel_hi:[0,1,1]
	ds_read_b128 v[228:231], v25 offset:46160
	s_waitcnt lgkmcnt(8)
	v_pk_fma_f32 v[120:121], v[92:93], v[182:183], v[124:125] op_sel_hi:[1,0,1]
	s_nop 0
	v_pk_fma_f32 v[116:117], v[182:183], v[86:87], v[120:121] op_sel:[1,0,0]
	s_nop 0
	v_pk_fma_f32 v[116:117], v[184:185], v[94:95], v[116:117] op_sel_hi:[0,1,1]
	v_mov_b32_e32 v118, v185
	v_pk_fma_f32 v[116:117], v[118:119], v[84:85], v[116:117] op_sel_hi:[0,1,1]
	ds_read_b128 v[232:235], v25 offset:54368
	s_waitcnt lgkmcnt(8)
	v_pk_fma_f32 v[122:123], v[92:93], v[186:187], v[126:127] op_sel_hi:[1,0,1]
	s_nop 0
	v_pk_fma_f32 v[118:119], v[186:187], v[86:87], v[122:123] op_sel:[1,0,0]
	s_nop 0
	v_pk_fma_f32 v[118:119], v[188:189], v[94:95], v[118:119] op_sel_hi:[0,1,1]
	v_mov_b32_e32 v120, v189
	v_pk_fma_f32 v[118:119], v[120:121], v[84:85], v[118:119] op_sel_hi:[0,1,1]
	ds_read_b128 v[242:245], v25 offset:62576
	s_waitcnt lgkmcnt(8)
	v_pk_fma_f32 v[92:93], v[92:93], v[158:159], v[128:129] op_sel_hi:[1,0,1]
	s_nop 0
	v_pk_fma_f32 v[86:87], v[158:159], v[86:87], v[92:93] op_sel:[1,0,0]
	v_mov_b32_e32 v92, v161
	v_pk_fma_f32 v[86:87], v[160:161], v[94:95], v[86:87] op_sel_hi:[0,1,1]
	v_pk_fma_f32 v[120:121], v[92:93], v[84:85], v[86:87] op_sel_hi:[0,1,1]
	ds_read_b128 v[246:249], v238 offset:5248
	s_waitcnt lgkmcnt(8)
	v_pk_fma_f32 v[88:89], v[80:81], v[198:199], v[88:89] op_sel_hi:[1,0,1]
	s_nop 0
	v_pk_fma_f32 v[84:85], v[198:199], v[78:79], v[88:89] op_sel:[1,0,0]
	s_nop 0
	v_pk_fma_f32 v[84:85], v[200:201], v[82:83], v[84:85] op_sel_hi:[0,1,1]
	v_mov_b32_e32 v86, v201
	v_pk_fma_f32 v[84:85], v[86:87], v[76:77], v[84:85] op_sel_hi:[0,1,1]
	ds_read_b128 v[250:253], v238 offset:13456
	s_waitcnt lgkmcnt(8)
	v_pk_fma_f32 v[92:93], v[80:81], v[202:203], v[130:131] op_sel_hi:[1,0,1]
	s_nop 0
	v_pk_fma_f32 v[86:87], v[202:203], v[78:79], v[92:93] op_sel:[1,0,0]
	s_nop 0
	v_pk_fma_f32 v[86:87], v[204:205], v[82:83], v[86:87] op_sel_hi:[0,1,1]
	v_mov_b32_e32 v88, v205
	v_pk_fma_f32 v[122:123], v[88:89], v[76:77], v[86:87] op_sel_hi:[0,1,1]
	ds_read_b128 v[162:165], v238 offset:21664
	s_waitcnt lgkmcnt(8)
	v_pk_fma_f32 v[90:91], v[80:81], v[216:217], v[90:91] op_sel_hi:[1,0,1]
	s_nop 0
	v_pk_fma_f32 v[86:87], v[216:217], v[78:79], v[90:91] op_sel:[1,0,0]
	s_nop 0
	v_pk_fma_f32 v[86:87], v[218:219], v[82:83], v[86:87] op_sel_hi:[0,1,1]
	v_mov_b32_e32 v88, v219
	v_pk_fma_f32 v[86:87], v[88:89], v[76:77], v[86:87] op_sel_hi:[0,1,1]
	ds_read_b128 v[166:169], v238 offset:29872
	s_waitcnt lgkmcnt(8)
	v_pk_fma_f32 v[92:93], v[80:81], v[220:221], v[96:97] op_sel_hi:[1,0,1]
	s_nop 0
	v_pk_fma_f32 v[88:89], v[220:221], v[78:79], v[92:93] op_sel:[1,0,0]
	s_nop 0
	v_pk_fma_f32 v[88:89], v[222:223], v[82:83], v[88:89] op_sel_hi:[0,1,1]
	v_mov_b32_e32 v90, v223
	v_pk_fma_f32 v[88:89], v[90:91], v[76:77], v[88:89] op_sel_hi:[0,1,1]
	ds_read_b128 v[170:173], v238 offset:38080
	s_waitcnt lgkmcnt(8)
	v_pk_fma_f32 v[94:95], v[80:81], v[224:225], v[98:99] op_sel_hi:[1,0,1]
	s_nop 0
	v_pk_fma_f32 v[90:91], v[224:225], v[78:79], v[94:95] op_sel:[1,0,0]
	s_nop 0
	v_pk_fma_f32 v[90:91], v[226:227], v[82:83], v[90:91] op_sel_hi:[0,1,1]
	v_mov_b32_e32 v92, v227
	v_pk_fma_f32 v[90:91], v[92:93], v[76:77], v[90:91] op_sel_hi:[0,1,1]
	ds_read_b128 v[174:177], v238 offset:46288
	s_waitcnt lgkmcnt(8)
	v_pk_fma_f32 v[96:97], v[80:81], v[228:229], v[100:101] op_sel_hi:[1,0,1]
	s_nop 0
	v_pk_fma_f32 v[92:93], v[228:229], v[78:79], v[96:97] op_sel:[1,0,0]
	s_nop 0
	v_pk_fma_f32 v[92:93], v[230:231], v[82:83], v[92:93] op_sel_hi:[0,1,1]
	v_mov_b32_e32 v94, v231
	v_pk_fma_f32 v[92:93], v[94:95], v[76:77], v[92:93] op_sel_hi:[0,1,1]
	ds_read_b128 v[178:181], v238 offset:54496
	s_waitcnt lgkmcnt(8)
; #define LAS __attribute__((address_space(3)))
; __global__ void __launch_bounds__(NTHREADS, 2) hybrid_fwd(Args a) {
;     ...
; #pragma unroll
;                     for (int j = 0; j < 8; ++j) {
; #pragma unroll
;                         for (int e = 0; e < 16; ++e) { const f32x4 w = *(const LAS f32x4*)(rwT + e * 2052 + j * 256 + lane * 4);
;                             acc2[e] += y2[j][0] * (f32x2){w[0], w[0]}; acc2[e] += y2[j][1] * (f32x2){w[1], w[1]};
;                             acc2[e] += y2[j][2] * (f32x2){w[2], w[2]}; acc2[e] += y2[j][3] * (f32x2){w[3], w[3]}; }
	v_pk_fma_f32 v[98:99], v[80:81], v[232:233], v[102:103] op_sel_hi:[1,0,1]
	s_nop 0
	v_pk_fma_f32 v[94:95], v[232:233], v[78:79], v[98:99] op_sel:[1,0,0]
	s_nop 0
	v_pk_fma_f32 v[94:95], v[234:235], v[82:83], v[94:95] op_sel_hi:[0,1,1]
	v_mov_b32_e32 v96, v235
	v_pk_fma_f32 v[94:95], v[96:97], v[76:77], v[94:95] op_sel_hi:[0,1,1]
	ds_read_b128 v[182:185], v238 offset:62704
	s_waitcnt lgkmcnt(8)
	v_pk_fma_f32 v[100:101], v[80:81], v[242:243], v[104:105] op_sel_hi:[1,0,1]
	s_nop 0
	v_pk_fma_f32 v[96:97], v[242:243], v[78:79], v[100:101] op_sel:[1,0,0]
	s_nop 0
	v_pk_fma_f32 v[96:97], v[244:245], v[82:83], v[96:97] op_sel_hi:[0,1,1]
	v_mov_b32_e32 v98, v245
	v_pk_fma_f32 v[96:97], v[98:99], v[76:77], v[96:97] op_sel_hi:[0,1,1]
	ds_read_b128 v[186:189], v25 offset:6144
	s_waitcnt lgkmcnt(8)
	v_pk_fma_f32 v[102:103], v[80:81], v[246:247], v[106:107] op_sel_hi:[1,0,1]
	s_nop 0
	v_pk_fma_f32 v[98:99], v[246:247], v[78:79], v[102:103] op_sel:[1,0,0]
	s_nop 0
	v_pk_fma_f32 v[98:99], v[248:249], v[82:83], v[98:99] op_sel_hi:[0,1,1]
	v_mov_b32_e32 v100, v249
	v_pk_fma_f32 v[98:99], v[100:101], v[76:77], v[98:99] op_sel_hi:[0,1,1]
	ds_read_b128 v[158:161], v25 offset:14352
	s_waitcnt lgkmcnt(8)
	v_pk_fma_f32 v[104:105], v[80:81], v[250:251], v[108:109] op_sel_hi:[1,0,1]
	s_nop 0
	v_pk_fma_f32 v[100:101], v[250:251], v[78:79], v[104:105] op_sel:[1,0,0]
	s_nop 0
	v_pk_fma_f32 v[100:101], v[252:253], v[82:83], v[100:101] op_sel_hi:[0,1,1]
	v_mov_b32_e32 v102, v253
	v_pk_fma_f32 v[100:101], v[102:103], v[76:77], v[100:101] op_sel_hi:[0,1,1]
	ds_read_b128 v[198:201], v25 offset:22560
	s_waitcnt lgkmcnt(8)
	v_pk_fma_f32 v[106:107], v[80:81], v[162:163], v[110:111] op_sel_hi:[1,0,1]
	s_nop 0
	v_pk_fma_f32 v[102:103], v[162:163], v[78:79], v[106:107] op_sel:[1,0,0]
	s_nop 0
	v_pk_fma_f32 v[102:103], v[164:165], v[82:83], v[102:103] op_sel_hi:[0,1,1]
	v_mov_b32_e32 v104, v165
	v_pk_fma_f32 v[102:103], v[104:105], v[76:77], v[102:103] op_sel_hi:[0,1,1]
	ds_read_b128 v[202:205], v25 offset:30768
	s_waitcnt lgkmcnt(8)
	v_pk_fma_f32 v[108:109], v[80:81], v[166:167], v[112:113] op_sel_hi:[1,0,1]
	s_nop 0
	v_pk_fma_f32 v[104:105], v[166:167], v[78:79], v[108:109] op_sel:[1,0,0]
	s_nop 0
	v_pk_fma_f32 v[104:105], v[168:169], v[82:83], v[104:105] op_sel_hi:[0,1,1]
	v_mov_b32_e32 v106, v169
	v_pk_fma_f32 v[104:105], v[106:107], v[76:77], v[104:105] op_sel_hi:[0,1,1]
	ds_read_b128 v[216:219], v25 offset:38976
	s_waitcnt lgkmcnt(8)
	v_pk_fma_f32 v[110:111], v[80:81], v[170:171], v[114:115] op_sel_hi:[1,0,1]
	s_nop 0
	v_pk_fma_f32 v[106:107], v[170:171], v[78:79], v[110:111] op_sel:[1,0,0]
	s_nop 0
	v_pk_fma_f32 v[106:107], v[172:173], v[82:83], v[106:107] op_sel_hi:[0,1,1]
	v_mov_b32_e32 v108, v173
	v_pk_fma_f32 v[106:107], v[108:109], v[76:77], v[106:107] op_sel_hi:[0,1,1]
	ds_read_b128 v[220:223], v25 offset:47184
	s_waitcnt lgkmcnt(8)
	v_pk_fma_f32 v[112:113], v[80:81], v[174:175], v[116:117] op_sel_hi:[1,0,1]
	s_nop 0
	v_pk_fma_f32 v[108:109], v[174:175], v[78:79], v[112:113] op_sel:[1,0,0]
	s_nop 0
	v_pk_fma_f32 v[108:109], v[176:177], v[82:83], v[108:109] op_sel_hi:[0,1,1]
	v_mov_b32_e32 v110, v177
	v_pk_fma_f32 v[108:109], v[110:111], v[76:77], v[108:109] op_sel_hi:[0,1,1]
	ds_read_b128 v[224:227], v25 offset:55392
	s_waitcnt lgkmcnt(8)
	v_pk_fma_f32 v[114:115], v[80:81], v[178:179], v[118:119] op_sel_hi:[1,0,1]
	s_nop 0
	v_pk_fma_f32 v[110:111], v[178:179], v[78:79], v[114:115] op_sel:[1,0,0]
	s_nop 0
	v_pk_fma_f32 v[110:111], v[180:181], v[82:83], v[110:111] op_sel_hi:[0,1,1]
	v_mov_b32_e32 v112, v181
	v_pk_fma_f32 v[110:111], v[112:113], v[76:77], v[110:111] op_sel_hi:[0,1,1]
	ds_read_b128 v[228:231], v25 offset:63600
	s_waitcnt lgkmcnt(8)
	v_pk_fma_f32 v[80:81], v[80:81], v[182:183], v[120:121] op_sel_hi:[1,0,1]
	s_nop 0
	v_pk_fma_f32 v[78:79], v[182:183], v[78:79], v[80:81] op_sel:[1,0,0]
	v_mov_b32_e32 v80, v185
	v_pk_fma_f32 v[78:79], v[184:185], v[82:83], v[78:79] op_sel_hi:[0,1,1]
	v_pk_fma_f32 v[112:113], v[80:81], v[76:77], v[78:79] op_sel_hi:[0,1,1]
	ds_read_b128 v[232:235], v238 offset:6272
	s_waitcnt lgkmcnt(8)
	v_pk_fma_f32 v[80:81], v[72:73], v[186:187], v[84:85] op_sel_hi:[1,0,1]
	s_nop 0
	v_pk_fma_f32 v[76:77], v[186:187], v[70:71], v[80:81] op_sel:[1,0,0]
	s_nop 0
	v_pk_fma_f32 v[76:77], v[188:189], v[74:75], v[76:77] op_sel_hi:[0,1,1]
	v_mov_b32_e32 v78, v189
	v_pk_fma_f32 v[76:77], v[78:79], v[68:69], v[76:77] op_sel_hi:[0,1,1]
	ds_read_b128 v[242:245], v238 offset:14480
	s_waitcnt lgkmcnt(8)
	v_pk_fma_f32 v[82:83], v[72:73], v[158:159], v[122:123] op_sel_hi:[1,0,1]
	s_nop 0
	v_pk_fma_f32 v[78:79], v[158:159], v[70:71], v[82:83] op_sel:[1,0,0]
	s_nop 0
	v_pk_fma_f32 v[78:79], v[160:161], v[74:75], v[78:79] op_sel_hi:[0,1,1]
	v_mov_b32_e32 v80, v161
	v_pk_fma_f32 v[114:115], v[80:81], v[68:69], v[78:79] op_sel_hi:[0,1,1]
	ds_read_b128 v[246:249], v238 offset:22688
	s_waitcnt lgkmcnt(8)
	v_pk_fma_f32 v[82:83], v[72:73], v[198:199], v[86:87] op_sel_hi:[1,0,1]
	s_nop 0
	v_pk_fma_f32 v[78:79], v[198:199], v[70:71], v[82:83] op_sel:[1,0,0]
	s_nop 0
	v_pk_fma_f32 v[78:79], v[200:201], v[74:75], v[78:79] op_sel_hi:[0,1,1]
	v_mov_b32_e32 v80, v201
	v_pk_fma_f32 v[78:79], v[80:81], v[68:69], v[78:79] op_sel_hi:[0,1,1]
	ds_read_b128 v[250:253], v238 offset:30896
	s_waitcnt lgkmcnt(8)
	v_pk_fma_f32 v[84:85], v[72:73], v[202:203], v[88:89] op_sel_hi:[1,0,1]
	s_nop 0
	v_pk_fma_f32 v[80:81], v[202:203], v[70:71], v[84:85] op_sel:[1,0,0]
	s_nop 0
	v_pk_fma_f32 v[80:81], v[204:205], v[74:75], v[80:81] op_sel_hi:[0,1,1]
	v_mov_b32_e32 v82, v205
	v_pk_fma_f32 v[80:81], v[82:83], v[68:69], v[80:81] op_sel_hi:[0,1,1]
	ds_read_b128 v[162:165], v238 offset:39104
	s_waitcnt lgkmcnt(8)
; #define LAS __attribute__((address_space(3)))
; __global__ void __launch_bounds__(NTHREADS, 2) hybrid_fwd(Args a) {
;     ...
; #pragma unroll
;                     for (int j = 0; j < 8; ++j) {
; #pragma unroll
;                         for (int e = 0; e < 16; ++e) { const f32x4 w = *(const LAS f32x4*)(rwT + e * 2052 + j * 256 + lane * 4);
;                             acc2[e] += y2[j][0] * (f32x2){w[0], w[0]}; acc2[e] += y2[j][1] * (f32x2){w[1], w[1]};
;                             acc2[e] += y2[j][2] * (f32x2){w[2], w[2]}; acc2[e] += y2[j][3] * (f32x2){w[3], w[3]}; }
	v_pk_fma_f32 v[86:87], v[72:73], v[216:217], v[90:91] op_sel_hi:[1,0,1]
	s_nop 0
	v_pk_fma_f32 v[82:83], v[216:217], v[70:71], v[86:87] op_sel:[1,0,0]
	s_nop 0
	v_pk_fma_f32 v[82:83], v[218:219], v[74:75], v[82:83] op_sel_hi:[0,1,1]
	v_mov_b32_e32 v84, v219
	v_pk_fma_f32 v[82:83], v[84:85], v[68:69], v[82:83] op_sel_hi:[0,1,1]
	ds_read_b128 v[166:169], v238 offset:47312
	s_waitcnt lgkmcnt(8)
	v_pk_fma_f32 v[88:89], v[72:73], v[220:221], v[92:93] op_sel_hi:[1,0,1]
	s_nop 0
	v_pk_fma_f32 v[84:85], v[220:221], v[70:71], v[88:89] op_sel:[1,0,0]
	s_nop 0
	v_pk_fma_f32 v[84:85], v[222:223], v[74:75], v[84:85] op_sel_hi:[0,1,1]
	v_mov_b32_e32 v86, v223
	v_pk_fma_f32 v[84:85], v[86:87], v[68:69], v[84:85] op_sel_hi:[0,1,1]
	ds_read_b128 v[170:173], v238 offset:55520
	s_waitcnt lgkmcnt(8)
	v_pk_fma_f32 v[90:91], v[72:73], v[224:225], v[94:95] op_sel_hi:[1,0,1]
	s_nop 0
	v_pk_fma_f32 v[86:87], v[224:225], v[70:71], v[90:91] op_sel:[1,0,0]
	s_nop 0
	v_pk_fma_f32 v[86:87], v[226:227], v[74:75], v[86:87] op_sel_hi:[0,1,1]
	v_mov_b32_e32 v88, v227
	v_pk_fma_f32 v[86:87], v[88:89], v[68:69], v[86:87] op_sel_hi:[0,1,1]
	ds_read_b128 v[174:177], v238 offset:63728
	s_waitcnt lgkmcnt(8)
	v_pk_fma_f32 v[92:93], v[72:73], v[228:229], v[96:97] op_sel_hi:[1,0,1]
	s_nop 0
	v_pk_fma_f32 v[88:89], v[228:229], v[70:71], v[92:93] op_sel:[1,0,0]
	s_nop 0
	v_pk_fma_f32 v[88:89], v[230:231], v[74:75], v[88:89] op_sel_hi:[0,1,1]
	v_mov_b32_e32 v90, v231
	v_pk_fma_f32 v[88:89], v[90:91], v[68:69], v[88:89] op_sel_hi:[0,1,1]
	ds_read_b128 v[178:181], v25 offset:7168
	s_waitcnt lgkmcnt(8)
	v_pk_fma_f32 v[94:95], v[72:73], v[232:233], v[98:99] op_sel_hi:[1,0,1]
	s_nop 0
	v_pk_fma_f32 v[90:91], v[232:233], v[70:71], v[94:95] op_sel:[1,0,0]
	s_nop 0
	v_pk_fma_f32 v[90:91], v[234:235], v[74:75], v[90:91] op_sel_hi:[0,1,1]
	v_mov_b32_e32 v92, v235
	v_pk_fma_f32 v[90:91], v[92:93], v[68:69], v[90:91] op_sel_hi:[0,1,1]
	ds_read_b128 v[182:185], v25 offset:15376
	s_waitcnt lgkmcnt(8)
	v_pk_fma_f32 v[96:97], v[72:73], v[242:243], v[100:101] op_sel_hi:[1,0,1]
	s_nop 0
	v_pk_fma_f32 v[92:93], v[242:243], v[70:71], v[96:97] op_sel:[1,0,0]
	s_nop 0
	v_pk_fma_f32 v[92:93], v[244:245], v[74:75], v[92:93] op_sel_hi:[0,1,1]
	v_mov_b32_e32 v94, v245
	v_pk_fma_f32 v[92:93], v[94:95], v[68:69], v[92:93] op_sel_hi:[0,1,1]
	ds_read_b128 v[186:189], v25 offset:23584
	s_waitcnt lgkmcnt(8)
	v_pk_fma_f32 v[98:99], v[72:73], v[246:247], v[102:103] op_sel_hi:[1,0,1]
	s_nop 0
	v_pk_fma_f32 v[94:95], v[246:247], v[70:71], v[98:99] op_sel:[1,0,0]
	s_nop 0
	v_pk_fma_f32 v[94:95], v[248:249], v[74:75], v[94:95] op_sel_hi:[0,1,1]
	v_mov_b32_e32 v96, v249
	v_pk_fma_f32 v[94:95], v[96:97], v[68:69], v[94:95] op_sel_hi:[0,1,1]
	ds_read_b128 v[158:161], v25 offset:31792
	s_waitcnt lgkmcnt(8)
	v_pk_fma_f32 v[100:101], v[72:73], v[250:251], v[104:105] op_sel_hi:[1,0,1]
	s_nop 0
	v_pk_fma_f32 v[96:97], v[250:251], v[70:71], v[100:101] op_sel:[1,0,0]
	s_nop 0
	v_pk_fma_f32 v[96:97], v[252:253], v[74:75], v[96:97] op_sel_hi:[0,1,1]
	v_mov_b32_e32 v98, v253
	v_pk_fma_f32 v[96:97], v[98:99], v[68:69], v[96:97] op_sel_hi:[0,1,1]
	ds_read_b128 v[198:201], v25 offset:40000
	s_waitcnt lgkmcnt(8)
	v_pk_fma_f32 v[102:103], v[72:73], v[162:163], v[106:107] op_sel_hi:[1,0,1]
	s_nop 0
	v_pk_fma_f32 v[98:99], v[162:163], v[70:71], v[102:103] op_sel:[1,0,0]
	s_nop 0
	v_pk_fma_f32 v[98:99], v[164:165], v[74:75], v[98:99] op_sel_hi:[0,1,1]
	v_mov_b32_e32 v100, v165
	v_pk_fma_f32 v[98:99], v[100:101], v[68:69], v[98:99] op_sel_hi:[0,1,1]
	ds_read_b128 v[202:205], v25 offset:48208
	s_waitcnt lgkmcnt(8)
	v_pk_fma_f32 v[104:105], v[72:73], v[166:167], v[108:109] op_sel_hi:[1,0,1]
	s_nop 0
	v_pk_fma_f32 v[100:101], v[166:167], v[70:71], v[104:105] op_sel:[1,0,0]
	s_nop 0
	v_pk_fma_f32 v[100:101], v[168:169], v[74:75], v[100:101] op_sel_hi:[0,1,1]
	v_mov_b32_e32 v102, v169
	v_pk_fma_f32 v[100:101], v[102:103], v[68:69], v[100:101] op_sel_hi:[0,1,1]
	ds_read_b128 v[216:219], v25 offset:56416
	s_waitcnt lgkmcnt(8)
	v_pk_fma_f32 v[106:107], v[72:73], v[170:171], v[110:111] op_sel_hi:[1,0,1]
	s_nop 0
	v_pk_fma_f32 v[102:103], v[170:171], v[70:71], v[106:107] op_sel:[1,0,0]
	s_nop 0
	v_pk_fma_f32 v[102:103], v[172:173], v[74:75], v[102:103] op_sel_hi:[0,1,1]
	v_mov_b32_e32 v104, v173
	v_pk_fma_f32 v[102:103], v[104:105], v[68:69], v[102:103] op_sel_hi:[0,1,1]
	ds_read_b128 v[220:223], v25 offset:64624
	s_waitcnt lgkmcnt(8)
	v_pk_fma_f32 v[72:73], v[72:73], v[174:175], v[112:113] op_sel_hi:[1,0,1]
	s_nop 0
	v_pk_fma_f32 v[70:71], v[174:175], v[70:71], v[72:73] op_sel:[1,0,0]
	v_mov_b32_e32 v72, v177
	v_pk_fma_f32 v[70:71], v[176:177], v[74:75], v[70:71] op_sel_hi:[0,1,1]
	v_pk_fma_f32 v[104:105], v[72:73], v[68:69], v[70:71] op_sel_hi:[0,1,1]
	ds_read_b128 v[224:227], v238 offset:7296
	s_waitcnt lgkmcnt(8)
	v_pk_fma_f32 v[72:73], v[66:67], v[178:179], v[76:77] op_sel_hi:[1,0,1]
	s_nop 0
	v_pk_fma_f32 v[68:69], v[178:179], v[62:63], v[72:73] op_sel:[1,0,0]
	s_nop 0
	v_pk_fma_f32 v[68:69], v[180:181], v[64:65], v[68:69] op_sel_hi:[0,1,1]
	v_mov_b32_e32 v70, v181
	v_pk_fma_f32 v[68:69], v[70:71], v[60:61], v[68:69] op_sel_hi:[0,1,1]
	ds_read_b128 v[228:231], v238 offset:15504
	s_waitcnt lgkmcnt(8)
	v_pk_fma_f32 v[74:75], v[66:67], v[182:183], v[114:115] op_sel_hi:[1,0,1]
	s_nop 0
	v_pk_fma_f32 v[70:71], v[182:183], v[62:63], v[74:75] op_sel:[1,0,0]
	s_nop 0
	v_pk_fma_f32 v[70:71], v[184:185], v[64:65], v[70:71] op_sel_hi:[0,1,1]
	v_mov_b32_e32 v72, v185
	v_pk_fma_f32 v[70:71], v[72:73], v[60:61], v[70:71] op_sel_hi:[0,1,1]
	ds_read_b128 v[232:235], v238 offset:23712
	s_waitcnt lgkmcnt(8)
; #define LAS __attribute__((address_space(3)))
; __global__ void __launch_bounds__(NTHREADS, 2) hybrid_fwd(Args a) {
;     ...
; #pragma unroll
;                     for (int j = 0; j < 8; ++j) {
; #pragma unroll
;                         for (int e = 0; e < 16; ++e) { const f32x4 w = *(const LAS f32x4*)(rwT + e * 2052 + j * 256 + lane * 4);
;                             acc2[e] += y2[j][0] * (f32x2){w[0], w[0]}; acc2[e] += y2[j][1] * (f32x2){w[1], w[1]};
;                             acc2[e] += y2[j][2] * (f32x2){w[2], w[2]}; acc2[e] += y2[j][3] * (f32x2){w[3], w[3]}; }
	v_pk_fma_f32 v[76:77], v[66:67], v[186:187], v[78:79] op_sel_hi:[1,0,1]
	s_nop 0
	v_pk_fma_f32 v[72:73], v[186:187], v[62:63], v[76:77] op_sel:[1,0,0]
	s_nop 0
	v_pk_fma_f32 v[72:73], v[188:189], v[64:65], v[72:73] op_sel_hi:[0,1,1]
	v_mov_b32_e32 v74, v189
	v_pk_fma_f32 v[72:73], v[74:75], v[60:61], v[72:73] op_sel_hi:[0,1,1]
	ds_read_b128 v[242:245], v238 offset:31920
	s_waitcnt lgkmcnt(8)
	v_pk_fma_f32 v[78:79], v[66:67], v[158:159], v[80:81] op_sel_hi:[1,0,1]
	s_nop 0
	v_pk_fma_f32 v[74:75], v[158:159], v[62:63], v[78:79] op_sel:[1,0,0]
	ds_read_b128 v[246:249], v238 offset:40128
	v_pk_fma_f32 v[74:75], v[160:161], v[64:65], v[74:75] op_sel_hi:[0,1,1]
	v_mov_b32_e32 v76, v161
	v_pk_fma_f32 v[76:77], v[76:77], v[60:61], v[74:75] op_sel_hi:[0,1,1]
	s_waitcnt lgkmcnt(8)
	v_pk_fma_f32 v[74:75], v[66:67], v[198:199], v[82:83] op_sel_hi:[1,0,1]
	s_nop 0
	v_pk_fma_f32 v[74:75], v[198:199], v[62:63], v[74:75] op_sel:[1,0,0]
	v_mov_b32_e32 v78, v201
	v_pk_fma_f32 v[74:75], v[200:201], v[64:65], v[74:75] op_sel_hi:[0,1,1]
	v_pk_fma_f32 v[74:75], v[78:79], v[60:61], v[74:75] op_sel_hi:[0,1,1]
	ds_read_b128 v[250:253], v238 offset:48336
	s_waitcnt lgkmcnt(8)
	v_pk_fma_f32 v[82:83], v[66:67], v[202:203], v[84:85] op_sel_hi:[1,0,1]
	s_nop 0
	v_pk_fma_f32 v[78:79], v[202:203], v[62:63], v[82:83] op_sel:[1,0,0]
	s_nop 0
	v_pk_fma_f32 v[78:79], v[204:205], v[64:65], v[78:79] op_sel_hi:[0,1,1]
	v_mov_b32_e32 v80, v205
	v_pk_fma_f32 v[78:79], v[80:81], v[60:61], v[78:79] op_sel_hi:[0,1,1]
	ds_read_b128 v[162:165], v238 offset:56544
	s_waitcnt lgkmcnt(8)
	v_pk_fma_f32 v[84:85], v[66:67], v[216:217], v[86:87] op_sel_hi:[1,0,1]
	s_nop 0
	v_pk_fma_f32 v[80:81], v[216:217], v[62:63], v[84:85] op_sel:[1,0,0]
	s_nop 0
	v_pk_fma_f32 v[80:81], v[218:219], v[64:65], v[80:81] op_sel_hi:[0,1,1]
	v_mov_b32_e32 v82, v219
	v_pk_fma_f32 v[80:81], v[82:83], v[60:61], v[80:81] op_sel_hi:[0,1,1]
	ds_read_b128 v[166:169], v238 offset:64752
	s_waitcnt lgkmcnt(8)
	v_pk_fma_f32 v[86:87], v[66:67], v[220:221], v[88:89] op_sel_hi:[1,0,1]
	s_nop 0
	v_pk_fma_f32 v[82:83], v[220:221], v[62:63], v[86:87] op_sel:[1,0,0]
	s_nop 0
	v_pk_fma_f32 v[82:83], v[222:223], v[64:65], v[82:83] op_sel_hi:[0,1,1]
	v_mov_b32_e32 v84, v223
	v_pk_fma_f32 v[82:83], v[84:85], v[60:61], v[82:83] op_sel_hi:[0,1,1]
	s_waitcnt lgkmcnt(7)
	v_pk_fma_f32 v[88:89], v[66:67], v[224:225], v[90:91] op_sel_hi:[1,0,1]
	s_nop 0
	v_pk_fma_f32 v[84:85], v[224:225], v[62:63], v[88:89] op_sel:[1,0,0]
	s_nop 0
	v_pk_fma_f32 v[84:85], v[226:227], v[64:65], v[84:85] op_sel_hi:[0,1,1]
	v_mov_b32_e32 v86, v227
	v_pk_fma_f32 v[84:85], v[86:87], v[60:61], v[84:85] op_sel_hi:[0,1,1]
	s_waitcnt lgkmcnt(6)
	v_pk_fma_f32 v[90:91], v[66:67], v[228:229], v[92:93] op_sel_hi:[1,0,1]
	s_nop 0
	v_pk_fma_f32 v[86:87], v[228:229], v[62:63], v[90:91] op_sel:[1,0,0]
	s_nop 0
	v_pk_fma_f32 v[86:87], v[230:231], v[64:65], v[86:87] op_sel_hi:[0,1,1]
	v_mov_b32_e32 v88, v231
	v_pk_fma_f32 v[86:87], v[88:89], v[60:61], v[86:87] op_sel_hi:[0,1,1]
	s_waitcnt lgkmcnt(5)
	v_pk_fma_f32 v[92:93], v[66:67], v[232:233], v[94:95] op_sel_hi:[1,0,1]
	s_nop 0
	v_pk_fma_f32 v[88:89], v[232:233], v[62:63], v[92:93] op_sel:[1,0,0]
	s_nop 0
	v_pk_fma_f32 v[88:89], v[234:235], v[64:65], v[88:89] op_sel_hi:[0,1,1]
	v_mov_b32_e32 v90, v235
	v_pk_fma_f32 v[88:89], v[90:91], v[60:61], v[88:89] op_sel_hi:[0,1,1]
	s_waitcnt lgkmcnt(4)
	v_pk_fma_f32 v[94:95], v[66:67], v[242:243], v[96:97] op_sel_hi:[1,0,1]
	s_nop 0
	v_pk_fma_f32 v[90:91], v[242:243], v[62:63], v[94:95] op_sel:[1,0,0]
	s_nop 0
	v_pk_fma_f32 v[90:91], v[244:245], v[64:65], v[90:91] op_sel_hi:[0,1,1]
	v_mov_b32_e32 v92, v245
	v_pk_fma_f32 v[90:91], v[92:93], v[60:61], v[90:91] op_sel_hi:[0,1,1]
	s_waitcnt lgkmcnt(3)
	v_pk_fma_f32 v[96:97], v[66:67], v[246:247], v[98:99] op_sel_hi:[1,0,1]
	s_nop 0
	v_pk_fma_f32 v[92:93], v[246:247], v[62:63], v[96:97] op_sel:[1,0,0]
	s_nop 0
	v_pk_fma_f32 v[92:93], v[248:249], v[64:65], v[92:93] op_sel_hi:[0,1,1]
	v_mov_b32_e32 v94, v249
	v_pk_fma_f32 v[92:93], v[94:95], v[60:61], v[92:93] op_sel_hi:[0,1,1]
	s_waitcnt lgkmcnt(2)
	v_pk_fma_f32 v[98:99], v[66:67], v[250:251], v[100:101] op_sel_hi:[1,0,1]
	s_nop 0
	v_pk_fma_f32 v[94:95], v[250:251], v[62:63], v[98:99] op_sel:[1,0,0]
	s_nop 0
	v_pk_fma_f32 v[94:95], v[252:253], v[64:65], v[94:95] op_sel_hi:[0,1,1]
	v_mov_b32_e32 v96, v253
	v_pk_fma_f32 v[94:95], v[96:97], v[60:61], v[94:95] op_sel_hi:[0,1,1]
	s_waitcnt lgkmcnt(1)
	v_pk_fma_f32 v[100:101], v[66:67], v[162:163], v[102:103] op_sel_hi:[1,0,1]
	s_nop 0
	v_pk_fma_f32 v[96:97], v[162:163], v[62:63], v[100:101] op_sel:[1,0,0]
	s_nop 0
	v_pk_fma_f32 v[96:97], v[164:165], v[64:65], v[96:97] op_sel_hi:[0,1,1]
	v_mov_b32_e32 v98, v165
	v_pk_fma_f32 v[96:97], v[98:99], v[60:61], v[96:97] op_sel_hi:[0,1,1]
	s_waitcnt lgkmcnt(0)
; __global__ void __launch_bounds__(NTHREADS, 2) hybrid_fwd(Args a) {
;     ...
;                     float acca[16], accb[16];
; #pragma unroll
;                     for (int e = 0; e < 16; ++e) { acca[e] = acc2[e][0]; accb[e] = acc2[e][1]; }
;                     P7_PICK(2 * qp, acca);
	v_pk_fma_f32 v[66:67], v[66:67], v[166:167], v[104:105] op_sel_hi:[1,0,1]
	s_nop 0
	v_pk_fma_f32 v[62:63], v[166:167], v[62:63], v[66:67] op_sel:[1,0,0]
	s_nop 0
	v_pk_fma_f32 v[62:63], v[168:169], v[64:65], v[62:63] op_sel_hi:[0,1,1]
	v_mov_b32_e32 v64, v169
	v_pk_fma_f32 v[60:61], v[64:65], v[60:61], v[62:63] op_sel_hi:[0,1,1]
	s_nop 1
	v_permlane32_swap_b32_e32 v60, v61
	v_permlane32_swap_b32_e32 v68, v69
	v_permlane32_swap_b32_e32 v70, v71
	v_permlane32_swap_b32_e32 v72, v73
	v_permlane32_swap_b32_e32 v74, v75
	v_permlane32_swap_b32_e32 v76, v77
	v_permlane32_swap_b32_e32 v78, v79
	v_permlane32_swap_b32_e32 v80, v81
	v_permlane32_swap_b32_e32 v82, v83
	v_permlane32_swap_b32_e32 v84, v85
	v_permlane32_swap_b32_e32 v86, v87
	v_permlane32_swap_b32_e32 v88, v89
	v_permlane32_swap_b32_e32 v90, v91
	v_permlane32_swap_b32_e32 v92, v93
	v_permlane32_swap_b32_e32 v94, v95
	v_permlane32_swap_b32_e32 v96, v97
	v_add_f32_e32 v60, v60, v61
	v_add_f32_e32 v68, v68, v69
	v_add_f32_e32 v70, v70, v71
	v_add_f32_e32 v72, v72, v73
	v_add_f32_e32 v74, v74, v75
	v_add_f32_e32 v76, v76, v77
	v_add_f32_e32 v78, v78, v79
	v_add_f32_e32 v80, v80, v81
	v_add_f32_e32 v82, v82, v83
	v_add_f32_e32 v84, v84, v85
	v_add_f32_e32 v86, v86, v87
	v_add_f32_e32 v88, v88, v89
	v_add_f32_e32 v90, v90, v91
	v_add_f32_e32 v92, v92, v93
	v_add_f32_e32 v94, v94, v95
	v_add_f32_e32 v96, v96, v97
	s_nop 1
	v_add_f32_dpp v62, v68, v68 quad_perm:[1,0,3,2] row_mask:0xf bank_mask:0xf bound_ctrl:1
	s_nop 0
	v_add_f32_dpp v60, v60, v60 quad_perm:[1,0,3,2] row_mask:0xf bank_mask:0xf bound_ctrl:1
	v_add_f32_dpp v68, v94, v94 quad_perm:[1,0,3,2] row_mask:0xf bank_mask:0xf bound_ctrl:1
	v_add_f32_dpp v62, v62, v62 quad_perm:[2,3,0,1] row_mask:0xf bank_mask:0xf bound_ctrl:1
	v_add_f32_dpp v60, v60, v60 quad_perm:[2,3,0,1] row_mask:0xf bank_mask:0xf bound_ctrl:1
	v_add_f32_dpp v68, v68, v68 quad_perm:[2,3,0,1] row_mask:0xf bank_mask:0xf bound_ctrl:1
	v_add_f32_dpp v62, v62, v62 row_ror:4 row_mask:0xf bank_mask:0xf bound_ctrl:1
	v_add_f32_dpp v60, v60, v60 row_ror:4 row_mask:0xf bank_mask:0xf bound_ctrl:1
	v_add_f32_dpp v68, v68, v68 row_ror:4 row_mask:0xf bank_mask:0xf bound_ctrl:1
	v_add_f32_dpp v62, v62, v62 row_ror:8 row_mask:0xf bank_mask:0xf bound_ctrl:1
	v_mov_b32_e32 v63, v62
	s_nop 1
	v_permlane16_swap_b32_e32 v62, v63
	v_add_f32_e32 v62, v62, v63
	v_mov_b32_e32 v63, v62
	s_nop 1
	s_nop 0
	v_mov_b32_e32 v62, v62
	s_nop 0
	v_add_f32_dpp v63, v70, v70 quad_perm:[1,0,3,2] row_mask:0xf bank_mask:0xf bound_ctrl:1
	v_mul_f32_e32 v62, 0xbfb8aa3b, v62
	v_exp_f32_e32 v62, v62
	v_add_f32_dpp v63, v63, v63 quad_perm:[2,3,0,1] row_mask:0xf bank_mask:0xf bound_ctrl:1
	v_add_f32_dpp v60, v60, v60 row_ror:8 row_mask:0xf bank_mask:0xf bound_ctrl:1
	v_add_f32_dpp v68, v68, v68 row_ror:8 row_mask:0xf bank_mask:0xf bound_ctrl:1
	v_add_f32_dpp v63, v63, v63 row_ror:4 row_mask:0xf bank_mask:0xf bound_ctrl:1
	v_add_f32_e32 v62, 1.0, v62
	v_rcp_f32_e32 v62, v62
	v_add_f32_dpp v63, v63, v63 row_ror:8 row_mask:0xf bank_mask:0xf bound_ctrl:1
	v_mov_b32_e32 v64, v63
	s_nop 1
	v_permlane16_swap_b32_e32 v63, v64
	v_add_f32_e32 v63, v63, v64
	v_mov_b32_e32 v64, v63
	s_nop 1
	s_nop 0
	v_mov_b32_e32 v63, v63
	s_nop 0
	v_add_f32_dpp v64, v72, v72 quad_perm:[1,0,3,2] row_mask:0xf bank_mask:0xf bound_ctrl:1
	v_mul_f32_e32 v63, 0xbfb8aa3b, v63
	v_exp_f32_e32 v63, v63
	v_add_f32_dpp v64, v64, v64 quad_perm:[2,3,0,1] row_mask:0xf bank_mask:0xf bound_ctrl:1
	v_add_f32_dpp v72, v96, v96 quad_perm:[1,0,3,2] row_mask:0xf bank_mask:0xf bound_ctrl:1
	v_mov_b32_e32 v70, v68
	v_add_f32_dpp v64, v64, v64 row_ror:4 row_mask:0xf bank_mask:0xf bound_ctrl:1
	v_add_f32_e32 v63, 1.0, v63
	v_rcp_f32_e32 v63, v63
	v_add_f32_dpp v64, v64, v64 row_ror:8 row_mask:0xf bank_mask:0xf bound_ctrl:1
	v_mov_b32_e32 v65, v64
	s_nop 1
	v_permlane16_swap_b32_e32 v64, v65
	v_add_f32_e32 v64, v64, v65
	v_mov_b32_e32 v65, v64
	s_nop 1
	s_nop 0
	v_mov_b32_e32 v64, v64
	s_nop 0
	v_add_f32_dpp v65, v76, v76 quad_perm:[1,0,3,2] row_mask:0xf bank_mask:0xf bound_ctrl:1
	v_mul_f32_e32 v64, 0xbfb8aa3b, v64
	v_exp_f32_e32 v64, v64
	v_add_f32_dpp v65, v65, v65 quad_perm:[2,3,0,1] row_mask:0xf bank_mask:0xf bound_ctrl:1
	v_mov_b32_e32 v76, v60
	s_nop 1
	v_permlane16_swap_b32_e32 v60, v76
	v_add_f32_dpp v65, v65, v65 row_ror:4 row_mask:0xf bank_mask:0xf bound_ctrl:1
	v_add_f32_e32 v64, 1.0, v64
	v_rcp_f32_e32 v102, v64
	v_add_f32_dpp v65, v65, v65 row_ror:8 row_mask:0xf bank_mask:0xf bound_ctrl:1
	v_mov_b32_e32 v66, v65
	s_nop 1
	v_permlane16_swap_b32_e32 v65, v66
	v_add_f32_e32 v65, v65, v66
	v_mov_b32_e32 v66, v65
	s_nop 1
	s_nop 0
	v_mov_b32_e32 v65, v65
	s_nop 0
	v_add_f32_dpp v66, v74, v74 quad_perm:[1,0,3,2] row_mask:0xf bank_mask:0xf bound_ctrl:1
	v_mul_f32_e32 v65, 0xbfb8aa3b, v65
	v_exp_f32_e32 v65, v65
	v_add_f32_dpp v66, v66, v66 quad_perm:[2,3,0,1] row_mask:0xf bank_mask:0xf bound_ctrl:1
	v_add_f32_e32 v111, v14, v102
	v_add_f32_e32 v76, v60, v76
	v_add_f32_dpp v66, v66, v66 row_ror:4 row_mask:0xf bank_mask:0xf bound_ctrl:1
	v_add_f32_e32 v64, 1.0, v65
	v_rcp_f32_e32 v104, v64
	v_add_f32_dpp v66, v66, v66 row_ror:8 row_mask:0xf bank_mask:0xf bound_ctrl:1
	v_mov_b32_e32 v67, v66
	s_nop 1
	v_permlane16_swap_b32_e32 v66, v67
	v_add_f32_e32 v101, v66, v67
	s_nop 0
	v_add_f32_dpp v66, v78, v78 quad_perm:[1,0,3,2] row_mask:0xf bank_mask:0xf bound_ctrl:1
	v_pk_add_f32 v[64:65], v[12:13], v[62:63]
	v_add_f32_e32 v112, v15, v104
	v_add_f32_dpp v66, v66, v66 quad_perm:[2,3,0,1] row_mask:0xf bank_mask:0xf bound_ctrl:1
	v_cmp_gt_f32_e32 vcc, v65, v64
	v_add_f32_dpp v72, v72, v72 quad_perm:[2,3,0,1] row_mask:0xf bank_mask:0xf bound_ctrl:1
	v_add_f32_dpp v66, v66, v66 row_ror:4 row_mask:0xf bank_mask:0xf bound_ctrl:1
	v_cndmask_b32_e32 v60, v64, v65, vcc
	v_cmp_gt_f32_e64 s[6:7], v111, v60
	v_add_f32_dpp v66, v66, v66 row_ror:8 row_mask:0xf bank_mask:0xf bound_ctrl:1
	v_mov_b32_e32 v67, v66
	s_nop 1
	v_permlane16_swap_b32_e32 v66, v67
	v_add_f32_e32 v105, v66, v67
	s_nop 0
	v_add_f32_dpp v66, v80, v80 quad_perm:[1,0,3,2] row_mask:0xf bank_mask:0xf bound_ctrl:1
	v_cndmask_b32_e64 v80, 0, 1, vcc
	v_cndmask_b32_e64 v60, v60, v111, s[6:7]
	v_add_f32_dpp v66, v66, v66 quad_perm:[2,3,0,1] row_mask:0xf bank_mask:0xf bound_ctrl:1
	v_cndmask_b32_e64 v80, v80, 2, s[6:7]
	v_cmp_ngt_f32_e64 s[8:9], v112, v60
	v_add_f32_dpp v66, v66, v66 row_ror:4 row_mask:0xf bank_mask:0xf bound_ctrl:1
	v_add_f32_dpp v72, v72, v72 row_ror:4 row_mask:0xf bank_mask:0xf bound_ctrl:1
	v_permlane16_swap_b32_e32 v68, v70
	v_add_f32_dpp v66, v66, v66 row_ror:8 row_mask:0xf bank_mask:0xf bound_ctrl:1
	v_mov_b32_e32 v67, v66
	s_nop 1
	v_permlane16_swap_b32_e32 v66, v67
	v_add_f32_e32 v107, v66, v67
	s_nop 0
	v_add_f32_dpp v66, v82, v82 quad_perm:[1,0,3,2] row_mask:0xf bank_mask:0xf bound_ctrl:1
	v_add_f32_dpp v72, v72, v72 row_ror:8 row_mask:0xf bank_mask:0xf bound_ctrl:1
	v_mov_b32_e32 v74, v72
	v_add_f32_dpp v66, v66, v66 quad_perm:[2,3,0,1] row_mask:0xf bank_mask:0xf bound_ctrl:1
	s_nop 0
	v_permlane16_swap_b32_e32 v72, v74
	v_add_f32_dpp v66, v66, v66 row_ror:4 row_mask:0xf bank_mask:0xf bound_ctrl:1
	v_add_f32_e32 v68, v68, v70
	v_add_f32_e32 v72, v72, v74
	v_add_f32_dpp v66, v66, v66 row_ror:8 row_mask:0xf bank_mask:0xf bound_ctrl:1
	v_mov_b32_e32 v67, v66
	s_nop 1
	v_permlane16_swap_b32_e32 v66, v67
	v_add_f32_e32 v109, v66, v67
	s_nop 0
	v_add_f32_dpp v66, v84, v84 quad_perm:[1,0,3,2] row_mask:0xf bank_mask:0xf bound_ctrl:1
	v_cndmask_b32_e64 v94, v112, v60, s[8:9]
	v_mov_b32_e32 v103, v101
	v_add_f32_dpp v66, v66, v66 quad_perm:[2,3,0,1] row_mask:0xf bank_mask:0xf bound_ctrl:1
	v_mov_b32_e32 v106, v105
	v_mov_b32_e32 v108, v107
	v_add_f32_dpp v66, v66, v66 row_ror:4 row_mask:0xf bank_mask:0xf bound_ctrl:1
	v_mov_b32_e32 v110, v109
	v_mov_b32_e32 v70, v68
	v_add_f32_dpp v66, v66, v66 row_ror:8 row_mask:0xf bank_mask:0xf bound_ctrl:1
	v_mov_b32_e32 v67, v66
	s_nop 1
	v_permlane16_swap_b32_e32 v66, v67
	v_add_f32_e32 v82, v66, v67
	s_nop 0
	v_add_f32_dpp v66, v86, v86 quad_perm:[1,0,3,2] row_mask:0xf bank_mask:0xf bound_ctrl:1
	v_mov_b32_e32 v84, v82
	v_mov_b32_e32 v74, v72
	v_add_f32_dpp v66, v66, v66 quad_perm:[2,3,0,1] row_mask:0xf bank_mask:0xf bound_ctrl:1
	v_mov_b32_e32 v78, v76
	s_nop 0
	v_add_f32_dpp v66, v66, v66 row_ror:4 row_mask:0xf bank_mask:0xf bound_ctrl:1
	s_nop 0
	s_nop 0
	v_add_f32_dpp v66, v66, v66 row_ror:8 row_mask:0xf bank_mask:0xf bound_ctrl:1
	v_mov_b32_e32 v67, v66
	s_nop 1
	v_permlane16_swap_b32_e32 v66, v67
	v_add_f32_e32 v86, v66, v67
	s_nop 0
	v_add_f32_dpp v66, v88, v88 quad_perm:[1,0,3,2] row_mask:0xf bank_mask:0xf bound_ctrl:1
	v_mov_b32_e32 v98, v86
	s_nop 0
	v_add_f32_dpp v66, v66, v66 quad_perm:[2,3,0,1] row_mask:0xf bank_mask:0xf bound_ctrl:1
	s_nop 0
	s_nop 0
	v_add_f32_dpp v66, v66, v66 row_ror:4 row_mask:0xf bank_mask:0xf bound_ctrl:1
	s_nop 0
	s_nop 0
	v_add_f32_dpp v66, v66, v66 row_ror:8 row_mask:0xf bank_mask:0xf bound_ctrl:1
	v_mov_b32_e32 v67, v66
	s_nop 1
	v_permlane16_swap_b32_e32 v66, v67
	v_add_f32_e32 v88, v66, v67
	s_nop 0
	v_add_f32_dpp v66, v90, v90 quad_perm:[1,0,3,2] row_mask:0xf bank_mask:0xf bound_ctrl:1
	v_mov_b32_e32 v99, v88
	s_nop 0
	v_add_f32_dpp v66, v66, v66 quad_perm:[2,3,0,1] row_mask:0xf bank_mask:0xf bound_ctrl:1
	s_nop 0
	s_nop 0
	v_add_f32_dpp v66, v66, v66 row_ror:4 row_mask:0xf bank_mask:0xf bound_ctrl:1
	s_nop 0
	s_nop 0
	v_add_f32_dpp v66, v66, v66 row_ror:8 row_mask:0xf bank_mask:0xf bound_ctrl:1
	v_mov_b32_e32 v67, v66
	s_nop 1
	v_permlane16_swap_b32_e32 v66, v67
	v_add_f32_e32 v90, v66, v67
	s_nop 0
	v_add_f32_dpp v66, v92, v92 quad_perm:[1,0,3,2] row_mask:0xf bank_mask:0xf bound_ctrl:1
	v_cndmask_b32_e64 v92, 3, v80, s[8:9]
	v_mov_b32_e32 v80, 0xff800000
	v_cmp_eq_u32_e64 s[10:11], 0, v92
	v_cmp_nlg_f32_e64 s[12:13], v64, v80
	s_or_b64 s[10:11], s[10:11], s[12:13]
	v_cndmask_b32_e64 v64, v64, v80, s[10:11]
	v_cmp_ne_u32_e64 s[12:13], 1, v92
	v_cmp_gt_f32_e64 s[14:15], v65, v64
	s_and_b64 s[12:13], s[12:13], s[14:15]
	v_cndmask_b32_e64 v64, v64, v65, s[12:13]
	v_add_f32_dpp v66, v66, v66 quad_perm:[2,3,0,1] row_mask:0xf bank_mask:0xf bound_ctrl:1
	v_cmp_ne_u32_e64 s[14:15], 2, v92
	v_cmp_gt_f32_e64 s[16:17], v111, v64
	v_add_f32_dpp v66, v66, v66 row_ror:4 row_mask:0xf bank_mask:0xf bound_ctrl:1
	s_and_b64 s[14:15], s[14:15], s[16:17]
	v_cndmask_b32_e64 v64, v64, v111, s[14:15]
	v_add_f32_dpp v66, v66, v66 row_ror:8 row_mask:0xf bank_mask:0xf bound_ctrl:1
	v_mov_b32_e32 v67, v66
	v_cmp_gt_f32_e64 s[16:17], v112, v64
	s_nop 0
	v_permlane16_swap_b32_e32 v66, v67
	s_and_b64 s[16:17], s[8:9], s[16:17]
	v_add_f32_e32 v66, v66, v67
	v_cndmask_b32_e64 v64, v64, v112, s[16:17]
	v_mov_b32_e32 v100, v90
	v_mov_b32_e32 v67, v66
	v_add_f32_e32 v94, v94, v64
	s_nop 0
	s_nop 0
	s_nop 0
	s_nop 0
	v_mov_b32_e32 v60, 1
	v_cmp_lg_f32_e64 s[18:19], v94, v80
	v_mov_b32_e32 v65, 0
	v_mov_b32_e32 v64, 0
	s_and_saveexec_b64 s[46:47], s[18:19]
	s_cbranch_execz .LBB0_891
	v_cndmask_b32_e64 v35, 0, 1, s[12:13]
	v_cndmask_b32_e64 v35, v35, 2, s[14:15]
	v_cndmask_b32_e64 v60, v35, 3, s[16:17]
	v_cndmask_b32_e64 v35, v62, 0, s[10:11]
	v_cndmask_b32_e64 v35, v35, v63, s[12:13]
	v_cndmask_b32_e32 v62, v62, v63, vcc
	v_cndmask_b32_e64 v35, v35, v102, s[14:15]
	v_cndmask_b32_e64 v62, v62, v102, s[6:7]
	v_cndmask_b32_e64 v35, v35, v104, s[16:17]
	v_cndmask_b32_e64 v65, v104, v62, s[8:9]
	v_mov_b32_e32 v64, v92
	v_mov_b32_e32 v80, v94

.LBB0_899:
	s_or_b64 exec, exec, s[6:7]
	v_mbcnt_lo_u32_b32 v242, -1, 0
	v_mbcnt_hi_u32_b32 v242, -1, v242
	v_lshlrev_b32_e32 v242, 4, v242
	v_mov_b32_e32 v243, 0
	v_lshl_add_u64 v[244:245], s[34:35], 0, v[242:243]
	global_load_dwordx4 v[158:161], v[244:245], off
	global_load_dwordx4 v[162:165], v[244:245], off offset:1024
	global_load_dwordx4 v[166:169], v[244:245], off offset:2048
	global_load_dwordx4 v[170:173], v[244:245], off offset:3072
	v_add_co_u32_e32 v244, vcc, 0x1000, v244
	s_nop 1
	v_addc_co_u32_e32 v245, vcc, 0, v245, vcc
	global_load_dwordx4 v[174:177], v[244:245], off
	global_load_dwordx4 v[178:181], v[244:245], off offset:1024
	global_load_dwordx4 v[182:185], v[244:245], off offset:2048
	global_load_dwordx4 v[186:189], v[244:245], off offset:3072
	v_lshl_add_u64 v[244:245], s[36:37], 0, v[242:243]
	global_load_dwordx4 v[198:201], v[244:245], off
	global_load_dwordx4 v[202:205], v[244:245], off offset:1024
	global_load_dwordx4 v[216:219], v[244:245], off offset:2048
	global_load_dwordx4 v[220:223], v[244:245], off offset:3072
	v_add_co_u32_e32 v244, vcc, 0x1000, v244
	s_nop 1
	v_addc_co_u32_e32 v245, vcc, 0, v245, vcc
	global_load_dwordx4 v[224:227], v[244:245], off
	global_load_dwordx4 v[228:231], v[244:245], off offset:1024
	global_load_dwordx4 v[232:235], v[244:245], off offset:2048
	global_load_dwordx4 v[246:249], v[244:245], off offset:3072
	s_waitcnt vmcnt(0)
	v_lshlrev_b32_e32 v80, 16, v58
	v_and_b32_e32 v81, 0xffff0000, v58
	v_lshlrev_b32_e32 v78, 16, v59
	v_and_b32_e32 v79, 0xffff0000, v59
	v_add_f32_e32 v35, v80, v81
	v_add_f32_e32 v58, v78, v79
	v_lshlrev_b32_e32 v62, 16, v56
	v_and_b32_e32 v63, 0xffff0000, v56
	v_lshlrev_b32_e32 v60, 16, v57
	v_and_b32_e32 v61, 0xffff0000, v57
	v_add_f32_e32 v35, v35, v58
	v_add_f32_e32 v56, v62, v63
	v_add_f32_e32 v57, v60, v61
	v_lshlrev_b32_e32 v68, 16, v54
	v_and_b32_e32 v69, 0xffff0000, v54
	v_lshlrev_b32_e32 v70, 16, v55
	v_and_b32_e32 v71, 0xffff0000, v55
	v_add_f32_e32 v35, 0, v35
	v_add_f32_e32 v56, v56, v57
	v_add_f32_e32 v54, v68, v69
	v_add_f32_e32 v55, v70, v71
	v_lshlrev_b32_e32 v72, 16, v52
	v_and_b32_e32 v73, 0xffff0000, v52
	v_lshlrev_b32_e32 v74, 16, v53
	v_and_b32_e32 v75, 0xffff0000, v53
	v_add_f32_e32 v35, v35, v56
	v_add_f32_e32 v54, v54, v55
	v_add_f32_e32 v52, v72, v73
	v_add_f32_e32 v53, v74, v75
	v_lshlrev_b32_e32 v64, 16, v50
	v_and_b32_e32 v65, 0xffff0000, v50
	v_lshlrev_b32_e32 v66, 16, v51
	v_and_b32_e32 v67, 0xffff0000, v51
	v_add_f32_e32 v35, v35, v54
	v_add_f32_e32 v52, v52, v53
	v_add_f32_e32 v50, v64, v65
	v_add_f32_e32 v51, v66, v67
	v_lshlrev_b32_e32 v56, 16, v48
	v_and_b32_e32 v57, 0xffff0000, v48
	v_lshlrev_b32_e32 v58, 16, v49
	v_and_b32_e32 v59, 0xffff0000, v49
	v_add_f32_e32 v35, v35, v52
	v_add_f32_e32 v50, v50, v51
	v_add_f32_e32 v48, v56, v57
	v_add_f32_e32 v49, v58, v59
	v_lshlrev_b32_e32 v52, 16, v46
	v_and_b32_e32 v53, 0xffff0000, v46
	v_lshlrev_b32_e32 v54, 16, v47
	v_and_b32_e32 v55, 0xffff0000, v47
	v_add_f32_e32 v35, v35, v50
	v_add_f32_e32 v48, v48, v49
	v_add_f32_e32 v46, v52, v53
	v_add_f32_e32 v47, v54, v55
	v_add_f32_e32 v35, v35, v48
	v_add_f32_e32 v46, v46, v47
	v_add_f32_e32 v35, v35, v46
	v_lshlrev_b32_e32 v46, 16, v44
	v_and_b32_e32 v47, 0xffff0000, v44
	v_lshlrev_b32_e32 v44, 16, v45
	v_and_b32_e32 v45, 0xffff0000, v45
	v_add_f32_e32 v48, v46, v47
	v_add_f32_e32 v49, v44, v45
	v_add_f32_e32 v48, v48, v49
	v_add_f32_e32 v35, v35, v48
	s_mov_b64 s[6:7], s[34:35]
	s_mov_b64 s[8:9], s[36:37]
	v_add_f32_dpp v35, v35, v35 quad_perm:[1,0,3,2] row_mask:0xf bank_mask:0xf bound_ctrl:1
	v_lshl_add_u64 v[92:93], s[6:7], 0, v[192:193]
	s_lshl_b64 s[6:7], s[38:39], 11
	v_add_f32_dpp v35, v35, v35 quad_perm:[2,3,0,1] row_mask:0xf bank_mask:0xf bound_ctrl:1
	v_lshl_add_u64 v[94:95], s[8:9], 0, v[192:193]
	v_add_co_u32_e32 v98, vcc, s33, v92
	v_add_f32_dpp v35, v35, v35 row_ror:4 row_mask:0xf bank_mask:0xf bound_ctrl:1
	s_nop 0
	v_addc_co_u32_e32 v99, vcc, 0, v93, vcc
	v_add_f32_dpp v35, v35, v35 row_ror:8 row_mask:0xf bank_mask:0xf bound_ctrl:1
	v_mov_b32_e32 v48, v35
	s_nop 1
	v_permlane16_swap_b32_e32 v35, v48
	v_add_f32_e32 v35, v35, v48
	v_mov_b32_e32 v48, v35
	s_nop 1
	v_permlane32_swap_b32_e32 v35, v48
	v_add_f32_e32 v35, v35, v48
	v_fmac_f32_e32 v79, 0xba000000, v35
	v_fmac_f32_e32 v81, 0xba000000, v35
	v_fmac_f32_e32 v78, 0xba000000, v35
	v_fmac_f32_e32 v80, 0xba000000, v35
	v_mul_f32_e32 v48, v81, v81
	v_mul_f32_e32 v49, v79, v79
	v_fmac_f32_e32 v48, v80, v80
	v_fmac_f32_e32 v49, v78, v78
	v_fmac_f32_e32 v61, 0xba000000, v35
	v_fmac_f32_e32 v63, 0xba000000, v35
	v_add_f32_e32 v48, v48, v49
	v_fmac_f32_e32 v60, 0xba000000, v35
	v_fmac_f32_e32 v62, 0xba000000, v35
	v_mul_f32_e32 v49, v63, v63
	v_mul_f32_e32 v50, v61, v61
	v_fmac_f32_e32 v49, v62, v62
	v_fmac_f32_e32 v50, v60, v60
	v_add_f32_e32 v49, v49, v50
	v_add_f32_e32 v76, v48, v49
	s_nop 0
	v_fmac_f32_e32 v71, 0xba000000, v35
	v_fmac_f32_e32 v69, 0xba000000, v35
	v_fmac_f32_e32 v70, 0xba000000, v35
	v_fmac_f32_e32 v68, 0xba000000, v35
	v_mul_f32_e32 v77, v69, v69
	v_mul_f32_e32 v82, v71, v71
	v_fmac_f32_e32 v77, v68, v68
	v_fmac_f32_e32 v82, v70, v70
	v_add_f32_e32 v77, v77, v82
	v_fmac_f32_e32 v75, 0xba000000, v35
	v_fmac_f32_e32 v73, 0xba000000, v35
	v_add_f32_e32 v76, v76, v77
	v_fmac_f32_e32 v74, 0xba000000, v35
	v_fmac_f32_e32 v72, 0xba000000, v35
	v_mul_f32_e32 v77, v73, v73
	v_mul_f32_e32 v82, v75, v75
	v_fmac_f32_e32 v77, v72, v72
	v_fmac_f32_e32 v82, v74, v74
	v_add_f32_e32 v77, v77, v82
	v_fmac_f32_e32 v67, 0xba000000, v35
	v_fmac_f32_e32 v65, 0xba000000, v35
	v_add_f32_e32 v76, v76, v77
	v_fmac_f32_e32 v66, 0xba000000, v35
	v_fmac_f32_e32 v64, 0xba000000, v35
	v_mul_f32_e32 v77, v65, v65
	v_mul_f32_e32 v82, v67, v67
	v_fmac_f32_e32 v77, v64, v64
	v_fmac_f32_e32 v82, v66, v66
	v_add_f32_e32 v77, v77, v82
	v_fmac_f32_e32 v59, 0xba000000, v35
	v_fmac_f32_e32 v57, 0xba000000, v35
	v_add_f32_e32 v76, v76, v77
	v_fmac_f32_e32 v58, 0xba000000, v35
	v_fmac_f32_e32 v56, 0xba000000, v35
	v_mul_f32_e32 v77, v57, v57
	v_mul_f32_e32 v82, v59, v59
	v_fmac_f32_e32 v77, v56, v56
	v_fmac_f32_e32 v82, v58, v58
	v_add_f32_e32 v77, v77, v82
	v_fmac_f32_e32 v55, 0xba000000, v35
	v_fmac_f32_e32 v53, 0xba000000, v35
	v_add_f32_e32 v76, v76, v77
	v_fmac_f32_e32 v54, 0xba000000, v35
	v_fmac_f32_e32 v52, 0xba000000, v35
	v_mul_f32_e32 v77, v53, v53
	v_mul_f32_e32 v82, v55, v55
	v_fmac_f32_e32 v77, v52, v52
	v_fmac_f32_e32 v82, v54, v54
	v_add_f32_e32 v77, v77, v82
	v_fmac_f32_e32 v45, 0xba000000, v35
	v_fmac_f32_e32 v47, 0xba000000, v35
	v_add_f32_e32 v76, v76, v77
	v_fmac_f32_e32 v44, 0xba000000, v35
	v_fmac_f32_e32 v46, 0xba000000, v35
	v_mul_f32_e32 v35, v47, v47
	v_mul_f32_e32 v77, v45, v45
	v_fmac_f32_e32 v35, v46, v46
	v_fmac_f32_e32 v77, v44, v44
	v_add_f32_e32 v35, v35, v77
	v_add_f32_e32 v35, v76, v35
	v_lshl_add_u64 v[82:83], v[30:31], 0, s[6:7]
	v_add_co_u32_e32 v100, vcc, s33, v94
	v_add_f32_dpp v35, v35, v35 quad_perm:[1,0,3,2] row_mask:0xf bank_mask:0xf bound_ctrl:1
	s_nop 0
	v_addc_co_u32_e32 v101, vcc, 0, v95, vcc
	v_add_f32_dpp v35, v35, v35 quad_perm:[2,3,0,1] row_mask:0xf bank_mask:0xf bound_ctrl:1
	s_nop 1
	v_add_f32_dpp v35, v35, v35 row_ror:4 row_mask:0xf bank_mask:0xf bound_ctrl:1
	s_nop 1
	v_add_f32_dpp v35, v35, v35 row_ror:8 row_mask:0xf bank_mask:0xf bound_ctrl:1
	v_mov_b32_e32 v76, v35
	s_nop 1
	v_permlane16_swap_b32_e32 v35, v76
	v_add_f32_e32 v35, v35, v76
	v_mov_b32_e32 v76, v35
	s_nop 1
	v_permlane32_swap_b32_e32 v35, v76
	v_add_f32_e32 v35, v35, v76
	v_fmamk_f32 v35, v35, 0x3a000000, v207
	v_rsq_f32_e32 v96, v35
	v_lshl_add_u64 v[76:77], v[28:29], 0, s[44:45]
	v_pk_mul_f32 v[80:81], v[96:97], v[80:81] op_sel_hi:[0,1]
	s_waitcnt vmcnt(0) lgkmcnt(0)
	v_pk_fma_f32 v[48:49], v[158:159], v[80:81], v[198:199]
	v_mov_b32_e32 v81, 0
	v_med3_f32 v35, v48, s69, v208
	v_med3_f32 v80, v49, s69, v208
	v_cvt_pk_fp8_f32 v81, v35, v80
	v_pk_mul_f32 v[78:79], v[96:97], v[78:79] op_sel_hi:[0,1]
	v_pk_fma_f32 v[50:51], v[160:161], v[78:79], v[200:201]
	v_pk_mul_f32 v[62:63], v[96:97], v[62:63] op_sel_hi:[0,1]
	v_med3_f32 v35, v50, s69, v208
	v_med3_f32 v78, v51, s69, v208
	v_cvt_pk_fp8_f32 v81, v35, v78 op_sel:[0,0,1]
	v_cvt_pk_bf16_f32 v78, v48, v49
	v_cvt_pk_bf16_f32 v79, v50, v51
	global_store_dwordx2 v[76:77], v[78:79], off nt
	global_store_dword v[82:83], v81, off nt
	s_nop 0
	s_nop 0
	v_pk_mul_f32 v[88:89], v[96:97], v[60:61] op_sel_hi:[0,1]
	v_pk_mul_f32 v[68:69], v[96:97], v[68:69] op_sel_hi:[0,1]
	v_pk_mul_f32 v[72:73], v[96:97], v[72:73] op_sel_hi:[0,1]
	v_pk_mul_f32 v[74:75], v[96:97], v[74:75] op_sel_hi:[0,1]
	v_pk_mul_f32 v[64:65], v[96:97], v[64:65] op_sel_hi:[0,1]
	v_pk_mul_f32 v[66:67], v[96:97], v[66:67] op_sel_hi:[0,1]
	v_pk_mul_f32 v[56:57], v[96:97], v[56:57] op_sel_hi:[0,1]
	v_pk_mul_f32 v[58:59], v[96:97], v[58:59] op_sel_hi:[0,1]
	v_pk_mul_f32 v[52:53], v[96:97], v[52:53] op_sel_hi:[0,1]
	v_pk_mul_f32 v[54:55], v[96:97], v[54:55] op_sel_hi:[0,1]
	v_pk_mul_f32 v[46:47], v[96:97], v[46:47] op_sel_hi:[0,1]
	v_pk_mul_f32 v[44:45], v[96:97], v[44:45] op_sel_hi:[0,1]
	s_nop 0
	v_pk_fma_f32 v[60:61], v[162:163], v[62:63], v[202:203]
	s_nop 0
	v_med3_f32 v35, v60, s69, v208
	v_med3_f32 v62, v61, s69, v208
	v_mov_b32_e32 v84, 0
	v_cvt_pk_fp8_f32 v84, v35, v62
	v_pk_fma_f32 v[62:63], v[164:165], v[88:89], v[204:205]
	v_pk_mul_f32 v[88:89], v[96:97], v[70:71] op_sel_hi:[0,1]
	v_med3_f32 v35, v62, s69, v208
	v_med3_f32 v78, v63, s69, v208
	v_cvt_pk_fp8_f32 v84, v35, v78 op_sel:[0,0,1]
	v_cvt_pk_bf16_f32 v78, v60, v61
	v_cvt_pk_bf16_f32 v79, v62, v63
	global_store_dwordx2 v[76:77], v[78:79], off offset:512 nt
	global_store_dword v[82:83], v84, off offset:256 nt
	s_nop 0
	s_nop 0
	v_mov_b32_e32 v35, 0
	s_nop 0
	v_pk_fma_f32 v[70:71], v[166:167], v[68:69], v[216:217]
	s_nop 0
	v_med3_f32 v68, v70, s69, v208
	v_med3_f32 v69, v71, s69, v208
	v_cvt_pk_fp8_f32 v35, v68, v69
	v_pk_fma_f32 v[68:69], v[168:169], v[88:89], v[218:219]
	s_nop 0
	v_med3_f32 v78, v68, s69, v208
	v_med3_f32 v79, v69, s69, v208
	v_cvt_pk_fp8_f32 v35, v78, v79 op_sel:[0,0,1]
	v_cvt_pk_bf16_f32 v78, v70, v71
	v_cvt_pk_bf16_f32 v79, v68, v69
	global_store_dwordx2 v[76:77], v[78:79], off offset:1024 nt
	global_store_dword v[82:83], v35, off offset:512 nt
	s_nop 0
	v_mov_b32_e32 v35, 0
	s_nop 0
	v_pk_fma_f32 v[80:81], v[170:171], v[72:73], v[220:221]
	s_nop 0
	v_med3_f32 v72, v80, s69, v208
	v_med3_f32 v73, v81, s69, v208
	v_cvt_pk_fp8_f32 v35, v72, v73
	v_pk_fma_f32 v[78:79], v[172:173], v[74:75], v[222:223]
	s_nop 0
	v_med3_f32 v72, v78, s69, v208
	v_med3_f32 v73, v79, s69, v208
	v_cvt_pk_fp8_f32 v35, v72, v73 op_sel:[0,0,1]
	v_cvt_pk_bf16_f32 v72, v80, v81
	v_cvt_pk_bf16_f32 v73, v78, v79
	global_store_dwordx2 v[76:77], v[72:73], off offset:1536 nt
	global_store_dword v[82:83], v35, off offset:768 nt
	s_nop 0
	s_nop 0
	v_mov_b32_e32 v35, 0
	s_nop 0
	v_pk_fma_f32 v[86:87], v[174:175], v[64:65], v[224:225]
	s_nop 0
	v_med3_f32 v64, v86, s69, v208
	v_med3_f32 v65, v87, s69, v208
	v_cvt_pk_fp8_f32 v35, v64, v65
	v_pk_fma_f32 v[84:85], v[176:177], v[66:67], v[226:227]
	s_nop 0
	v_med3_f32 v64, v84, s69, v208
	v_med3_f32 v65, v85, s69, v208
	v_cvt_pk_fp8_f32 v35, v64, v65 op_sel:[0,0,1]
	v_cvt_pk_bf16_f32 v64, v86, v87
	v_cvt_pk_bf16_f32 v65, v84, v85
	global_store_dwordx2 v[76:77], v[64:65], off offset:2048 nt
	global_store_dword v[82:83], v35, off offset:1024 nt
	s_nop 0
	s_nop 0
	v_mov_b32_e32 v35, 0
	s_nop 0
	v_pk_fma_f32 v[90:91], v[178:179], v[56:57], v[228:229]
	s_nop 0
	v_med3_f32 v56, v90, s69, v208
	v_med3_f32 v57, v91, s69, v208
	v_cvt_pk_fp8_f32 v35, v56, v57
	v_pk_fma_f32 v[88:89], v[180:181], v[58:59], v[230:231]
	s_nop 0
	v_med3_f32 v56, v88, s69, v208
	v_med3_f32 v57, v89, s69, v208
	v_cvt_pk_fp8_f32 v35, v56, v57 op_sel:[0,0,1]
	v_cvt_pk_bf16_f32 v56, v90, v91
	v_cvt_pk_bf16_f32 v57, v88, v89
	global_store_dwordx2 v[76:77], v[56:57], off offset:2560 nt
	global_store_dword v[82:83], v35, off offset:1280 nt
	s_nop 0
	s_nop 0
	v_mov_b32_e32 v35, 0
	s_nop 0
	v_pk_fma_f32 v[94:95], v[182:183], v[52:53], v[232:233]
	s_nop 0
	v_med3_f32 v52, v94, s69, v208
	v_med3_f32 v53, v95, s69, v208
	v_cvt_pk_fp8_f32 v35, v52, v53
	v_pk_fma_f32 v[92:93], v[184:185], v[54:55], v[234:235]
	s_nop 0
	v_med3_f32 v52, v92, s69, v208
	v_med3_f32 v53, v93, s69, v208
	v_cvt_pk_fp8_f32 v35, v52, v53 op_sel:[0,0,1]
	v_cvt_pk_bf16_f32 v52, v94, v95
	v_cvt_pk_bf16_f32 v53, v92, v93
	global_store_dwordx2 v[76:77], v[52:53], off offset:3072 nt
	global_store_dword v[82:83], v35, off offset:1536 nt
	s_nop 0
	s_nop 0
	v_mov_b32_e32 v35, 0
	s_nop 0
	v_pk_fma_f32 v[96:97], v[186:187], v[46:47], v[246:247]
	s_nop 0
	v_med3_f32 v46, v96, s69, v208
	v_med3_f32 v47, v97, s69, v208
	v_mov_b32_e32 v52, 0
	v_cvt_pk_fp8_f32 v52, v46, v47
	v_pk_fma_f32 v[98:99], v[188:189], v[44:45], v[248:249]
	s_nop 0
	v_med3_f32 v44, v98, s69, v208
	v_med3_f32 v45, v99, s69, v208
	v_cvt_pk_fp8_f32 v52, v44, v45 op_sel:[0,0,1]
	v_cvt_pk_bf16_f32 v44, v96, v97
	v_cvt_pk_bf16_f32 v45, v98, v99
	global_store_dwordx2 v[76:77], v[44:45], off offset:3584 nt
	global_store_dword v[82:83], v52, off offset:1792 nt
	v_lshlrev_b32_e32 v102, 16, v42
	v_and_b32_e32 v103, 0xffff0000, v42
	v_lshlrev_b32_e32 v100, 16, v43
	v_and_b32_e32 v101, 0xffff0000, v43
	v_add_f32_e32 v42, v102, v103
	v_add_f32_e32 v43, v100, v101
	v_lshlrev_b32_e32 v74, 16, v40
	v_and_b32_e32 v75, 0xffff0000, v40
	v_lshlrev_b32_e32 v72, 16, v41
	v_and_b32_e32 v73, 0xffff0000, v41
	v_add_f32_e32 v42, v42, v43
	v_add_f32_e32 v40, v74, v75
	v_add_f32_e32 v41, v72, v73
	v_lshlrev_b32_e32 v64, 16, v38
	v_and_b32_e32 v65, 0xffff0000, v38
	v_lshlrev_b32_e32 v66, 16, v39
	v_and_b32_e32 v67, 0xffff0000, v39
	v_add_f32_e32 v42, 0, v42
	v_add_f32_e32 v40, v40, v41
	v_add_f32_e32 v38, v64, v65
	v_add_f32_e32 v39, v66, v67
	v_lshlrev_b32_e32 v56, 16, v36
	v_and_b32_e32 v57, 0xffff0000, v36
	v_lshlrev_b32_e32 v58, 16, v37
	v_and_b32_e32 v59, 0xffff0000, v37
	v_add_f32_e32 v40, v42, v40
	v_add_f32_e32 v38, v38, v39
	v_add_f32_e32 v36, v56, v57
	v_add_f32_e32 v37, v58, v59
	v_lshlrev_b32_e32 v52, 16, v22
	v_and_b32_e32 v53, 0xffff0000, v22
	v_lshlrev_b32_e32 v54, 16, v23
	v_and_b32_e32 v55, 0xffff0000, v23
	v_add_f32_e32 v38, v40, v38
	v_add_f32_e32 v36, v36, v37
	v_add_f32_e32 v22, v52, v53
	v_add_f32_e32 v23, v54, v55
	v_add_f32_e32 v36, v38, v36
	v_add_f32_e32 v22, v22, v23
	v_lshlrev_b32_e32 v44, 16, v20
	v_and_b32_e32 v45, 0xffff0000, v20
	v_lshlrev_b32_e32 v46, 16, v21
	v_and_b32_e32 v47, 0xffff0000, v21
	v_add_f32_e32 v22, v36, v22
	v_add_f32_e32 v20, v44, v45
	v_add_f32_e32 v21, v46, v47
	v_lshlrev_b32_e32 v36, 16, v18
	v_and_b32_e32 v37, 0xffff0000, v18
	v_lshlrev_b32_e32 v38, 16, v19
	v_and_b32_e32 v39, 0xffff0000, v19
	v_add_f32_e32 v20, v20, v21
	v_add_f32_e32 v18, v36, v37
	v_add_f32_e32 v19, v38, v39
	v_lshlrev_b32_e32 v42, 16, v16
	v_and_b32_e32 v43, 0xffff0000, v16
	v_lshlrev_b32_e32 v40, 16, v17
	v_and_b32_e32 v41, 0xffff0000, v17
	v_add_f32_e32 v20, v22, v20
	v_add_f32_e32 v18, v18, v19
	v_add_f32_e32 v16, v42, v43
	v_add_f32_e32 v17, v40, v41
	v_add_f32_e32 v18, v20, v18
	v_add_f32_e32 v16, v16, v17
	v_add_f32_e32 v16, v18, v16
	s_mov_b64 s[6:7], s[34:35]
	s_mov_b64 s[8:9], s[36:37]
	v_add_f32_dpp v16, v16, v16 quad_perm:[1,0,3,2] row_mask:0xf bank_mask:0xf bound_ctrl:1
	v_lshl_add_u64 v[108:109], s[6:7], 0, v[192:193]
	v_lshl_add_u64 v[104:105], v[28:29], 0, s[42:43]
	v_add_f32_dpp v16, v16, v16 quad_perm:[2,3,0,1] row_mask:0xf bank_mask:0xf bound_ctrl:1
	v_lshl_add_u64 v[106:107], s[8:9], 0, v[192:193]
	s_lshl_b64 s[6:7], s[40:41], 11
	v_add_f32_dpp v16, v16, v16 row_ror:4 row_mask:0xf bank_mask:0xf bound_ctrl:1
	v_lshl_add_u64 v[82:83], v[30:31], 0, s[6:7]
	s_nop 0
	v_add_f32_dpp v16, v16, v16 row_ror:8 row_mask:0xf bank_mask:0xf bound_ctrl:1
	v_mov_b32_e32 v17, v16
	s_nop 1
	v_permlane16_swap_b32_e32 v16, v17
	v_add_f32_e32 v16, v16, v17
	v_mov_b32_e32 v17, v16
	s_nop 1
	v_permlane32_swap_b32_e32 v16, v17
	v_add_f32_e32 v16, v16, v17
	v_fmac_f32_e32 v101, 0xba000000, v16
	v_fmac_f32_e32 v103, 0xba000000, v16
	v_fmac_f32_e32 v100, 0xba000000, v16
	v_fmac_f32_e32 v102, 0xba000000, v16
	v_mul_f32_e32 v17, v103, v103
	v_mul_f32_e32 v18, v101, v101
	v_fmac_f32_e32 v17, v102, v102
	v_fmac_f32_e32 v18, v100, v100
	v_fmac_f32_e32 v73, 0xba000000, v16
	v_fmac_f32_e32 v75, 0xba000000, v16
	v_add_f32_e32 v17, v17, v18
	v_fmac_f32_e32 v72, 0xba000000, v16
	v_fmac_f32_e32 v74, 0xba000000, v16
	v_mul_f32_e32 v18, v75, v75
	v_mul_f32_e32 v19, v73, v73
	v_fmac_f32_e32 v18, v74, v74
	v_fmac_f32_e32 v19, v72, v72
	v_add_f32_e32 v18, v18, v19
	v_fmac_f32_e32 v67, 0xba000000, v16
	v_fmac_f32_e32 v65, 0xba000000, v16
	v_add_f32_e32 v17, v17, v18
	v_fmac_f32_e32 v66, 0xba000000, v16
	v_fmac_f32_e32 v64, 0xba000000, v16
	v_mul_f32_e32 v18, v65, v65
	v_mul_f32_e32 v19, v67, v67
	v_fmac_f32_e32 v18, v64, v64
	v_fmac_f32_e32 v19, v66, v66
	v_add_f32_e32 v18, v18, v19
	v_fmac_f32_e32 v59, 0xba000000, v16
	v_fmac_f32_e32 v57, 0xba000000, v16
	v_add_f32_e32 v17, v17, v18
	v_fmac_f32_e32 v58, 0xba000000, v16
	v_fmac_f32_e32 v56, 0xba000000, v16
	v_mul_f32_e32 v18, v57, v57
	v_mul_f32_e32 v19, v59, v59
	v_fmac_f32_e32 v18, v56, v56
	v_fmac_f32_e32 v19, v58, v58
	v_add_f32_e32 v18, v18, v19
	v_fmac_f32_e32 v55, 0xba000000, v16
	v_fmac_f32_e32 v53, 0xba000000, v16
	v_add_f32_e32 v17, v17, v18
	v_fmac_f32_e32 v54, 0xba000000, v16
	v_fmac_f32_e32 v52, 0xba000000, v16
	v_mul_f32_e32 v18, v53, v53
	v_mul_f32_e32 v19, v55, v55
	v_fmac_f32_e32 v18, v52, v52
	v_fmac_f32_e32 v19, v54, v54
	v_add_f32_e32 v18, v18, v19
	v_fmac_f32_e32 v47, 0xba000000, v16
	v_fmac_f32_e32 v45, 0xba000000, v16
	v_add_f32_e32 v17, v17, v18
	v_fmac_f32_e32 v46, 0xba000000, v16
	v_fmac_f32_e32 v44, 0xba000000, v16
	v_mul_f32_e32 v18, v45, v45
	v_mul_f32_e32 v19, v47, v47
	v_fmac_f32_e32 v18, v44, v44
	v_fmac_f32_e32 v19, v46, v46
	v_add_f32_e32 v18, v18, v19
	v_fmac_f32_e32 v39, 0xba000000, v16
	v_fmac_f32_e32 v37, 0xba000000, v16
	v_add_f32_e32 v17, v17, v18
	v_fmac_f32_e32 v38, 0xba000000, v16
	v_fmac_f32_e32 v36, 0xba000000, v16
	v_mul_f32_e32 v18, v37, v37
	v_mul_f32_e32 v19, v39, v39
	v_fmac_f32_e32 v18, v36, v36
	v_fmac_f32_e32 v19, v38, v38
	v_add_f32_e32 v18, v18, v19
	v_fmac_f32_e32 v41, 0xba000000, v16
	v_fmac_f32_e32 v43, 0xba000000, v16
	v_add_f32_e32 v17, v17, v18
	v_fmac_f32_e32 v40, 0xba000000, v16
	v_fmac_f32_e32 v42, 0xba000000, v16
	v_mul_f32_e32 v16, v43, v43
	v_mul_f32_e32 v18, v41, v41
	v_fmac_f32_e32 v16, v42, v42
	v_fmac_f32_e32 v18, v40, v40
	v_add_f32_e32 v16, v16, v18
	v_add_f32_e32 v16, v17, v16
	s_nop 1
	v_add_f32_dpp v16, v16, v16 quad_perm:[1,0,3,2] row_mask:0xf bank_mask:0xf bound_ctrl:1
	s_nop 1
	v_add_f32_dpp v16, v16, v16 quad_perm:[2,3,0,1] row_mask:0xf bank_mask:0xf bound_ctrl:1
	s_nop 1
	v_add_f32_dpp v16, v16, v16 row_ror:4 row_mask:0xf bank_mask:0xf bound_ctrl:1
	s_nop 1
	v_add_f32_dpp v16, v16, v16 row_ror:8 row_mask:0xf bank_mask:0xf bound_ctrl:1
	v_mov_b32_e32 v17, v16
	s_nop 1
	v_permlane16_swap_b32_e32 v16, v17
	v_add_f32_e32 v16, v16, v17
	v_mov_b32_e32 v17, v16
	s_nop 1
	v_permlane32_swap_b32_e32 v16, v17
	v_add_f32_e32 v16, v16, v17
	v_fmamk_f32 v16, v16, 0x3a000000, v207
	v_rsq_f32_e32 v76, v16
	s_nop 0
	v_pk_mul_f32 v[102:103], v[76:77], v[102:103] op_sel_hi:[0,1]
	v_pk_mul_f32 v[100:101], v[76:77], v[100:101] op_sel_hi:[0,1]
	v_pk_mul_f32 v[74:75], v[76:77], v[74:75] op_sel_hi:[0,1]
	v_pk_mul_f32 v[72:73], v[76:77], v[72:73] op_sel_hi:[0,1]
	v_pk_mul_f32 v[110:111], v[76:77], v[64:65] op_sel_hi:[0,1]
	v_pk_mul_f32 v[64:65], v[76:77], v[66:67] op_sel_hi:[0,1]
	s_waitcnt lgkmcnt(0)
	v_pk_fma_f32 v[100:101], v[160:161], v[100:101], v[200:201]
	v_pk_fma_f32 v[102:103], v[158:159], v[102:103], v[198:199]
	v_mov_b32_e32 v20, 0
	v_cvt_pk_bf16_f32 v16, v102, v103
	v_cvt_pk_bf16_f32 v17, v100, v101
	global_store_dwordx2 v[104:105], v[16:17], off nt
	v_med3_f32 v16, v102, s69, v208
	v_med3_f32 v17, v103, s69, v208
	v_cvt_pk_fp8_f32 v20, v16, v17
	v_med3_f32 v18, v100, s69, v208
	v_med3_f32 v19, v101, s69, v208
	v_cvt_pk_fp8_f32 v20, v18, v19 op_sel:[0,0,1]
	global_store_dword v[82:83], v20, off nt
	s_nop 0
	s_nop 0
	s_nop 0
	v_pk_fma_f32 v[72:73], v[164:165], v[72:73], v[204:205]
	v_pk_fma_f32 v[74:75], v[162:163], v[74:75], v[202:203]
	v_mov_b32_e32 v20, 0
	v_cvt_pk_bf16_f32 v16, v74, v75
	v_cvt_pk_bf16_f32 v17, v72, v73
	global_store_dwordx2 v[104:105], v[16:17], off offset:512 nt
	v_med3_f32 v16, v74, s69, v208
	v_med3_f32 v17, v75, s69, v208
	v_cvt_pk_fp8_f32 v20, v16, v17
	v_med3_f32 v18, v72, s69, v208
	v_med3_f32 v19, v73, s69, v208
	v_cvt_pk_fp8_f32 v20, v18, v19 op_sel:[0,0,1]
	global_store_dword v[82:83], v20, off offset:256 nt
	s_nop 0
	s_nop 0
	s_nop 0
	v_pk_fma_f32 v[64:65], v[168:169], v[64:65], v[218:219]
	v_pk_fma_f32 v[66:67], v[166:167], v[110:111], v[216:217]
	v_mov_b32_e32 v20, 0
	v_cvt_pk_bf16_f32 v16, v66, v67
	v_cvt_pk_bf16_f32 v17, v64, v65
	global_store_dwordx2 v[104:105], v[16:17], off offset:1024 nt
	v_med3_f32 v16, v66, s69, v208
	v_med3_f32 v17, v67, s69, v208
	v_cvt_pk_fp8_f32 v20, v16, v17
	v_med3_f32 v18, v64, s69, v208
	v_med3_f32 v19, v65, s69, v208
	v_pk_mul_f32 v[110:111], v[76:77], v[56:57] op_sel_hi:[0,1]
	v_cvt_pk_fp8_f32 v20, v18, v19 op_sel:[0,0,1]
	v_pk_mul_f32 v[56:57], v[76:77], v[58:59] op_sel_hi:[0,1]
	global_store_dword v[82:83], v20, off offset:512 nt
	s_nop 0
	s_nop 0
	s_nop 0
	v_pk_fma_f32 v[56:57], v[172:173], v[56:57], v[222:223]
	v_pk_fma_f32 v[58:59], v[170:171], v[110:111], v[220:221]
	v_mov_b32_e32 v20, 0
	v_cvt_pk_bf16_f32 v16, v58, v59
	v_cvt_pk_bf16_f32 v17, v56, v57
	global_store_dwordx2 v[104:105], v[16:17], off offset:1536 nt
	v_med3_f32 v16, v58, s69, v208
	v_med3_f32 v17, v59, s69, v208
	v_cvt_pk_fp8_f32 v20, v16, v17
	v_med3_f32 v18, v56, s69, v208
	v_med3_f32 v19, v57, s69, v208
	v_add_co_u32_e32 v16, vcc, s33, v108
	v_cvt_pk_fp8_f32 v20, v18, v19 op_sel:[0,0,1]
	s_nop 0
	v_addc_co_u32_e32 v17, vcc, 0, v109, vcc
	v_add_co_u32_e32 v18, vcc, s33, v106
	global_store_dword v[82:83], v20, off offset:768 nt
	s_nop 0
	v_addc_co_u32_e32 v19, vcc, 0, v107, vcc
	s_nop 0
	v_pk_mul_f32 v[110:111], v[76:77], v[52:53] op_sel_hi:[0,1]
	v_pk_mul_f32 v[52:53], v[76:77], v[54:55] op_sel_hi:[0,1]
	v_mov_b32_e32 v77, 0
	s_nop 0
	v_pk_fma_f32 v[52:53], v[176:177], v[52:53], v[226:227]
	v_pk_fma_f32 v[54:55], v[174:175], v[110:111], v[224:225]
	v_med3_f32 v22, v52, s69, v208
	v_cvt_pk_bf16_f32 v20, v54, v55
	v_cvt_pk_bf16_f32 v21, v52, v53
	global_store_dwordx2 v[104:105], v[20:21], off offset:2048 nt
	v_med3_f32 v20, v54, s69, v208
	v_med3_f32 v21, v55, s69, v208
	v_cvt_pk_fp8_f32 v77, v20, v21
	v_med3_f32 v23, v53, s69, v208
; #define LAS __attribute__((address_space(3)))
; __global__ void __launch_bounds__(NTHREADS, 2) hybrid_fwd(Args a) {
;     ...
;                     f32x2 y2[8][4];
; #pragma unroll
;                     for (int j = 0; j < 8; ++j)
; #pragma unroll
;                         for (int c = 0; c < 4; ++c) y2[j][c] = (f32x2){ya[j][c], yb[j][c]};
;                     f32x2 acc2[16];
; #pragma unroll
;                     for (int e = 0; e < 16; ++e) acc2[e] = (f32x2){0.f, 0.f};
; #pragma unroll
;                     for (int j = 0; j < 8; ++j) {
; #pragma unroll
;                         for (int e = 0; e < 16; ++e) { const f32x4 w = *(const LAS f32x4*)(rwT + e * 2052 + j * 256 + lane * 4);
;                             acc2[e] += y2[j][0] * (f32x2){w[0], w[0]}; acc2[e] += y2[j][1] * (f32x2){w[1], w[1]};
;                             acc2[e] += y2[j][2] * (f32x2){w[2], w[2]}; acc2[e] += y2[j][3] * (f32x2){w[3], w[3]}; }
	v_cvt_pk_fp8_f32 v77, v22, v23 op_sel:[0,0,1]
	global_store_dword v[82:83], v77, off offset:1024 nt
	s_nop 0
	v_pk_mul_f32 v[110:111], v[76:77], v[44:45] op_sel_hi:[0,1]
	v_pk_mul_f32 v[44:45], v[76:77], v[46:47] op_sel_hi:[0,1]
	v_mov_b32_e32 v77, 0
	s_nop 0
	v_pk_fma_f32 v[44:45], v[180:181], v[44:45], v[230:231]
	v_pk_fma_f32 v[46:47], v[178:179], v[110:111], v[228:229]
	v_med3_f32 v22, v44, s69, v208
	v_cvt_pk_bf16_f32 v20, v46, v47
	v_cvt_pk_bf16_f32 v21, v44, v45
	global_store_dwordx2 v[104:105], v[20:21], off offset:2560 nt
	v_med3_f32 v20, v46, s69, v208
	v_med3_f32 v21, v47, s69, v208
	v_cvt_pk_fp8_f32 v77, v20, v21
	v_med3_f32 v23, v45, s69, v208
	v_cvt_pk_fp8_f32 v77, v22, v23 op_sel:[0,0,1]
	global_store_dword v[82:83], v77, off offset:1280 nt
	s_nop 0
	v_pk_mul_f32 v[110:111], v[76:77], v[36:37] op_sel_hi:[0,1]
	v_pk_mul_f32 v[36:37], v[76:77], v[38:39] op_sel_hi:[0,1]
	v_mov_b32_e32 v77, 0
	s_nop 0
	v_pk_fma_f32 v[36:37], v[184:185], v[36:37], v[234:235]
	v_pk_fma_f32 v[38:39], v[182:183], v[110:111], v[232:233]
	v_med3_f32 v22, v36, s69, v208
	v_cvt_pk_bf16_f32 v20, v38, v39
	v_cvt_pk_bf16_f32 v21, v36, v37
	global_store_dwordx2 v[104:105], v[20:21], off offset:3072 nt
	v_med3_f32 v20, v38, s69, v208
	v_med3_f32 v21, v39, s69, v208
	v_cvt_pk_fp8_f32 v77, v20, v21
	v_med3_f32 v23, v37, s69, v208
	v_cvt_pk_fp8_f32 v77, v22, v23 op_sel:[0,0,1]
	global_store_dword v[82:83], v77, off offset:1536 nt
	s_nop 0
	v_pk_mul_f32 v[18:19], v[76:77], v[42:43] op_sel_hi:[0,1]
	v_pk_mul_f32 v[16:17], v[76:77], v[40:41] op_sel_hi:[0,1]
	v_mov_b32_e32 v40, 0
	s_nop 0
	v_pk_fma_f32 v[16:17], v[188:189], v[16:17], v[248:249]
	v_pk_fma_f32 v[18:19], v[186:187], v[18:19], v[246:247]
	v_med3_f32 v22, v16, s69, v208
	v_cvt_pk_bf16_f32 v20, v18, v19
	v_cvt_pk_bf16_f32 v21, v16, v17
	global_store_dwordx2 v[104:105], v[20:21], off offset:3584 nt
	v_med3_f32 v20, v18, s69, v208
	v_med3_f32 v21, v19, s69, v208
	v_cvt_pk_fp8_f32 v40, v20, v21
	v_med3_f32 v23, v17, s69, v208
	v_cvt_pk_fp8_f32 v40, v22, v23 op_sel:[0,0,1]
	global_store_dword v[82:83], v40, off offset:1792 nt
	v_add_u32_e32 v238, 0x10000, v25
	ds_read_b128 v[158:161], v25 offset:0
	ds_read_b128 v[162:165], v25 offset:8208
	ds_read_b128 v[166:169], v25 offset:16416
	ds_read_b128 v[170:173], v25 offset:24624
	ds_read_b128 v[174:177], v25 offset:32832
	ds_read_b128 v[178:181], v25 offset:41040
	ds_read_b128 v[182:185], v25 offset:49248
	ds_read_b128 v[186:189], v25 offset:57456
	v_mov_b32_e32 v76, v70
	v_mov_b32_e32 v77, v66
	v_mov_b32_e32 v66, v71
	v_mov_b32_e32 v82, v68
	v_mov_b32_e32 v83, v64
	v_mov_b32_e32 v64, v69
	v_mov_b32_e32 v68, v80
	v_mov_b32_e32 v69, v58
	v_mov_b32_e32 v58, v81
	v_mov_b32_e32 v70, v78
	v_mov_b32_e32 v71, v56
	v_mov_b32_e32 v56, v79
	ds_read_b128 v[198:201], v238 offset:128
	v_mov_b32_e32 v108, v48
	v_mov_b32_e32 v109, v102
	v_mov_b32_e32 v102, v49
	v_mov_b32_e32 v106, v62
	v_mov_b32_e32 v107, v72
	v_mov_b32_e32 v72, v63
	v_mov_b32_e32 v62, v84
	v_mov_b32_e32 v63, v52
	v_mov_b32_e32 v52, v85
	s_waitcnt lgkmcnt(8)
	v_pk_fma_f32 v[84:85], v[108:109], v[158:159], 0 op_sel_hi:[1,0,0]
	v_mov_b32_e32 v104, v60
	v_mov_b32_e32 v105, v74
	v_mov_b32_e32 v74, v61
	v_mov_b32_e32 v60, v86
	v_mov_b32_e32 v61, v54
	v_mov_b32_e32 v54, v87
	v_pk_fma_f32 v[78:79], v[158:159], v[102:103], v[84:85] op_sel:[1,0,0]
	ds_read_b128 v[202:205], v238 offset:8336
	v_mov_b32_e32 v110, v50
	v_mov_b32_e32 v111, v100
	v_mov_b32_e32 v100, v51
	v_pk_fma_f32 v[78:79], v[160:161], v[110:111], v[78:79] op_sel_hi:[0,1,1]
	v_mov_b32_e32 v80, v161
	v_pk_fma_f32 v[78:79], v[80:81], v[100:101], v[78:79] op_sel_hi:[0,1,1]
	s_waitcnt lgkmcnt(8)
	v_pk_fma_f32 v[80:81], v[108:109], v[162:163], 0 op_sel_hi:[1,0,0]
	v_mov_b32_e32 v50, v88
	v_pk_fma_f32 v[80:81], v[162:163], v[102:103], v[80:81] op_sel:[1,0,0]
	v_mov_b32_e32 v84, v165
	v_pk_fma_f32 v[80:81], v[164:165], v[110:111], v[80:81] op_sel_hi:[0,1,1]
	v_pk_fma_f32 v[120:121], v[84:85], v[100:101], v[80:81] op_sel_hi:[0,1,1]
	ds_read_b128 v[216:219], v238 offset:16544
	v_mov_b32_e32 v51, v44
	v_mov_b32_e32 v44, v89
	v_mov_b32_e32 v48, v90
	v_mov_b32_e32 v49, v46
	s_waitcnt lgkmcnt(8)
	v_pk_fma_f32 v[80:81], v[108:109], v[166:167], 0 op_sel_hi:[1,0,0]
	v_mov_b32_e32 v46, v91
	v_pk_fma_f32 v[80:81], v[166:167], v[102:103], v[80:81] op_sel:[1,0,0]
	v_mov_b32_e32 v84, v169
	v_pk_fma_f32 v[80:81], v[168:169], v[110:111], v[80:81] op_sel_hi:[0,1,1]
	v_pk_fma_f32 v[122:123], v[84:85], v[100:101], v[80:81] op_sel_hi:[0,1,1]
	ds_read_b128 v[220:223], v238 offset:24752
	v_mov_b32_e32 v42, v92
	v_mov_b32_e32 v43, v36
	v_mov_b32_e32 v36, v93
	v_mov_b32_e32 v40, v94
	s_waitcnt lgkmcnt(8)
	v_pk_fma_f32 v[80:81], v[108:109], v[170:171], 0 op_sel_hi:[1,0,0]
	v_mov_b32_e32 v41, v38
	v_pk_fma_f32 v[80:81], v[170:171], v[102:103], v[80:81] op_sel:[1,0,0]
	v_mov_b32_e32 v84, v173
	v_pk_fma_f32 v[80:81], v[172:173], v[110:111], v[80:81] op_sel_hi:[0,1,1]
	v_pk_fma_f32 v[80:81], v[84:85], v[100:101], v[80:81] op_sel_hi:[0,1,1]
	ds_read_b128 v[224:227], v238 offset:32960
	v_mov_b32_e32 v38, v95
	v_mov_b32_e32 v22, v96
	v_mov_b32_e32 v23, v18
	v_mov_b32_e32 v18, v97
	s_waitcnt lgkmcnt(8)
	v_pk_fma_f32 v[88:89], v[108:109], v[174:175], 0 op_sel_hi:[1,0,0]
	v_mov_b32_e32 v20, v98
	v_pk_fma_f32 v[84:85], v[174:175], v[102:103], v[88:89] op_sel:[1,0,0]
	v_mov_b32_e32 v21, v16
	v_pk_fma_f32 v[84:85], v[176:177], v[110:111], v[84:85] op_sel_hi:[0,1,1]
	v_mov_b32_e32 v86, v177
	v_pk_fma_f32 v[84:85], v[86:87], v[100:101], v[84:85] op_sel_hi:[0,1,1]
	ds_read_b128 v[228:231], v238 offset:41168
	v_mov_b32_e32 v16, v99
	s_waitcnt lgkmcnt(8)
; #define LAS __attribute__((address_space(3)))
; __global__ void __launch_bounds__(NTHREADS, 2) hybrid_fwd(Args a) {
;     ...
; #pragma unroll
;                     for (int j = 0; j < 8; ++j) {
; #pragma unroll
;                         for (int e = 0; e < 16; ++e) { const f32x4 w = *(const LAS f32x4*)(rwT + e * 2052 + j * 256 + lane * 4);
;                             acc2[e] += y2[j][0] * (f32x2){w[0], w[0]}; acc2[e] += y2[j][1] * (f32x2){w[1], w[1]};
;                             acc2[e] += y2[j][2] * (f32x2){w[2], w[2]}; acc2[e] += y2[j][3] * (f32x2){w[3], w[3]}; }
;                         __builtin_amdgcn_sched_barrier(0);
;                     }
	v_pk_fma_f32 v[90:91], v[108:109], v[178:179], 0 op_sel_hi:[1,0,0]
	s_nop 0
	v_pk_fma_f32 v[86:87], v[178:179], v[102:103], v[90:91] op_sel:[1,0,0]
	s_nop 0
	v_pk_fma_f32 v[86:87], v[180:181], v[110:111], v[86:87] op_sel_hi:[0,1,1]
	v_mov_b32_e32 v88, v181
	v_pk_fma_f32 v[86:87], v[88:89], v[100:101], v[86:87] op_sel_hi:[0,1,1]
	ds_read_b128 v[232:235], v238 offset:49376
	s_waitcnt lgkmcnt(8)
	v_pk_fma_f32 v[92:93], v[108:109], v[182:183], 0 op_sel_hi:[1,0,0]
	s_nop 0
	v_pk_fma_f32 v[88:89], v[182:183], v[102:103], v[92:93] op_sel:[1,0,0]
	s_nop 0
	v_pk_fma_f32 v[88:89], v[184:185], v[110:111], v[88:89] op_sel_hi:[0,1,1]
	v_mov_b32_e32 v90, v185
	v_pk_fma_f32 v[88:89], v[90:91], v[100:101], v[88:89] op_sel_hi:[0,1,1]
	ds_read_b128 v[242:245], v238 offset:57584
	s_waitcnt lgkmcnt(8)
	v_pk_fma_f32 v[94:95], v[108:109], v[186:187], 0 op_sel_hi:[1,0,0]
	s_nop 0
	v_pk_fma_f32 v[90:91], v[186:187], v[102:103], v[94:95] op_sel:[1,0,0]
	s_nop 0
	v_pk_fma_f32 v[90:91], v[188:189], v[110:111], v[90:91] op_sel_hi:[0,1,1]
	v_mov_b32_e32 v92, v189
	v_pk_fma_f32 v[90:91], v[92:93], v[100:101], v[90:91] op_sel_hi:[0,1,1]
	ds_read_b128 v[246:249], v25 offset:1024
	s_waitcnt lgkmcnt(8)
	v_pk_fma_f32 v[96:97], v[108:109], v[198:199], 0 op_sel_hi:[1,0,0]
	s_nop 0
	v_pk_fma_f32 v[92:93], v[198:199], v[102:103], v[96:97] op_sel:[1,0,0]
	s_nop 0
	v_pk_fma_f32 v[92:93], v[200:201], v[110:111], v[92:93] op_sel_hi:[0,1,1]
	v_mov_b32_e32 v94, v201
	v_pk_fma_f32 v[92:93], v[94:95], v[100:101], v[92:93] op_sel_hi:[0,1,1]
	ds_read_b128 v[250:253], v25 offset:9232
	s_waitcnt lgkmcnt(8)
	v_pk_fma_f32 v[98:99], v[108:109], v[202:203], 0 op_sel_hi:[1,0,0]
	s_nop 0
	v_pk_fma_f32 v[94:95], v[202:203], v[102:103], v[98:99] op_sel:[1,0,0]
	s_nop 0
	v_pk_fma_f32 v[94:95], v[204:205], v[110:111], v[94:95] op_sel_hi:[0,1,1]
	v_mov_b32_e32 v96, v205
	v_pk_fma_f32 v[94:95], v[96:97], v[100:101], v[94:95] op_sel_hi:[0,1,1]
	ds_read_b128 v[158:161], v25 offset:17440
	s_waitcnt lgkmcnt(8)
	v_pk_fma_f32 v[112:113], v[108:109], v[216:217], 0 op_sel_hi:[1,0,0]
	s_nop 0
	v_pk_fma_f32 v[96:97], v[216:217], v[102:103], v[112:113] op_sel:[1,0,0]
	ds_read_b128 v[162:165], v25 offset:25648
	v_pk_fma_f32 v[96:97], v[218:219], v[110:111], v[96:97] op_sel_hi:[0,1,1]
	v_mov_b32_e32 v98, v219
	v_pk_fma_f32 v[96:97], v[98:99], v[100:101], v[96:97] op_sel_hi:[0,1,1]
	s_waitcnt lgkmcnt(8)
	v_pk_fma_f32 v[98:99], v[108:109], v[220:221], 0 op_sel_hi:[1,0,0]
	s_nop 0
	v_pk_fma_f32 v[98:99], v[220:221], v[102:103], v[98:99] op_sel:[1,0,0]
	v_mov_b32_e32 v112, v223
	v_pk_fma_f32 v[98:99], v[222:223], v[110:111], v[98:99] op_sel_hi:[0,1,1]
	v_pk_fma_f32 v[98:99], v[112:113], v[100:101], v[98:99] op_sel_hi:[0,1,1]
	ds_read_b128 v[166:169], v25 offset:33856
	s_waitcnt lgkmcnt(8)
	v_pk_fma_f32 v[116:117], v[108:109], v[224:225], 0 op_sel_hi:[1,0,0]
	s_nop 0
	v_pk_fma_f32 v[112:113], v[224:225], v[102:103], v[116:117] op_sel:[1,0,0]
	s_nop 0
	v_pk_fma_f32 v[112:113], v[226:227], v[110:111], v[112:113] op_sel_hi:[0,1,1]
	v_mov_b32_e32 v114, v227
	v_pk_fma_f32 v[112:113], v[114:115], v[100:101], v[112:113] op_sel_hi:[0,1,1]
	ds_read_b128 v[170:173], v25 offset:42064
	s_waitcnt lgkmcnt(8)
	v_pk_fma_f32 v[118:119], v[108:109], v[228:229], 0 op_sel_hi:[1,0,0]
	s_nop 0
	v_pk_fma_f32 v[114:115], v[228:229], v[102:103], v[118:119] op_sel:[1,0,0]
	s_nop 0
	v_pk_fma_f32 v[114:115], v[230:231], v[110:111], v[114:115] op_sel_hi:[0,1,1]
	v_mov_b32_e32 v116, v231
	v_pk_fma_f32 v[114:115], v[116:117], v[100:101], v[114:115] op_sel_hi:[0,1,1]
	ds_read_b128 v[174:177], v25 offset:50272
	s_waitcnt lgkmcnt(8)
	v_pk_fma_f32 v[124:125], v[108:109], v[232:233], 0 op_sel_hi:[1,0,0]
	s_nop 0
	v_pk_fma_f32 v[116:117], v[232:233], v[102:103], v[124:125] op_sel:[1,0,0]
	ds_read_b128 v[178:181], v25 offset:58480
	v_pk_fma_f32 v[116:117], v[234:235], v[110:111], v[116:117] op_sel_hi:[0,1,1]
	v_mov_b32_e32 v118, v235
	v_pk_fma_f32 v[116:117], v[118:119], v[100:101], v[116:117] op_sel_hi:[0,1,1]
	s_waitcnt lgkmcnt(8)
	v_pk_fma_f32 v[108:109], v[108:109], v[242:243], 0 op_sel_hi:[1,0,0]
	s_nop 0
	v_pk_fma_f32 v[102:103], v[242:243], v[102:103], v[108:109] op_sel:[1,0,0]
	v_mov_b32_e32 v108, v245
	v_pk_fma_f32 v[102:103], v[244:245], v[110:111], v[102:103] op_sel_hi:[0,1,1]
	v_pk_fma_f32 v[118:119], v[108:109], v[100:101], v[102:103] op_sel_hi:[0,1,1]
	ds_read_b128 v[182:185], v238 offset:1152
	s_waitcnt lgkmcnt(8)
	v_pk_fma_f32 v[78:79], v[104:105], v[246:247], v[78:79] op_sel_hi:[1,0,1]
	s_nop 0
	v_pk_fma_f32 v[78:79], v[246:247], v[74:75], v[78:79] op_sel:[1,0,0]
	v_mov_b32_e32 v100, v249
	v_pk_fma_f32 v[78:79], v[248:249], v[106:107], v[78:79] op_sel_hi:[0,1,1]
	v_pk_fma_f32 v[78:79], v[100:101], v[72:73], v[78:79] op_sel_hi:[0,1,1]
	ds_read_b128 v[186:189], v238 offset:9360
	s_waitcnt lgkmcnt(8)
	v_pk_fma_f32 v[108:109], v[104:105], v[250:251], v[120:121] op_sel_hi:[1,0,1]
	s_nop 0
	v_pk_fma_f32 v[100:101], v[250:251], v[74:75], v[108:109] op_sel:[1,0,0]
	s_nop 0
	v_pk_fma_f32 v[100:101], v[252:253], v[106:107], v[100:101] op_sel_hi:[0,1,1]
	v_mov_b32_e32 v102, v253
	v_pk_fma_f32 v[120:121], v[102:103], v[72:73], v[100:101] op_sel_hi:[0,1,1]
	ds_read_b128 v[198:201], v238 offset:17568
	s_waitcnt lgkmcnt(8)
	v_pk_fma_f32 v[108:109], v[104:105], v[158:159], v[122:123] op_sel_hi:[1,0,1]
	s_nop 0
	v_pk_fma_f32 v[100:101], v[158:159], v[74:75], v[108:109] op_sel:[1,0,0]
	ds_read_b128 v[202:205], v238 offset:25776
	v_pk_fma_f32 v[100:101], v[160:161], v[106:107], v[100:101] op_sel_hi:[0,1,1]
	v_mov_b32_e32 v102, v161
	v_pk_fma_f32 v[100:101], v[102:103], v[72:73], v[100:101] op_sel_hi:[0,1,1]
	s_waitcnt lgkmcnt(8)
; #define LAS __attribute__((address_space(3)))
; __global__ void __launch_bounds__(NTHREADS, 2) hybrid_fwd(Args a) {
;     ...
; #pragma unroll
;                     for (int j = 0; j < 8; ++j) {
; #pragma unroll
;                         for (int e = 0; e < 16; ++e) { const f32x4 w = *(const LAS f32x4*)(rwT + e * 2052 + j * 256 + lane * 4);
;                             acc2[e] += y2[j][0] * (f32x2){w[0], w[0]}; acc2[e] += y2[j][1] * (f32x2){w[1], w[1]};
;                             acc2[e] += y2[j][2] * (f32x2){w[2], w[2]}; acc2[e] += y2[j][3] * (f32x2){w[3], w[3]}; }
;                         __builtin_amdgcn_sched_barrier(0);
;                     }
	v_pk_fma_f32 v[80:81], v[104:105], v[162:163], v[80:81] op_sel_hi:[1,0,1]
	s_nop 0
	v_pk_fma_f32 v[80:81], v[162:163], v[74:75], v[80:81] op_sel:[1,0,0]
	v_mov_b32_e32 v102, v165
	v_pk_fma_f32 v[80:81], v[164:165], v[106:107], v[80:81] op_sel_hi:[0,1,1]
	ds_read_b128 v[216:219], v238 offset:33984
	v_pk_fma_f32 v[80:81], v[102:103], v[72:73], v[80:81] op_sel_hi:[0,1,1]
	s_waitcnt lgkmcnt(8)
	v_pk_fma_f32 v[84:85], v[104:105], v[166:167], v[84:85] op_sel_hi:[1,0,1]
	s_nop 0
	v_pk_fma_f32 v[84:85], v[166:167], v[74:75], v[84:85] op_sel:[1,0,0]
	v_mov_b32_e32 v102, v169
	v_pk_fma_f32 v[84:85], v[168:169], v[106:107], v[84:85] op_sel_hi:[0,1,1]
	ds_read_b128 v[220:223], v238 offset:42192
	v_pk_fma_f32 v[84:85], v[102:103], v[72:73], v[84:85] op_sel_hi:[0,1,1]
	s_waitcnt lgkmcnt(8)
	v_pk_fma_f32 v[86:87], v[104:105], v[170:171], v[86:87] op_sel_hi:[1,0,1]
	s_nop 0
	v_pk_fma_f32 v[86:87], v[170:171], v[74:75], v[86:87] op_sel:[1,0,0]
	v_mov_b32_e32 v102, v173
	v_pk_fma_f32 v[86:87], v[172:173], v[106:107], v[86:87] op_sel_hi:[0,1,1]
	ds_read_b128 v[224:227], v238 offset:50400
	v_pk_fma_f32 v[86:87], v[102:103], v[72:73], v[86:87] op_sel_hi:[0,1,1]
	s_waitcnt lgkmcnt(8)
	v_pk_fma_f32 v[88:89], v[104:105], v[174:175], v[88:89] op_sel_hi:[1,0,1]
	s_nop 0
	v_pk_fma_f32 v[88:89], v[174:175], v[74:75], v[88:89] op_sel:[1,0,0]
	v_mov_b32_e32 v102, v177
	v_pk_fma_f32 v[88:89], v[176:177], v[106:107], v[88:89] op_sel_hi:[0,1,1]
	ds_read_b128 v[228:231], v238 offset:58608
	v_pk_fma_f32 v[88:89], v[102:103], v[72:73], v[88:89] op_sel_hi:[0,1,1]
	s_waitcnt lgkmcnt(8)
	v_pk_fma_f32 v[90:91], v[104:105], v[178:179], v[90:91] op_sel_hi:[1,0,1]
	s_nop 0
	v_pk_fma_f32 v[90:91], v[178:179], v[74:75], v[90:91] op_sel:[1,0,0]
	v_mov_b32_e32 v102, v181
	v_pk_fma_f32 v[90:91], v[180:181], v[106:107], v[90:91] op_sel_hi:[0,1,1]
	ds_read_b128 v[232:235], v25 offset:2048
	v_pk_fma_f32 v[90:91], v[102:103], v[72:73], v[90:91] op_sel_hi:[0,1,1]
	s_waitcnt lgkmcnt(8)
	v_pk_fma_f32 v[92:93], v[104:105], v[182:183], v[92:93] op_sel_hi:[1,0,1]
	s_nop 0
	v_pk_fma_f32 v[92:93], v[182:183], v[74:75], v[92:93] op_sel:[1,0,0]
	v_mov_b32_e32 v102, v185
	v_pk_fma_f32 v[92:93], v[184:185], v[106:107], v[92:93] op_sel_hi:[0,1,1]
	ds_read_b128 v[242:245], v25 offset:10256
	v_pk_fma_f32 v[92:93], v[102:103], v[72:73], v[92:93] op_sel_hi:[0,1,1]
	s_waitcnt lgkmcnt(8)
	v_pk_fma_f32 v[94:95], v[104:105], v[186:187], v[94:95] op_sel_hi:[1,0,1]
	s_nop 0
	v_pk_fma_f32 v[94:95], v[186:187], v[74:75], v[94:95] op_sel:[1,0,0]
	v_mov_b32_e32 v102, v189
	v_pk_fma_f32 v[94:95], v[188:189], v[106:107], v[94:95] op_sel_hi:[0,1,1]
	ds_read_b128 v[246:249], v25 offset:18464
	v_pk_fma_f32 v[94:95], v[102:103], v[72:73], v[94:95] op_sel_hi:[0,1,1]
	s_waitcnt lgkmcnt(8)
	v_pk_fma_f32 v[96:97], v[104:105], v[198:199], v[96:97] op_sel_hi:[1,0,1]
	s_nop 0
	v_pk_fma_f32 v[96:97], v[198:199], v[74:75], v[96:97] op_sel:[1,0,0]
	v_mov_b32_e32 v102, v201
	v_pk_fma_f32 v[96:97], v[200:201], v[106:107], v[96:97] op_sel_hi:[0,1,1]
	ds_read_b128 v[250:253], v25 offset:26672
	v_pk_fma_f32 v[96:97], v[102:103], v[72:73], v[96:97] op_sel_hi:[0,1,1]
	s_waitcnt lgkmcnt(8)
	v_pk_fma_f32 v[98:99], v[104:105], v[202:203], v[98:99] op_sel_hi:[1,0,1]
	s_nop 0
	v_pk_fma_f32 v[98:99], v[202:203], v[74:75], v[98:99] op_sel:[1,0,0]
	v_mov_b32_e32 v102, v205
	v_pk_fma_f32 v[98:99], v[204:205], v[106:107], v[98:99] op_sel_hi:[0,1,1]
	ds_read_b128 v[162:165], v25 offset:34880
	v_pk_fma_f32 v[98:99], v[102:103], v[72:73], v[98:99] op_sel_hi:[0,1,1]
	s_waitcnt lgkmcnt(8)
	v_pk_fma_f32 v[102:103], v[104:105], v[216:217], v[112:113] op_sel_hi:[1,0,1]
	s_nop 0
	v_pk_fma_f32 v[102:103], v[216:217], v[74:75], v[102:103] op_sel:[1,0,0]
	v_mov_b32_e32 v108, v219
	v_pk_fma_f32 v[102:103], v[218:219], v[106:107], v[102:103] op_sel_hi:[0,1,1]
	v_pk_fma_f32 v[102:103], v[108:109], v[72:73], v[102:103] op_sel_hi:[0,1,1]
	ds_read_b128 v[166:169], v25 offset:43088
	s_waitcnt lgkmcnt(8)
	v_pk_fma_f32 v[112:113], v[104:105], v[220:221], v[114:115] op_sel_hi:[1,0,1]
	s_nop 0
	v_pk_fma_f32 v[108:109], v[220:221], v[74:75], v[112:113] op_sel:[1,0,0]
	s_nop 0
	v_pk_fma_f32 v[108:109], v[222:223], v[106:107], v[108:109] op_sel_hi:[0,1,1]
	v_mov_b32_e32 v110, v223
	v_pk_fma_f32 v[108:109], v[110:111], v[72:73], v[108:109] op_sel_hi:[0,1,1]
	ds_read_b128 v[170:173], v25 offset:51296
	s_waitcnt lgkmcnt(8)
	v_pk_fma_f32 v[114:115], v[104:105], v[224:225], v[116:117] op_sel_hi:[1,0,1]
	s_nop 0
	v_pk_fma_f32 v[110:111], v[224:225], v[74:75], v[114:115] op_sel:[1,0,0]
	s_nop 0
	v_pk_fma_f32 v[110:111], v[226:227], v[106:107], v[110:111] op_sel_hi:[0,1,1]
	v_mov_b32_e32 v112, v227
	v_pk_fma_f32 v[110:111], v[112:113], v[72:73], v[110:111] op_sel_hi:[0,1,1]
	ds_read_b128 v[174:177], v25 offset:59504
	s_waitcnt lgkmcnt(8)
	v_pk_fma_f32 v[104:105], v[104:105], v[228:229], v[118:119] op_sel_hi:[1,0,1]
	s_nop 0
	v_pk_fma_f32 v[74:75], v[228:229], v[74:75], v[104:105] op_sel:[1,0,0]
	v_mov_b32_e32 v104, v231
	v_pk_fma_f32 v[74:75], v[230:231], v[106:107], v[74:75] op_sel_hi:[0,1,1]
	v_pk_fma_f32 v[104:105], v[104:105], v[72:73], v[74:75] op_sel_hi:[0,1,1]
	ds_read_b128 v[178:181], v238 offset:2176
	ds_read_b128 v[182:185], v238 offset:10384
	s_waitcnt lgkmcnt(8)
	v_pk_fma_f32 v[78:79], v[76:77], v[232:233], v[78:79] op_sel_hi:[1,0,1]
	s_nop 0
	v_pk_fma_f32 v[72:73], v[232:233], v[66:67], v[78:79] op_sel:[1,0,0]
	v_mov_b32_e32 v78, v245
	v_pk_fma_f32 v[72:73], v[234:235], v[82:83], v[72:73] op_sel_hi:[0,1,1]
	v_mov_b32_e32 v74, v235
	v_pk_fma_f32 v[72:73], v[74:75], v[64:65], v[72:73] op_sel_hi:[0,1,1]
	v_pk_fma_f32 v[74:75], v[76:77], v[242:243], v[120:121] op_sel_hi:[1,0,1]
	s_nop 0
	v_pk_fma_f32 v[74:75], v[242:243], v[66:67], v[74:75] op_sel:[1,0,0]
	s_nop 0
	v_pk_fma_f32 v[74:75], v[244:245], v[82:83], v[74:75] op_sel_hi:[0,1,1]
	ds_read_b128 v[186:189], v238 offset:18592
	v_pk_fma_f32 v[106:107], v[78:79], v[64:65], v[74:75] op_sel_hi:[0,1,1]
	s_waitcnt lgkmcnt(8)
; #define LAS __attribute__((address_space(3)))
; __global__ void __launch_bounds__(NTHREADS, 2) hybrid_fwd(Args a) {
;     ...
; #pragma unroll
;                     for (int j = 0; j < 8; ++j) {
; #pragma unroll
;                         for (int e = 0; e < 16; ++e) { const f32x4 w = *(const LAS f32x4*)(rwT + e * 2052 + j * 256 + lane * 4);
;                             acc2[e] += y2[j][0] * (f32x2){w[0], w[0]}; acc2[e] += y2[j][1] * (f32x2){w[1], w[1]};
;                             acc2[e] += y2[j][2] * (f32x2){w[2], w[2]}; acc2[e] += y2[j][3] * (f32x2){w[3], w[3]}; }
;                         __builtin_amdgcn_sched_barrier(0);
;                     }
	v_pk_fma_f32 v[74:75], v[76:77], v[246:247], v[100:101] op_sel_hi:[1,0,1]
	s_nop 0
	v_pk_fma_f32 v[74:75], v[246:247], v[66:67], v[74:75] op_sel:[1,0,0]
	v_mov_b32_e32 v78, v249
	v_pk_fma_f32 v[74:75], v[248:249], v[82:83], v[74:75] op_sel_hi:[0,1,1]
	ds_read_b128 v[198:201], v238 offset:26800
	v_pk_fma_f32 v[74:75], v[78:79], v[64:65], v[74:75] op_sel_hi:[0,1,1]
	s_waitcnt lgkmcnt(8)
	v_pk_fma_f32 v[78:79], v[76:77], v[250:251], v[80:81] op_sel_hi:[1,0,1]
	s_nop 0
	v_pk_fma_f32 v[78:79], v[250:251], v[66:67], v[78:79] op_sel:[1,0,0]
	v_mov_b32_e32 v80, v253
	v_pk_fma_f32 v[78:79], v[252:253], v[82:83], v[78:79] op_sel_hi:[0,1,1]
	ds_read_b128 v[202:205], v238 offset:35008
	v_pk_fma_f32 v[78:79], v[80:81], v[64:65], v[78:79] op_sel_hi:[0,1,1]
	s_waitcnt lgkmcnt(8)
	v_pk_fma_f32 v[80:81], v[76:77], v[162:163], v[84:85] op_sel_hi:[1,0,1]
	s_nop 0
	v_pk_fma_f32 v[80:81], v[162:163], v[66:67], v[80:81] op_sel:[1,0,0]
	v_mov_b32_e32 v84, v165
	v_pk_fma_f32 v[80:81], v[164:165], v[82:83], v[80:81] op_sel_hi:[0,1,1]
	ds_read_b128 v[158:161], v238 offset:51424
	v_pk_fma_f32 v[80:81], v[84:85], v[64:65], v[80:81] op_sel_hi:[0,1,1]
	s_waitcnt lgkmcnt(8)
	v_pk_fma_f32 v[84:85], v[76:77], v[166:167], v[86:87] op_sel_hi:[1,0,1]
	s_nop 0
	v_pk_fma_f32 v[84:85], v[166:167], v[66:67], v[84:85] op_sel:[1,0,0]
	v_mov_b32_e32 v86, v169
	v_pk_fma_f32 v[84:85], v[168:169], v[82:83], v[84:85] op_sel_hi:[0,1,1]
	ds_read_b128 v[216:219], v238 offset:43216
	v_pk_fma_f32 v[84:85], v[86:87], v[64:65], v[84:85] op_sel_hi:[0,1,1]
	s_waitcnt lgkmcnt(8)
	v_pk_fma_f32 v[86:87], v[76:77], v[170:171], v[88:89] op_sel_hi:[1,0,1]
	s_nop 0
	v_pk_fma_f32 v[86:87], v[170:171], v[66:67], v[86:87] op_sel:[1,0,0]
	v_mov_b32_e32 v88, v173
	v_pk_fma_f32 v[86:87], v[172:173], v[82:83], v[86:87] op_sel_hi:[0,1,1]
	ds_read_b128 v[220:223], v238 offset:59632
	v_pk_fma_f32 v[86:87], v[88:89], v[64:65], v[86:87] op_sel_hi:[0,1,1]
	s_waitcnt lgkmcnt(8)
	v_pk_fma_f32 v[88:89], v[76:77], v[174:175], v[90:91] op_sel_hi:[1,0,1]
	s_nop 0
	v_pk_fma_f32 v[88:89], v[174:175], v[66:67], v[88:89] op_sel:[1,0,0]
	v_mov_b32_e32 v90, v177
	v_pk_fma_f32 v[88:89], v[176:177], v[82:83], v[88:89] op_sel_hi:[0,1,1]
	ds_read_b128 v[224:227], v25 offset:3072
	v_pk_fma_f32 v[88:89], v[90:91], v[64:65], v[88:89] op_sel_hi:[0,1,1]
	s_waitcnt lgkmcnt(8)
	v_pk_fma_f32 v[90:91], v[76:77], v[178:179], v[92:93] op_sel_hi:[1,0,1]
	s_nop 0
	v_pk_fma_f32 v[90:91], v[178:179], v[66:67], v[90:91] op_sel:[1,0,0]
	v_mov_b32_e32 v92, v181
	v_pk_fma_f32 v[90:91], v[180:181], v[82:83], v[90:91] op_sel_hi:[0,1,1]
	ds_read_b128 v[228:231], v25 offset:11280
	v_pk_fma_f32 v[90:91], v[92:93], v[64:65], v[90:91] op_sel_hi:[0,1,1]
	s_waitcnt lgkmcnt(8)
	v_pk_fma_f32 v[92:93], v[76:77], v[182:183], v[94:95] op_sel_hi:[1,0,1]
	s_nop 0
	v_pk_fma_f32 v[92:93], v[182:183], v[66:67], v[92:93] op_sel:[1,0,0]
	v_mov_b32_e32 v94, v185
	v_pk_fma_f32 v[92:93], v[184:185], v[82:83], v[92:93] op_sel_hi:[0,1,1]
	ds_read_b128 v[232:235], v25 offset:19488
	v_pk_fma_f32 v[92:93], v[94:95], v[64:65], v[92:93] op_sel_hi:[0,1,1]
	s_waitcnt lgkmcnt(8)
	v_pk_fma_f32 v[94:95], v[76:77], v[186:187], v[96:97] op_sel_hi:[1,0,1]
	s_nop 0
	v_pk_fma_f32 v[94:95], v[186:187], v[66:67], v[94:95] op_sel:[1,0,0]
	v_mov_b32_e32 v96, v189
	v_pk_fma_f32 v[94:95], v[188:189], v[82:83], v[94:95] op_sel_hi:[0,1,1]
	ds_read_b128 v[242:245], v25 offset:27696
	v_pk_fma_f32 v[94:95], v[96:97], v[64:65], v[94:95] op_sel_hi:[0,1,1]
	s_waitcnt lgkmcnt(8)
	v_pk_fma_f32 v[96:97], v[76:77], v[198:199], v[98:99] op_sel_hi:[1,0,1]
	s_nop 0
	v_pk_fma_f32 v[96:97], v[198:199], v[66:67], v[96:97] op_sel:[1,0,0]
	v_mov_b32_e32 v98, v201
	v_pk_fma_f32 v[96:97], v[200:201], v[82:83], v[96:97] op_sel_hi:[0,1,1]
	v_pk_fma_f32 v[96:97], v[98:99], v[64:65], v[96:97] op_sel_hi:[0,1,1]
	ds_read_b128 v[246:249], v25 offset:35904
	ds_read_b128 v[250:253], v25 offset:44112
	s_waitcnt lgkmcnt(8)
	v_pk_fma_f32 v[102:103], v[76:77], v[202:203], v[102:103] op_sel_hi:[1,0,1]
	s_nop 0
	v_pk_fma_f32 v[98:99], v[202:203], v[66:67], v[102:103] op_sel:[1,0,0]
	s_nop 0
	v_pk_fma_f32 v[98:99], v[204:205], v[82:83], v[98:99] op_sel_hi:[0,1,1]
	v_mov_b32_e32 v100, v205
	v_pk_fma_f32 v[98:99], v[100:101], v[64:65], v[98:99] op_sel_hi:[0,1,1]
	ds_read_b128 v[162:165], v25 offset:52320
	s_waitcnt lgkmcnt(8)
	v_pk_fma_f32 v[108:109], v[76:77], v[216:217], v[108:109] op_sel_hi:[1,0,1]
	s_nop 0
	v_pk_fma_f32 v[100:101], v[216:217], v[66:67], v[108:109] op_sel:[1,0,0]
	v_mov_b32_e32 v108, v161
	v_pk_fma_f32 v[100:101], v[218:219], v[82:83], v[100:101] op_sel_hi:[0,1,1]
	v_mov_b32_e32 v102, v219
	v_pk_fma_f32 v[100:101], v[102:103], v[64:65], v[100:101] op_sel_hi:[0,1,1]
	v_pk_fma_f32 v[102:103], v[76:77], v[158:159], v[110:111] op_sel_hi:[1,0,1]
	s_nop 0
	v_pk_fma_f32 v[102:103], v[158:159], v[66:67], v[102:103] op_sel:[1,0,0]
	s_nop 0
	v_pk_fma_f32 v[102:103], v[160:161], v[82:83], v[102:103] op_sel_hi:[0,1,1]
	v_pk_fma_f32 v[102:103], v[108:109], v[64:65], v[102:103] op_sel_hi:[0,1,1]
	ds_read_b128 v[166:169], v25 offset:60528
	s_waitcnt lgkmcnt(8)
	v_pk_fma_f32 v[76:77], v[76:77], v[220:221], v[104:105] op_sel_hi:[1,0,1]
	s_nop 0
	v_pk_fma_f32 v[66:67], v[220:221], v[66:67], v[76:77] op_sel:[1,0,0]
	v_mov_b32_e32 v76, v223
	v_pk_fma_f32 v[66:67], v[222:223], v[82:83], v[66:67] op_sel_hi:[0,1,1]
	v_pk_fma_f32 v[104:105], v[76:77], v[64:65], v[66:67] op_sel_hi:[0,1,1]
	ds_read_b128 v[170:173], v238 offset:3200
	ds_read_b128 v[174:177], v238 offset:11408
	s_waitcnt lgkmcnt(8)
; #define LAS __attribute__((address_space(3)))
; __global__ void __launch_bounds__(NTHREADS, 2) hybrid_fwd(Args a) {
;     ...
; #pragma unroll
;                     for (int j = 0; j < 8; ++j) {
; #pragma unroll
;                         for (int e = 0; e < 16; ++e) { const f32x4 w = *(const LAS f32x4*)(rwT + e * 2052 + j * 256 + lane * 4);
;                             acc2[e] += y2[j][0] * (f32x2){w[0], w[0]}; acc2[e] += y2[j][1] * (f32x2){w[1], w[1]};
;                             acc2[e] += y2[j][2] * (f32x2){w[2], w[2]}; acc2[e] += y2[j][3] * (f32x2){w[3], w[3]}; }
;                         __builtin_amdgcn_sched_barrier(0);
;                     }
	v_pk_fma_f32 v[72:73], v[68:69], v[224:225], v[72:73] op_sel_hi:[1,0,1]
	s_nop 0
	v_pk_fma_f32 v[64:65], v[224:225], v[58:59], v[72:73] op_sel:[1,0,0]
	v_mov_b32_e32 v72, v231
	v_pk_fma_f32 v[64:65], v[226:227], v[70:71], v[64:65] op_sel_hi:[0,1,1]
	v_mov_b32_e32 v66, v227
	v_pk_fma_f32 v[64:65], v[66:67], v[56:57], v[64:65] op_sel_hi:[0,1,1]
	v_pk_fma_f32 v[66:67], v[68:69], v[228:229], v[106:107] op_sel_hi:[1,0,1]
	s_nop 0
	v_pk_fma_f32 v[66:67], v[228:229], v[58:59], v[66:67] op_sel:[1,0,0]
	s_nop 0
	v_pk_fma_f32 v[66:67], v[230:231], v[70:71], v[66:67] op_sel_hi:[0,1,1]
	ds_read_b128 v[178:181], v238 offset:19616
	v_pk_fma_f32 v[106:107], v[72:73], v[56:57], v[66:67] op_sel_hi:[0,1,1]
	s_waitcnt lgkmcnt(8)
	v_pk_fma_f32 v[66:67], v[68:69], v[232:233], v[74:75] op_sel_hi:[1,0,1]
	s_nop 0
	v_pk_fma_f32 v[66:67], v[232:233], v[58:59], v[66:67] op_sel:[1,0,0]
	v_mov_b32_e32 v72, v235
	v_pk_fma_f32 v[66:67], v[234:235], v[70:71], v[66:67] op_sel_hi:[0,1,1]
	v_pk_fma_f32 v[66:67], v[72:73], v[56:57], v[66:67] op_sel_hi:[0,1,1]
	ds_read_b128 v[182:185], v238 offset:27824
	s_waitcnt lgkmcnt(8)
	v_pk_fma_f32 v[76:77], v[68:69], v[242:243], v[78:79] op_sel_hi:[1,0,1]
	s_nop 0
	v_pk_fma_f32 v[72:73], v[242:243], v[58:59], v[76:77] op_sel:[1,0,0]
	s_nop 0
	v_pk_fma_f32 v[72:73], v[244:245], v[70:71], v[72:73] op_sel_hi:[0,1,1]
	v_mov_b32_e32 v74, v245
	v_pk_fma_f32 v[72:73], v[74:75], v[56:57], v[72:73] op_sel_hi:[0,1,1]
	ds_read_b128 v[186:189], v238 offset:36032
	s_waitcnt lgkmcnt(8)
	v_pk_fma_f32 v[78:79], v[68:69], v[246:247], v[80:81] op_sel_hi:[1,0,1]
	s_nop 0
	v_pk_fma_f32 v[74:75], v[246:247], v[58:59], v[78:79] op_sel:[1,0,0]
	s_nop 0
	v_pk_fma_f32 v[74:75], v[248:249], v[70:71], v[74:75] op_sel_hi:[0,1,1]
	v_mov_b32_e32 v76, v249
	v_pk_fma_f32 v[74:75], v[76:77], v[56:57], v[74:75] op_sel_hi:[0,1,1]
	ds_read_b128 v[198:201], v238 offset:44240
	s_waitcnt lgkmcnt(8)
	v_pk_fma_f32 v[80:81], v[68:69], v[250:251], v[84:85] op_sel_hi:[1,0,1]
	s_nop 0
	v_pk_fma_f32 v[76:77], v[250:251], v[58:59], v[80:81] op_sel:[1,0,0]
	s_nop 0
	v_pk_fma_f32 v[76:77], v[252:253], v[70:71], v[76:77] op_sel_hi:[0,1,1]
	v_mov_b32_e32 v78, v253
	v_pk_fma_f32 v[76:77], v[78:79], v[56:57], v[76:77] op_sel_hi:[0,1,1]
	ds_read_b128 v[202:205], v238 offset:52448
	s_waitcnt lgkmcnt(8)
	v_pk_fma_f32 v[82:83], v[68:69], v[162:163], v[86:87] op_sel_hi:[1,0,1]
	s_nop 0
	v_pk_fma_f32 v[78:79], v[162:163], v[58:59], v[82:83] op_sel:[1,0,0]
	s_nop 0
	v_pk_fma_f32 v[78:79], v[164:165], v[70:71], v[78:79] op_sel_hi:[0,1,1]
	v_mov_b32_e32 v80, v165
	v_pk_fma_f32 v[78:79], v[80:81], v[56:57], v[78:79] op_sel_hi:[0,1,1]
	ds_read_b128 v[216:219], v238 offset:60656
	s_waitcnt lgkmcnt(8)
	v_pk_fma_f32 v[84:85], v[68:69], v[166:167], v[88:89] op_sel_hi:[1,0,1]
	s_nop 0
	v_pk_fma_f32 v[80:81], v[166:167], v[58:59], v[84:85] op_sel:[1,0,0]
	s_nop 0
	v_pk_fma_f32 v[80:81], v[168:169], v[70:71], v[80:81] op_sel_hi:[0,1,1]
	v_mov_b32_e32 v82, v169
	v_pk_fma_f32 v[80:81], v[82:83], v[56:57], v[80:81] op_sel_hi:[0,1,1]
	ds_read_b128 v[158:161], v25 offset:4096
	s_waitcnt lgkmcnt(8)
	v_pk_fma_f32 v[86:87], v[68:69], v[170:171], v[90:91] op_sel_hi:[1,0,1]
	s_nop 0
	v_pk_fma_f32 v[82:83], v[170:171], v[58:59], v[86:87] op_sel:[1,0,0]
	s_nop 0
	v_pk_fma_f32 v[82:83], v[172:173], v[70:71], v[82:83] op_sel_hi:[0,1,1]
	v_mov_b32_e32 v84, v173
	v_pk_fma_f32 v[82:83], v[84:85], v[56:57], v[82:83] op_sel_hi:[0,1,1]
	ds_read_b128 v[220:223], v25 offset:12304
	s_waitcnt lgkmcnt(8)
	v_pk_fma_f32 v[88:89], v[68:69], v[174:175], v[92:93] op_sel_hi:[1,0,1]
	s_nop 0
	v_pk_fma_f32 v[84:85], v[174:175], v[58:59], v[88:89] op_sel:[1,0,0]
	s_nop 0
	v_pk_fma_f32 v[84:85], v[176:177], v[70:71], v[84:85] op_sel_hi:[0,1,1]
	v_mov_b32_e32 v86, v177
	v_pk_fma_f32 v[84:85], v[86:87], v[56:57], v[84:85] op_sel_hi:[0,1,1]
	ds_read_b128 v[224:227], v25 offset:20512
	s_waitcnt lgkmcnt(8)
	v_pk_fma_f32 v[90:91], v[68:69], v[178:179], v[94:95] op_sel_hi:[1,0,1]
	s_nop 0
	v_pk_fma_f32 v[86:87], v[178:179], v[58:59], v[90:91] op_sel:[1,0,0]
	s_nop 0
	v_pk_fma_f32 v[86:87], v[180:181], v[70:71], v[86:87] op_sel_hi:[0,1,1]
	v_mov_b32_e32 v88, v181
	v_pk_fma_f32 v[86:87], v[88:89], v[56:57], v[86:87] op_sel_hi:[0,1,1]
	ds_read_b128 v[228:231], v25 offset:28720
	s_waitcnt lgkmcnt(8)
	v_pk_fma_f32 v[92:93], v[68:69], v[182:183], v[96:97] op_sel_hi:[1,0,1]
	s_nop 0
	v_pk_fma_f32 v[88:89], v[182:183], v[58:59], v[92:93] op_sel:[1,0,0]
	s_nop 0
	v_pk_fma_f32 v[88:89], v[184:185], v[70:71], v[88:89] op_sel_hi:[0,1,1]
	v_mov_b32_e32 v90, v185
	v_pk_fma_f32 v[88:89], v[90:91], v[56:57], v[88:89] op_sel_hi:[0,1,1]
	ds_read_b128 v[232:235], v25 offset:36928
	s_waitcnt lgkmcnt(8)
	v_pk_fma_f32 v[94:95], v[68:69], v[186:187], v[98:99] op_sel_hi:[1,0,1]
	s_nop 0
	v_pk_fma_f32 v[90:91], v[186:187], v[58:59], v[94:95] op_sel:[1,0,0]
	s_nop 0
	v_pk_fma_f32 v[90:91], v[188:189], v[70:71], v[90:91] op_sel_hi:[0,1,1]
	v_mov_b32_e32 v92, v189
	v_pk_fma_f32 v[90:91], v[92:93], v[56:57], v[90:91] op_sel_hi:[0,1,1]
	ds_read_b128 v[242:245], v25 offset:45136
	s_waitcnt lgkmcnt(8)
	v_pk_fma_f32 v[96:97], v[68:69], v[198:199], v[100:101] op_sel_hi:[1,0,1]
	s_nop 0
	v_pk_fma_f32 v[92:93], v[198:199], v[58:59], v[96:97] op_sel:[1,0,0]
	s_nop 0
	v_pk_fma_f32 v[92:93], v[200:201], v[70:71], v[92:93] op_sel_hi:[0,1,1]
	v_mov_b32_e32 v94, v201
	v_pk_fma_f32 v[92:93], v[94:95], v[56:57], v[92:93] op_sel_hi:[0,1,1]
	ds_read_b128 v[246:249], v25 offset:53344
	s_waitcnt lgkmcnt(8)
; #define LAS __attribute__((address_space(3)))
; __global__ void __launch_bounds__(NTHREADS, 2) hybrid_fwd(Args a) {
;     ...
; #pragma unroll
;                     for (int j = 0; j < 8; ++j) {
; #pragma unroll
;                         for (int e = 0; e < 16; ++e) { const f32x4 w = *(const LAS f32x4*)(rwT + e * 2052 + j * 256 + lane * 4);
;                             acc2[e] += y2[j][0] * (f32x2){w[0], w[0]}; acc2[e] += y2[j][1] * (f32x2){w[1], w[1]};
;                             acc2[e] += y2[j][2] * (f32x2){w[2], w[2]}; acc2[e] += y2[j][3] * (f32x2){w[3], w[3]}; }
;                         __builtin_amdgcn_sched_barrier(0);
;                     }
	v_pk_fma_f32 v[98:99], v[68:69], v[202:203], v[102:103] op_sel_hi:[1,0,1]
	s_nop 0
	v_pk_fma_f32 v[94:95], v[202:203], v[58:59], v[98:99] op_sel:[1,0,0]
	s_nop 0
	v_pk_fma_f32 v[94:95], v[204:205], v[70:71], v[94:95] op_sel_hi:[0,1,1]
	v_mov_b32_e32 v96, v205
	v_pk_fma_f32 v[94:95], v[96:97], v[56:57], v[94:95] op_sel_hi:[0,1,1]
	ds_read_b128 v[250:253], v25 offset:61552
	s_waitcnt lgkmcnt(8)
	v_pk_fma_f32 v[68:69], v[68:69], v[216:217], v[104:105] op_sel_hi:[1,0,1]
	s_nop 0
	v_pk_fma_f32 v[58:59], v[216:217], v[58:59], v[68:69] op_sel:[1,0,0]
	v_mov_b32_e32 v68, v219
	v_pk_fma_f32 v[58:59], v[218:219], v[70:71], v[58:59] op_sel_hi:[0,1,1]
	v_pk_fma_f32 v[96:97], v[68:69], v[56:57], v[58:59] op_sel_hi:[0,1,1]
	ds_read_b128 v[162:165], v238 offset:4224
	ds_read_b128 v[166:169], v238 offset:12432
	s_waitcnt lgkmcnt(8)
	v_pk_fma_f32 v[64:65], v[60:61], v[158:159], v[64:65] op_sel_hi:[1,0,1]
	s_nop 0
	v_pk_fma_f32 v[56:57], v[158:159], v[54:55], v[64:65] op_sel:[1,0,0]
	v_mov_b32_e32 v64, v223
	v_pk_fma_f32 v[56:57], v[160:161], v[62:63], v[56:57] op_sel_hi:[0,1,1]
	v_mov_b32_e32 v58, v161
	v_pk_fma_f32 v[56:57], v[58:59], v[52:53], v[56:57] op_sel_hi:[0,1,1]
	v_pk_fma_f32 v[58:59], v[60:61], v[220:221], v[106:107] op_sel_hi:[1,0,1]
	s_nop 0
	v_pk_fma_f32 v[58:59], v[220:221], v[54:55], v[58:59] op_sel:[1,0,0]
	s_nop 0
	v_pk_fma_f32 v[58:59], v[222:223], v[62:63], v[58:59] op_sel_hi:[0,1,1]
	ds_read_b128 v[170:173], v238 offset:20640
	v_pk_fma_f32 v[98:99], v[64:65], v[52:53], v[58:59] op_sel_hi:[0,1,1]
	s_waitcnt lgkmcnt(8)
	v_pk_fma_f32 v[58:59], v[60:61], v[224:225], v[66:67] op_sel_hi:[1,0,1]
	s_nop 0
	v_pk_fma_f32 v[58:59], v[224:225], v[54:55], v[58:59] op_sel:[1,0,0]
	v_mov_b32_e32 v64, v227
	v_pk_fma_f32 v[58:59], v[226:227], v[62:63], v[58:59] op_sel_hi:[0,1,1]
	v_pk_fma_f32 v[58:59], v[64:65], v[52:53], v[58:59] op_sel_hi:[0,1,1]
	ds_read_b128 v[174:177], v238 offset:28848
	s_waitcnt lgkmcnt(8)
	v_pk_fma_f32 v[68:69], v[60:61], v[228:229], v[72:73] op_sel_hi:[1,0,1]
	s_nop 0
	v_pk_fma_f32 v[64:65], v[228:229], v[54:55], v[68:69] op_sel:[1,0,0]
	s_nop 0
	v_pk_fma_f32 v[64:65], v[230:231], v[62:63], v[64:65] op_sel_hi:[0,1,1]
	v_mov_b32_e32 v66, v231
	v_pk_fma_f32 v[64:65], v[66:67], v[52:53], v[64:65] op_sel_hi:[0,1,1]
	ds_read_b128 v[178:181], v238 offset:37056
	s_waitcnt lgkmcnt(8)
	v_pk_fma_f32 v[70:71], v[60:61], v[232:233], v[74:75] op_sel_hi:[1,0,1]
	s_nop 0
	v_pk_fma_f32 v[66:67], v[232:233], v[54:55], v[70:71] op_sel:[1,0,0]
	s_nop 0
	v_pk_fma_f32 v[66:67], v[234:235], v[62:63], v[66:67] op_sel_hi:[0,1,1]
	v_mov_b32_e32 v68, v235
	v_pk_fma_f32 v[66:67], v[68:69], v[52:53], v[66:67] op_sel_hi:[0,1,1]
	ds_read_b128 v[182:185], v238 offset:45264
	s_waitcnt lgkmcnt(8)
	v_pk_fma_f32 v[72:73], v[60:61], v[242:243], v[76:77] op_sel_hi:[1,0,1]
	s_nop 0
	v_pk_fma_f32 v[68:69], v[242:243], v[54:55], v[72:73] op_sel:[1,0,0]
	s_nop 0
	v_pk_fma_f32 v[68:69], v[244:245], v[62:63], v[68:69] op_sel_hi:[0,1,1]
	v_mov_b32_e32 v70, v245
	v_pk_fma_f32 v[68:69], v[70:71], v[52:53], v[68:69] op_sel_hi:[0,1,1]
	ds_read_b128 v[186:189], v238 offset:53472
	s_waitcnt lgkmcnt(8)
	v_pk_fma_f32 v[74:75], v[60:61], v[246:247], v[78:79] op_sel_hi:[1,0,1]
	s_nop 0
	v_pk_fma_f32 v[70:71], v[246:247], v[54:55], v[74:75] op_sel:[1,0,0]
	s_nop 0
	v_pk_fma_f32 v[70:71], v[248:249], v[62:63], v[70:71] op_sel_hi:[0,1,1]
	v_mov_b32_e32 v72, v249
	v_pk_fma_f32 v[70:71], v[72:73], v[52:53], v[70:71] op_sel_hi:[0,1,1]
	ds_read_b128 v[198:201], v238 offset:61680
	s_waitcnt lgkmcnt(8)
	v_pk_fma_f32 v[76:77], v[60:61], v[250:251], v[80:81] op_sel_hi:[1,0,1]
	s_nop 0
	v_pk_fma_f32 v[72:73], v[250:251], v[54:55], v[76:77] op_sel:[1,0,0]
	s_nop 0
	v_pk_fma_f32 v[72:73], v[252:253], v[62:63], v[72:73] op_sel_hi:[0,1,1]
	v_mov_b32_e32 v74, v253
	v_pk_fma_f32 v[72:73], v[74:75], v[52:53], v[72:73] op_sel_hi:[0,1,1]
	ds_read_b128 v[202:205], v25 offset:5120
	s_waitcnt lgkmcnt(8)
	v_pk_fma_f32 v[78:79], v[60:61], v[162:163], v[82:83] op_sel_hi:[1,0,1]
	s_nop 0
	v_pk_fma_f32 v[74:75], v[162:163], v[54:55], v[78:79] op_sel:[1,0,0]
	s_nop 0
	v_pk_fma_f32 v[74:75], v[164:165], v[62:63], v[74:75] op_sel_hi:[0,1,1]
	v_mov_b32_e32 v76, v165
	v_pk_fma_f32 v[74:75], v[76:77], v[52:53], v[74:75] op_sel_hi:[0,1,1]
	ds_read_b128 v[216:219], v25 offset:13328
	s_waitcnt lgkmcnt(8)
	v_pk_fma_f32 v[80:81], v[60:61], v[166:167], v[84:85] op_sel_hi:[1,0,1]
	s_nop 0
	v_pk_fma_f32 v[76:77], v[166:167], v[54:55], v[80:81] op_sel:[1,0,0]
	s_nop 0
	v_pk_fma_f32 v[76:77], v[168:169], v[62:63], v[76:77] op_sel_hi:[0,1,1]
	v_mov_b32_e32 v78, v169
	v_pk_fma_f32 v[76:77], v[78:79], v[52:53], v[76:77] op_sel_hi:[0,1,1]
	ds_read_b128 v[158:161], v25 offset:21536
	s_waitcnt lgkmcnt(8)
	v_pk_fma_f32 v[82:83], v[60:61], v[170:171], v[86:87] op_sel_hi:[1,0,1]
	s_nop 0
	v_pk_fma_f32 v[78:79], v[170:171], v[54:55], v[82:83] op_sel:[1,0,0]
	s_nop 0
	v_pk_fma_f32 v[78:79], v[172:173], v[62:63], v[78:79] op_sel_hi:[0,1,1]
	v_mov_b32_e32 v80, v173
	v_pk_fma_f32 v[78:79], v[80:81], v[52:53], v[78:79] op_sel_hi:[0,1,1]
	ds_read_b128 v[220:223], v25 offset:29744
	s_waitcnt lgkmcnt(8)
	v_pk_fma_f32 v[84:85], v[60:61], v[174:175], v[88:89] op_sel_hi:[1,0,1]
	s_nop 0
	v_pk_fma_f32 v[80:81], v[174:175], v[54:55], v[84:85] op_sel:[1,0,0]
	s_nop 0
	v_pk_fma_f32 v[80:81], v[176:177], v[62:63], v[80:81] op_sel_hi:[0,1,1]
	v_mov_b32_e32 v82, v177
	v_pk_fma_f32 v[80:81], v[82:83], v[52:53], v[80:81] op_sel_hi:[0,1,1]
	ds_read_b128 v[224:227], v25 offset:37952
	s_waitcnt lgkmcnt(8)
; #define LAS __attribute__((address_space(3)))
; __global__ void __launch_bounds__(NTHREADS, 2) hybrid_fwd(Args a) {
;     ...
; #pragma unroll
;                     for (int j = 0; j < 8; ++j) {
; #pragma unroll
;                         for (int e = 0; e < 16; ++e) { const f32x4 w = *(const LAS f32x4*)(rwT + e * 2052 + j * 256 + lane * 4);
;                             acc2[e] += y2[j][0] * (f32x2){w[0], w[0]}; acc2[e] += y2[j][1] * (f32x2){w[1], w[1]};
;                             acc2[e] += y2[j][2] * (f32x2){w[2], w[2]}; acc2[e] += y2[j][3] * (f32x2){w[3], w[3]}; }
;                         __builtin_amdgcn_sched_barrier(0);
;                     }
	v_pk_fma_f32 v[86:87], v[60:61], v[178:179], v[90:91] op_sel_hi:[1,0,1]
	s_nop 0
	v_pk_fma_f32 v[82:83], v[178:179], v[54:55], v[86:87] op_sel:[1,0,0]
	s_nop 0
	v_pk_fma_f32 v[82:83], v[180:181], v[62:63], v[82:83] op_sel_hi:[0,1,1]
	v_mov_b32_e32 v84, v181
	v_pk_fma_f32 v[82:83], v[84:85], v[52:53], v[82:83] op_sel_hi:[0,1,1]
	ds_read_b128 v[228:231], v25 offset:46160
	s_waitcnt lgkmcnt(8)
	v_pk_fma_f32 v[88:89], v[60:61], v[182:183], v[92:93] op_sel_hi:[1,0,1]
	s_nop 0
	v_pk_fma_f32 v[84:85], v[182:183], v[54:55], v[88:89] op_sel:[1,0,0]
	s_nop 0
	v_pk_fma_f32 v[84:85], v[184:185], v[62:63], v[84:85] op_sel_hi:[0,1,1]
	v_mov_b32_e32 v86, v185
	v_pk_fma_f32 v[84:85], v[86:87], v[52:53], v[84:85] op_sel_hi:[0,1,1]
	ds_read_b128 v[232:235], v25 offset:54368
	s_waitcnt lgkmcnt(8)
	v_pk_fma_f32 v[90:91], v[60:61], v[186:187], v[94:95] op_sel_hi:[1,0,1]
	s_nop 0
	v_pk_fma_f32 v[86:87], v[186:187], v[54:55], v[90:91] op_sel:[1,0,0]
	s_nop 0
	v_pk_fma_f32 v[86:87], v[188:189], v[62:63], v[86:87] op_sel_hi:[0,1,1]
	v_mov_b32_e32 v88, v189
	v_pk_fma_f32 v[86:87], v[88:89], v[52:53], v[86:87] op_sel_hi:[0,1,1]
	ds_read_b128 v[242:245], v25 offset:62576
	s_waitcnt lgkmcnt(8)
	v_pk_fma_f32 v[60:61], v[60:61], v[198:199], v[96:97] op_sel_hi:[1,0,1]
	s_nop 0
	v_pk_fma_f32 v[54:55], v[198:199], v[54:55], v[60:61] op_sel:[1,0,0]
	v_mov_b32_e32 v60, v201
	v_pk_fma_f32 v[54:55], v[200:201], v[62:63], v[54:55] op_sel_hi:[0,1,1]
	v_pk_fma_f32 v[88:89], v[60:61], v[52:53], v[54:55] op_sel_hi:[0,1,1]
	ds_read_b128 v[246:249], v238 offset:5248
	s_waitcnt lgkmcnt(8)
	v_pk_fma_f32 v[56:57], v[48:49], v[202:203], v[56:57] op_sel_hi:[1,0,1]
	s_nop 0
	v_pk_fma_f32 v[52:53], v[202:203], v[46:47], v[56:57] op_sel:[1,0,0]
	s_nop 0
	v_pk_fma_f32 v[52:53], v[204:205], v[50:51], v[52:53] op_sel_hi:[0,1,1]
	v_mov_b32_e32 v54, v205
	v_pk_fma_f32 v[52:53], v[54:55], v[44:45], v[52:53] op_sel_hi:[0,1,1]
	ds_read_b128 v[250:253], v238 offset:13456
	s_waitcnt lgkmcnt(8)
	v_pk_fma_f32 v[60:61], v[48:49], v[216:217], v[98:99] op_sel_hi:[1,0,1]
	s_nop 0
	v_pk_fma_f32 v[54:55], v[216:217], v[46:47], v[60:61] op_sel:[1,0,0]
	s_nop 0
	v_pk_fma_f32 v[54:55], v[218:219], v[50:51], v[54:55] op_sel_hi:[0,1,1]
	v_mov_b32_e32 v56, v219
	v_pk_fma_f32 v[90:91], v[56:57], v[44:45], v[54:55] op_sel_hi:[0,1,1]
	ds_read_b128 v[162:165], v238 offset:21664
	s_waitcnt lgkmcnt(8)
	v_pk_fma_f32 v[58:59], v[48:49], v[158:159], v[58:59] op_sel_hi:[1,0,1]
	s_nop 0
	v_pk_fma_f32 v[54:55], v[158:159], v[46:47], v[58:59] op_sel:[1,0,0]
	s_nop 0
	v_pk_fma_f32 v[54:55], v[160:161], v[50:51], v[54:55] op_sel_hi:[0,1,1]
	v_mov_b32_e32 v56, v161
	v_pk_fma_f32 v[54:55], v[56:57], v[44:45], v[54:55] op_sel_hi:[0,1,1]
	ds_read_b128 v[166:169], v238 offset:29872
	s_waitcnt lgkmcnt(8)
	v_pk_fma_f32 v[60:61], v[48:49], v[220:221], v[64:65] op_sel_hi:[1,0,1]
	s_nop 0
	v_pk_fma_f32 v[56:57], v[220:221], v[46:47], v[60:61] op_sel:[1,0,0]
	s_nop 0
	v_pk_fma_f32 v[56:57], v[222:223], v[50:51], v[56:57] op_sel_hi:[0,1,1]
	v_mov_b32_e32 v58, v223
	v_pk_fma_f32 v[56:57], v[58:59], v[44:45], v[56:57] op_sel_hi:[0,1,1]
	ds_read_b128 v[170:173], v238 offset:38080
	s_waitcnt lgkmcnt(8)
	v_pk_fma_f32 v[62:63], v[48:49], v[224:225], v[66:67] op_sel_hi:[1,0,1]
	s_nop 0
	v_pk_fma_f32 v[58:59], v[224:225], v[46:47], v[62:63] op_sel:[1,0,0]
	s_nop 0
	v_pk_fma_f32 v[58:59], v[226:227], v[50:51], v[58:59] op_sel_hi:[0,1,1]
	v_mov_b32_e32 v60, v227
	v_pk_fma_f32 v[58:59], v[60:61], v[44:45], v[58:59] op_sel_hi:[0,1,1]
	ds_read_b128 v[174:177], v238 offset:46288
	s_waitcnt lgkmcnt(8)
	v_pk_fma_f32 v[64:65], v[48:49], v[228:229], v[68:69] op_sel_hi:[1,0,1]
	s_nop 0
	v_pk_fma_f32 v[60:61], v[228:229], v[46:47], v[64:65] op_sel:[1,0,0]
	s_nop 0
	v_pk_fma_f32 v[60:61], v[230:231], v[50:51], v[60:61] op_sel_hi:[0,1,1]
	v_mov_b32_e32 v62, v231
	v_pk_fma_f32 v[60:61], v[62:63], v[44:45], v[60:61] op_sel_hi:[0,1,1]
	ds_read_b128 v[178:181], v238 offset:54496
	s_waitcnt lgkmcnt(8)
	v_pk_fma_f32 v[66:67], v[48:49], v[232:233], v[70:71] op_sel_hi:[1,0,1]
	s_nop 0
	v_pk_fma_f32 v[62:63], v[232:233], v[46:47], v[66:67] op_sel:[1,0,0]
	s_nop 0
	v_pk_fma_f32 v[62:63], v[234:235], v[50:51], v[62:63] op_sel_hi:[0,1,1]
	v_mov_b32_e32 v64, v235
	v_pk_fma_f32 v[62:63], v[64:65], v[44:45], v[62:63] op_sel_hi:[0,1,1]
	ds_read_b128 v[182:185], v238 offset:62704
	s_waitcnt lgkmcnt(8)
	v_pk_fma_f32 v[68:69], v[48:49], v[242:243], v[72:73] op_sel_hi:[1,0,1]
	s_nop 0
	v_pk_fma_f32 v[64:65], v[242:243], v[46:47], v[68:69] op_sel:[1,0,0]
	s_nop 0
	v_pk_fma_f32 v[64:65], v[244:245], v[50:51], v[64:65] op_sel_hi:[0,1,1]
	v_mov_b32_e32 v66, v245
	v_pk_fma_f32 v[64:65], v[66:67], v[44:45], v[64:65] op_sel_hi:[0,1,1]
	ds_read_b128 v[186:189], v25 offset:6144
	s_waitcnt lgkmcnt(8)
	v_pk_fma_f32 v[70:71], v[48:49], v[246:247], v[74:75] op_sel_hi:[1,0,1]
	s_nop 0
	v_pk_fma_f32 v[66:67], v[246:247], v[46:47], v[70:71] op_sel:[1,0,0]
	s_nop 0
	v_pk_fma_f32 v[66:67], v[248:249], v[50:51], v[66:67] op_sel_hi:[0,1,1]
	v_mov_b32_e32 v68, v249
	v_pk_fma_f32 v[66:67], v[68:69], v[44:45], v[66:67] op_sel_hi:[0,1,1]
	ds_read_b128 v[198:201], v25 offset:14352
	s_waitcnt lgkmcnt(8)
	v_pk_fma_f32 v[72:73], v[48:49], v[250:251], v[76:77] op_sel_hi:[1,0,1]
	s_nop 0
	v_pk_fma_f32 v[68:69], v[250:251], v[46:47], v[72:73] op_sel:[1,0,0]
	s_nop 0
	v_pk_fma_f32 v[68:69], v[252:253], v[50:51], v[68:69] op_sel_hi:[0,1,1]
	v_mov_b32_e32 v70, v253
	v_pk_fma_f32 v[68:69], v[70:71], v[44:45], v[68:69] op_sel_hi:[0,1,1]
	ds_read_b128 v[202:205], v25 offset:22560
	s_waitcnt lgkmcnt(8)
; #define LAS __attribute__((address_space(3)))
; __global__ void __launch_bounds__(NTHREADS, 2) hybrid_fwd(Args a) {
;     ...
; #pragma unroll
;                     for (int j = 0; j < 8; ++j) {
; #pragma unroll
;                         for (int e = 0; e < 16; ++e) { const f32x4 w = *(const LAS f32x4*)(rwT + e * 2052 + j * 256 + lane * 4);
;                             acc2[e] += y2[j][0] * (f32x2){w[0], w[0]}; acc2[e] += y2[j][1] * (f32x2){w[1], w[1]};
;                             acc2[e] += y2[j][2] * (f32x2){w[2], w[2]}; acc2[e] += y2[j][3] * (f32x2){w[3], w[3]}; }
;                         __builtin_amdgcn_sched_barrier(0);
;                     }
	v_pk_fma_f32 v[74:75], v[48:49], v[162:163], v[78:79] op_sel_hi:[1,0,1]
	s_nop 0
	v_pk_fma_f32 v[70:71], v[162:163], v[46:47], v[74:75] op_sel:[1,0,0]
	s_nop 0
	v_pk_fma_f32 v[70:71], v[164:165], v[50:51], v[70:71] op_sel_hi:[0,1,1]
	v_mov_b32_e32 v72, v165
	v_pk_fma_f32 v[70:71], v[72:73], v[44:45], v[70:71] op_sel_hi:[0,1,1]
	ds_read_b128 v[216:219], v25 offset:30768
	s_waitcnt lgkmcnt(8)
	v_pk_fma_f32 v[76:77], v[48:49], v[166:167], v[80:81] op_sel_hi:[1,0,1]
	s_nop 0
	v_pk_fma_f32 v[72:73], v[166:167], v[46:47], v[76:77] op_sel:[1,0,0]
	s_nop 0
	v_pk_fma_f32 v[72:73], v[168:169], v[50:51], v[72:73] op_sel_hi:[0,1,1]
	v_mov_b32_e32 v74, v169
	v_pk_fma_f32 v[72:73], v[74:75], v[44:45], v[72:73] op_sel_hi:[0,1,1]
	ds_read_b128 v[158:161], v25 offset:38976
	s_waitcnt lgkmcnt(8)
	v_pk_fma_f32 v[78:79], v[48:49], v[170:171], v[82:83] op_sel_hi:[1,0,1]
	s_nop 0
	v_pk_fma_f32 v[74:75], v[170:171], v[46:47], v[78:79] op_sel:[1,0,0]
	s_nop 0
	v_pk_fma_f32 v[74:75], v[172:173], v[50:51], v[74:75] op_sel_hi:[0,1,1]
	v_mov_b32_e32 v76, v173
	v_pk_fma_f32 v[74:75], v[76:77], v[44:45], v[74:75] op_sel_hi:[0,1,1]
	ds_read_b128 v[220:223], v25 offset:47184
	s_waitcnt lgkmcnt(8)
	v_pk_fma_f32 v[80:81], v[48:49], v[174:175], v[84:85] op_sel_hi:[1,0,1]
	s_nop 0
	v_pk_fma_f32 v[76:77], v[174:175], v[46:47], v[80:81] op_sel:[1,0,0]
	s_nop 0
	v_pk_fma_f32 v[76:77], v[176:177], v[50:51], v[76:77] op_sel_hi:[0,1,1]
	v_mov_b32_e32 v78, v177
	v_pk_fma_f32 v[76:77], v[78:79], v[44:45], v[76:77] op_sel_hi:[0,1,1]
	ds_read_b128 v[224:227], v25 offset:55392
	s_waitcnt lgkmcnt(8)
	v_pk_fma_f32 v[82:83], v[48:49], v[178:179], v[86:87] op_sel_hi:[1,0,1]
	s_nop 0
	v_pk_fma_f32 v[78:79], v[178:179], v[46:47], v[82:83] op_sel:[1,0,0]
	s_nop 0
	v_pk_fma_f32 v[78:79], v[180:181], v[50:51], v[78:79] op_sel_hi:[0,1,1]
	v_mov_b32_e32 v80, v181
	v_pk_fma_f32 v[78:79], v[80:81], v[44:45], v[78:79] op_sel_hi:[0,1,1]
	ds_read_b128 v[228:231], v25 offset:63600
	s_waitcnt lgkmcnt(8)
	v_pk_fma_f32 v[48:49], v[48:49], v[182:183], v[88:89] op_sel_hi:[1,0,1]
	s_nop 0
	v_pk_fma_f32 v[46:47], v[182:183], v[46:47], v[48:49] op_sel:[1,0,0]
	v_mov_b32_e32 v48, v185
	v_pk_fma_f32 v[46:47], v[184:185], v[50:51], v[46:47] op_sel_hi:[0,1,1]
	v_pk_fma_f32 v[80:81], v[48:49], v[44:45], v[46:47] op_sel_hi:[0,1,1]
	ds_read_b128 v[232:235], v238 offset:6272
	s_waitcnt lgkmcnt(8)
	v_pk_fma_f32 v[48:49], v[40:41], v[186:187], v[52:53] op_sel_hi:[1,0,1]
	s_nop 0
	v_pk_fma_f32 v[44:45], v[186:187], v[38:39], v[48:49] op_sel:[1,0,0]
	s_nop 0
	v_pk_fma_f32 v[44:45], v[188:189], v[42:43], v[44:45] op_sel_hi:[0,1,1]
	v_mov_b32_e32 v46, v189
	v_pk_fma_f32 v[44:45], v[46:47], v[36:37], v[44:45] op_sel_hi:[0,1,1]
	ds_read_b128 v[242:245], v238 offset:14480
	s_waitcnt lgkmcnt(8)
	v_pk_fma_f32 v[50:51], v[40:41], v[198:199], v[90:91] op_sel_hi:[1,0,1]
	s_nop 0
	v_pk_fma_f32 v[46:47], v[198:199], v[38:39], v[50:51] op_sel:[1,0,0]
	s_nop 0
	v_pk_fma_f32 v[46:47], v[200:201], v[42:43], v[46:47] op_sel_hi:[0,1,1]
	v_mov_b32_e32 v48, v201
	v_pk_fma_f32 v[82:83], v[48:49], v[36:37], v[46:47] op_sel_hi:[0,1,1]
	ds_read_b128 v[246:249], v238 offset:22688
	s_waitcnt lgkmcnt(8)
	v_pk_fma_f32 v[50:51], v[40:41], v[202:203], v[54:55] op_sel_hi:[1,0,1]
	s_nop 0
	v_pk_fma_f32 v[46:47], v[202:203], v[38:39], v[50:51] op_sel:[1,0,0]
	s_nop 0
	v_pk_fma_f32 v[46:47], v[204:205], v[42:43], v[46:47] op_sel_hi:[0,1,1]
	v_mov_b32_e32 v48, v205
	v_pk_fma_f32 v[46:47], v[48:49], v[36:37], v[46:47] op_sel_hi:[0,1,1]
	ds_read_b128 v[250:253], v238 offset:30896
	s_waitcnt lgkmcnt(8)
	v_pk_fma_f32 v[52:53], v[40:41], v[216:217], v[56:57] op_sel_hi:[1,0,1]
	s_nop 0
	v_pk_fma_f32 v[48:49], v[216:217], v[38:39], v[52:53] op_sel:[1,0,0]
	s_nop 0
	v_pk_fma_f32 v[48:49], v[218:219], v[42:43], v[48:49] op_sel_hi:[0,1,1]
	v_mov_b32_e32 v50, v219
	v_pk_fma_f32 v[48:49], v[50:51], v[36:37], v[48:49] op_sel_hi:[0,1,1]
	ds_read_b128 v[162:165], v238 offset:39104
	s_waitcnt lgkmcnt(8)
	v_pk_fma_f32 v[54:55], v[40:41], v[158:159], v[58:59] op_sel_hi:[1,0,1]
	s_nop 0
	v_pk_fma_f32 v[50:51], v[158:159], v[38:39], v[54:55] op_sel:[1,0,0]
	s_nop 0
	v_pk_fma_f32 v[50:51], v[160:161], v[42:43], v[50:51] op_sel_hi:[0,1,1]
	v_mov_b32_e32 v52, v161
	v_pk_fma_f32 v[50:51], v[52:53], v[36:37], v[50:51] op_sel_hi:[0,1,1]
	ds_read_b128 v[166:169], v238 offset:47312
	s_waitcnt lgkmcnt(8)
	v_pk_fma_f32 v[56:57], v[40:41], v[220:221], v[60:61] op_sel_hi:[1,0,1]
	s_nop 0
	v_pk_fma_f32 v[52:53], v[220:221], v[38:39], v[56:57] op_sel:[1,0,0]
	s_nop 0
	v_pk_fma_f32 v[52:53], v[222:223], v[42:43], v[52:53] op_sel_hi:[0,1,1]
	v_mov_b32_e32 v54, v223
	v_pk_fma_f32 v[52:53], v[54:55], v[36:37], v[52:53] op_sel_hi:[0,1,1]
	ds_read_b128 v[170:173], v238 offset:55520
	s_waitcnt lgkmcnt(8)
	v_pk_fma_f32 v[58:59], v[40:41], v[224:225], v[62:63] op_sel_hi:[1,0,1]
	s_nop 0
	v_pk_fma_f32 v[54:55], v[224:225], v[38:39], v[58:59] op_sel:[1,0,0]
	s_nop 0
	v_pk_fma_f32 v[54:55], v[226:227], v[42:43], v[54:55] op_sel_hi:[0,1,1]
	v_mov_b32_e32 v56, v227
	v_pk_fma_f32 v[54:55], v[56:57], v[36:37], v[54:55] op_sel_hi:[0,1,1]
	ds_read_b128 v[174:177], v238 offset:63728
	s_waitcnt lgkmcnt(8)
	v_pk_fma_f32 v[60:61], v[40:41], v[228:229], v[64:65] op_sel_hi:[1,0,1]
	s_nop 0
	v_pk_fma_f32 v[56:57], v[228:229], v[38:39], v[60:61] op_sel:[1,0,0]
	s_nop 0
	v_pk_fma_f32 v[56:57], v[230:231], v[42:43], v[56:57] op_sel_hi:[0,1,1]
	v_mov_b32_e32 v58, v231
	v_pk_fma_f32 v[56:57], v[58:59], v[36:37], v[56:57] op_sel_hi:[0,1,1]
	ds_read_b128 v[178:181], v25 offset:7168
	s_waitcnt lgkmcnt(8)
; #define LAS __attribute__((address_space(3)))
; __global__ void __launch_bounds__(NTHREADS, 2) hybrid_fwd(Args a) {
;     ...
; #pragma unroll
;                     for (int j = 0; j < 8; ++j) {
; #pragma unroll
;                         for (int e = 0; e < 16; ++e) { const f32x4 w = *(const LAS f32x4*)(rwT + e * 2052 + j * 256 + lane * 4);
;                             acc2[e] += y2[j][0] * (f32x2){w[0], w[0]}; acc2[e] += y2[j][1] * (f32x2){w[1], w[1]};
;                             acc2[e] += y2[j][2] * (f32x2){w[2], w[2]}; acc2[e] += y2[j][3] * (f32x2){w[3], w[3]}; }
;                         __builtin_amdgcn_sched_barrier(0);
;                     }
	v_pk_fma_f32 v[62:63], v[40:41], v[232:233], v[66:67] op_sel_hi:[1,0,1]
	s_nop 0
	v_pk_fma_f32 v[58:59], v[232:233], v[38:39], v[62:63] op_sel:[1,0,0]
	s_nop 0
	v_pk_fma_f32 v[58:59], v[234:235], v[42:43], v[58:59] op_sel_hi:[0,1,1]
	v_mov_b32_e32 v60, v235
	v_pk_fma_f32 v[58:59], v[60:61], v[36:37], v[58:59] op_sel_hi:[0,1,1]
	ds_read_b128 v[182:185], v25 offset:15376
	s_waitcnt lgkmcnt(8)
	v_pk_fma_f32 v[64:65], v[40:41], v[242:243], v[68:69] op_sel_hi:[1,0,1]
	s_nop 0
	v_pk_fma_f32 v[60:61], v[242:243], v[38:39], v[64:65] op_sel:[1,0,0]
	s_nop 0
	v_pk_fma_f32 v[60:61], v[244:245], v[42:43], v[60:61] op_sel_hi:[0,1,1]
	v_mov_b32_e32 v62, v245
	v_pk_fma_f32 v[60:61], v[62:63], v[36:37], v[60:61] op_sel_hi:[0,1,1]
	ds_read_b128 v[186:189], v25 offset:23584
	s_waitcnt lgkmcnt(8)
	v_pk_fma_f32 v[66:67], v[40:41], v[246:247], v[70:71] op_sel_hi:[1,0,1]
	s_nop 0
	v_pk_fma_f32 v[62:63], v[246:247], v[38:39], v[66:67] op_sel:[1,0,0]
	s_nop 0
	v_pk_fma_f32 v[62:63], v[248:249], v[42:43], v[62:63] op_sel_hi:[0,1,1]
	v_mov_b32_e32 v64, v249
	v_pk_fma_f32 v[62:63], v[64:65], v[36:37], v[62:63] op_sel_hi:[0,1,1]
	ds_read_b128 v[198:201], v25 offset:31792
	s_waitcnt lgkmcnt(8)
	v_pk_fma_f32 v[68:69], v[40:41], v[250:251], v[72:73] op_sel_hi:[1,0,1]
	s_nop 0
	v_pk_fma_f32 v[64:65], v[250:251], v[38:39], v[68:69] op_sel:[1,0,0]
	s_nop 0
	v_pk_fma_f32 v[64:65], v[252:253], v[42:43], v[64:65] op_sel_hi:[0,1,1]
	v_mov_b32_e32 v66, v253
	v_pk_fma_f32 v[64:65], v[66:67], v[36:37], v[64:65] op_sel_hi:[0,1,1]
	ds_read_b128 v[202:205], v25 offset:40000
	s_waitcnt lgkmcnt(8)
	v_pk_fma_f32 v[70:71], v[40:41], v[162:163], v[74:75] op_sel_hi:[1,0,1]
	s_nop 0
	v_pk_fma_f32 v[66:67], v[162:163], v[38:39], v[70:71] op_sel:[1,0,0]
	s_nop 0
	v_pk_fma_f32 v[66:67], v[164:165], v[42:43], v[66:67] op_sel_hi:[0,1,1]
	v_mov_b32_e32 v68, v165
	v_pk_fma_f32 v[66:67], v[68:69], v[36:37], v[66:67] op_sel_hi:[0,1,1]
	ds_read_b128 v[216:219], v25 offset:48208
	s_waitcnt lgkmcnt(8)
	v_pk_fma_f32 v[72:73], v[40:41], v[166:167], v[76:77] op_sel_hi:[1,0,1]
	s_nop 0
	v_pk_fma_f32 v[68:69], v[166:167], v[38:39], v[72:73] op_sel:[1,0,0]
	s_nop 0
	v_pk_fma_f32 v[68:69], v[168:169], v[42:43], v[68:69] op_sel_hi:[0,1,1]
	v_mov_b32_e32 v70, v169
	v_pk_fma_f32 v[68:69], v[70:71], v[36:37], v[68:69] op_sel_hi:[0,1,1]
	ds_read_b128 v[158:161], v25 offset:56416
	s_waitcnt lgkmcnt(8)
	v_pk_fma_f32 v[74:75], v[40:41], v[170:171], v[78:79] op_sel_hi:[1,0,1]
	s_nop 0
	v_pk_fma_f32 v[70:71], v[170:171], v[38:39], v[74:75] op_sel:[1,0,0]
	s_nop 0
	v_pk_fma_f32 v[70:71], v[172:173], v[42:43], v[70:71] op_sel_hi:[0,1,1]
	v_mov_b32_e32 v72, v173
	v_pk_fma_f32 v[70:71], v[72:73], v[36:37], v[70:71] op_sel_hi:[0,1,1]
	ds_read_b128 v[220:223], v25 offset:64624
	s_waitcnt lgkmcnt(8)
	v_pk_fma_f32 v[40:41], v[40:41], v[174:175], v[80:81] op_sel_hi:[1,0,1]
	s_nop 0
	v_pk_fma_f32 v[38:39], v[174:175], v[38:39], v[40:41] op_sel:[1,0,0]
	v_mov_b32_e32 v40, v177
	v_pk_fma_f32 v[38:39], v[176:177], v[42:43], v[38:39] op_sel_hi:[0,1,1]
	v_pk_fma_f32 v[72:73], v[40:41], v[36:37], v[38:39] op_sel_hi:[0,1,1]
	ds_read_b128 v[224:227], v238 offset:7296
	s_waitcnt lgkmcnt(8)
	v_pk_fma_f32 v[40:41], v[22:23], v[178:179], v[44:45] op_sel_hi:[1,0,1]
	s_nop 0
	v_pk_fma_f32 v[36:37], v[178:179], v[18:19], v[40:41] op_sel:[1,0,0]
	s_nop 0
	v_pk_fma_f32 v[36:37], v[180:181], v[20:21], v[36:37] op_sel_hi:[0,1,1]
	v_mov_b32_e32 v38, v181
	v_pk_fma_f32 v[36:37], v[38:39], v[16:17], v[36:37] op_sel_hi:[0,1,1]
	ds_read_b128 v[228:231], v238 offset:15504
	s_waitcnt lgkmcnt(8)
	v_pk_fma_f32 v[42:43], v[22:23], v[182:183], v[82:83] op_sel_hi:[1,0,1]
	s_nop 0
	v_pk_fma_f32 v[38:39], v[182:183], v[18:19], v[42:43] op_sel:[1,0,0]
	s_nop 0
	v_pk_fma_f32 v[38:39], v[184:185], v[20:21], v[38:39] op_sel_hi:[0,1,1]
	v_mov_b32_e32 v40, v185
	v_pk_fma_f32 v[38:39], v[40:41], v[16:17], v[38:39] op_sel_hi:[0,1,1]
	ds_read_b128 v[232:235], v238 offset:23712
	s_waitcnt lgkmcnt(8)
	v_pk_fma_f32 v[44:45], v[22:23], v[186:187], v[46:47] op_sel_hi:[1,0,1]
	s_nop 0
	v_pk_fma_f32 v[40:41], v[186:187], v[18:19], v[44:45] op_sel:[1,0,0]
	s_nop 0
	v_pk_fma_f32 v[40:41], v[188:189], v[20:21], v[40:41] op_sel_hi:[0,1,1]
	v_mov_b32_e32 v42, v189
	v_pk_fma_f32 v[40:41], v[42:43], v[16:17], v[40:41] op_sel_hi:[0,1,1]
	ds_read_b128 v[242:245], v238 offset:31920
	s_waitcnt lgkmcnt(8)
	v_pk_fma_f32 v[46:47], v[22:23], v[198:199], v[48:49] op_sel_hi:[1,0,1]
	s_nop 0
	v_pk_fma_f32 v[42:43], v[198:199], v[18:19], v[46:47] op_sel:[1,0,0]
	ds_read_b128 v[246:249], v238 offset:40128
	v_pk_fma_f32 v[42:43], v[200:201], v[20:21], v[42:43] op_sel_hi:[0,1,1]
	v_mov_b32_e32 v44, v201
	v_pk_fma_f32 v[44:45], v[44:45], v[16:17], v[42:43] op_sel_hi:[0,1,1]
	s_waitcnt lgkmcnt(8)
	v_pk_fma_f32 v[42:43], v[22:23], v[202:203], v[50:51] op_sel_hi:[1,0,1]
	s_nop 0
	v_pk_fma_f32 v[42:43], v[202:203], v[18:19], v[42:43] op_sel:[1,0,0]
	v_mov_b32_e32 v46, v205
	v_pk_fma_f32 v[42:43], v[204:205], v[20:21], v[42:43] op_sel_hi:[0,1,1]
	v_pk_fma_f32 v[42:43], v[46:47], v[16:17], v[42:43] op_sel_hi:[0,1,1]
	ds_read_b128 v[250:253], v238 offset:48336
	s_waitcnt lgkmcnt(8)
	v_pk_fma_f32 v[50:51], v[22:23], v[216:217], v[52:53] op_sel_hi:[1,0,1]
	s_nop 0
	v_pk_fma_f32 v[46:47], v[216:217], v[18:19], v[50:51] op_sel:[1,0,0]
	s_nop 0
	v_pk_fma_f32 v[46:47], v[218:219], v[20:21], v[46:47] op_sel_hi:[0,1,1]
	v_mov_b32_e32 v48, v219
	v_pk_fma_f32 v[46:47], v[48:49], v[16:17], v[46:47] op_sel_hi:[0,1,1]
	ds_read_b128 v[162:165], v238 offset:56544
	s_waitcnt lgkmcnt(8)
; #define LAS __attribute__((address_space(3)))
; #define WS_STEP(ctrl) v += __int_as_float(__builtin_amdgcn_update_dpp(0, __float_as_int(v), (ctrl), 0xf, 0xf, true))
; __device__ __forceinline__ float wave_sum(float v) {
;     ...
;     WS_STEP(0xB1); WS_STEP(0x4E); WS_STEP(0x124); WS_STEP(0x128);
;     ...
;     const auto r16 = __builtin_amdgcn_permlane16_swap(__float_as_uint(v), __float_as_uint(v), false, false);
;     v = __uint_as_float(r16[0]) + __uint_as_float(r16[1]);
;     const auto rr = __builtin_amdgcn_permlane32_swap(__float_as_uint(v), __float_as_uint(v), false, false);
;     return __uint_as_float(rr[0]) + __uint_as_float(rr[1]);
; __global__ void __launch_bounds__(NTHREADS, 2) hybrid_fwd(Args a) {
;     ...
;                     for (int j = 0; j < 8; ++j) {
; #pragma unroll
;                         for (int e = 0; e < 16; ++e) { const f32x4 w = *(const LAS f32x4*)(rwT + e * 2052 + j * 256 + lane * 4);
;                             acc2[e] += y2[j][0] * (f32x2){w[0], w[0]}; acc2[e] += y2[j][1] * (f32x2){w[1], w[1]};
;                             acc2[e] += y2[j][2] * (f32x2){w[2], w[2]}; acc2[e] += y2[j][3] * (f32x2){w[3], w[3]}; }
;                         __builtin_amdgcn_sched_barrier(0);
;                     }
;                     float acca[16], accb[16];
; #pragma unroll
;                     for (int e = 0; e < 16; ++e) { acca[e] = acc2[e][0]; accb[e] = acc2[e][1]; }
	v_pk_fma_f32 v[52:53], v[22:23], v[158:159], v[54:55] op_sel_hi:[1,0,1]
	s_nop 0
	v_pk_fma_f32 v[48:49], v[158:159], v[18:19], v[52:53] op_sel:[1,0,0]
	s_nop 0
	v_pk_fma_f32 v[48:49], v[160:161], v[20:21], v[48:49] op_sel_hi:[0,1,1]
	v_mov_b32_e32 v50, v161
	v_pk_fma_f32 v[48:49], v[50:51], v[16:17], v[48:49] op_sel_hi:[0,1,1]
	ds_read_b128 v[166:169], v238 offset:64752
	s_waitcnt lgkmcnt(8)
	v_pk_fma_f32 v[54:55], v[22:23], v[220:221], v[56:57] op_sel_hi:[1,0,1]
	s_nop 0
	v_pk_fma_f32 v[50:51], v[220:221], v[18:19], v[54:55] op_sel:[1,0,0]
	s_nop 0
	v_pk_fma_f32 v[50:51], v[222:223], v[20:21], v[50:51] op_sel_hi:[0,1,1]
	v_mov_b32_e32 v52, v223
	v_pk_fma_f32 v[50:51], v[52:53], v[16:17], v[50:51] op_sel_hi:[0,1,1]
	s_waitcnt lgkmcnt(7)
	v_pk_fma_f32 v[56:57], v[22:23], v[224:225], v[58:59] op_sel_hi:[1,0,1]
	s_nop 0
	v_pk_fma_f32 v[52:53], v[224:225], v[18:19], v[56:57] op_sel:[1,0,0]
	s_nop 0
	v_pk_fma_f32 v[52:53], v[226:227], v[20:21], v[52:53] op_sel_hi:[0,1,1]
	v_mov_b32_e32 v54, v227
	v_pk_fma_f32 v[52:53], v[54:55], v[16:17], v[52:53] op_sel_hi:[0,1,1]
	s_waitcnt lgkmcnt(6)
	v_pk_fma_f32 v[58:59], v[22:23], v[228:229], v[60:61] op_sel_hi:[1,0,1]
	s_nop 0
	v_pk_fma_f32 v[54:55], v[228:229], v[18:19], v[58:59] op_sel:[1,0,0]
	s_nop 0
	v_pk_fma_f32 v[54:55], v[230:231], v[20:21], v[54:55] op_sel_hi:[0,1,1]
	v_mov_b32_e32 v56, v231
	v_pk_fma_f32 v[54:55], v[56:57], v[16:17], v[54:55] op_sel_hi:[0,1,1]
	s_waitcnt lgkmcnt(5)
	v_pk_fma_f32 v[60:61], v[22:23], v[232:233], v[62:63] op_sel_hi:[1,0,1]
	s_nop 0
	v_pk_fma_f32 v[56:57], v[232:233], v[18:19], v[60:61] op_sel:[1,0,0]
	s_nop 0
	v_pk_fma_f32 v[56:57], v[234:235], v[20:21], v[56:57] op_sel_hi:[0,1,1]
	v_mov_b32_e32 v58, v235
	v_pk_fma_f32 v[56:57], v[58:59], v[16:17], v[56:57] op_sel_hi:[0,1,1]
	s_waitcnt lgkmcnt(4)
	v_pk_fma_f32 v[62:63], v[22:23], v[242:243], v[64:65] op_sel_hi:[1,0,1]
	s_nop 0
	v_pk_fma_f32 v[58:59], v[242:243], v[18:19], v[62:63] op_sel:[1,0,0]
	s_nop 0
	v_pk_fma_f32 v[58:59], v[244:245], v[20:21], v[58:59] op_sel_hi:[0,1,1]
	v_mov_b32_e32 v60, v245
	v_pk_fma_f32 v[58:59], v[60:61], v[16:17], v[58:59] op_sel_hi:[0,1,1]
	s_waitcnt lgkmcnt(3)
	v_pk_fma_f32 v[64:65], v[22:23], v[246:247], v[66:67] op_sel_hi:[1,0,1]
	s_nop 0
	v_pk_fma_f32 v[60:61], v[246:247], v[18:19], v[64:65] op_sel:[1,0,0]
	s_nop 0
	v_pk_fma_f32 v[60:61], v[248:249], v[20:21], v[60:61] op_sel_hi:[0,1,1]
	v_mov_b32_e32 v62, v249
	v_pk_fma_f32 v[60:61], v[62:63], v[16:17], v[60:61] op_sel_hi:[0,1,1]
	s_waitcnt lgkmcnt(2)
	v_pk_fma_f32 v[66:67], v[22:23], v[250:251], v[68:69] op_sel_hi:[1,0,1]
	s_nop 0
	v_pk_fma_f32 v[62:63], v[250:251], v[18:19], v[66:67] op_sel:[1,0,0]
	s_nop 0
	v_pk_fma_f32 v[62:63], v[252:253], v[20:21], v[62:63] op_sel_hi:[0,1,1]
	v_mov_b32_e32 v64, v253
	v_pk_fma_f32 v[62:63], v[64:65], v[16:17], v[62:63] op_sel_hi:[0,1,1]
	s_waitcnt lgkmcnt(1)
	v_pk_fma_f32 v[68:69], v[22:23], v[162:163], v[70:71] op_sel_hi:[1,0,1]
	s_nop 0
	v_pk_fma_f32 v[64:65], v[162:163], v[18:19], v[68:69] op_sel:[1,0,0]
	s_nop 0
	v_pk_fma_f32 v[64:65], v[164:165], v[20:21], v[64:65] op_sel_hi:[0,1,1]
	v_mov_b32_e32 v66, v165
	v_pk_fma_f32 v[64:65], v[66:67], v[16:17], v[64:65] op_sel_hi:[0,1,1]
	s_waitcnt lgkmcnt(0)
	v_pk_fma_f32 v[22:23], v[22:23], v[166:167], v[72:73] op_sel_hi:[1,0,1]
	s_nop 0
	v_pk_fma_f32 v[18:19], v[166:167], v[18:19], v[22:23] op_sel:[1,0,0]
	s_nop 0
	v_pk_fma_f32 v[18:19], v[168:169], v[20:21], v[18:19] op_sel_hi:[0,1,1]
	v_mov_b32_e32 v20, v169
	v_pk_fma_f32 v[16:17], v[20:21], v[16:17], v[18:19] op_sel_hi:[0,1,1]
	s_nop 1
	v_permlane32_swap_b32_e32 v16, v17
	v_permlane32_swap_b32_e32 v36, v37
	v_permlane32_swap_b32_e32 v38, v39
	v_permlane32_swap_b32_e32 v40, v41
	v_permlane32_swap_b32_e32 v42, v43
	v_permlane32_swap_b32_e32 v44, v45
	v_permlane32_swap_b32_e32 v46, v47
	v_permlane32_swap_b32_e32 v48, v49
	v_permlane32_swap_b32_e32 v50, v51
	v_permlane32_swap_b32_e32 v52, v53
	v_permlane32_swap_b32_e32 v54, v55
	v_permlane32_swap_b32_e32 v56, v57
	v_permlane32_swap_b32_e32 v58, v59
	v_permlane32_swap_b32_e32 v60, v61
	v_permlane32_swap_b32_e32 v62, v63
	v_permlane32_swap_b32_e32 v64, v65
	v_add_f32_e32 v16, v16, v17
	v_add_f32_e32 v36, v36, v37
	v_add_f32_e32 v38, v38, v39
	v_add_f32_e32 v40, v40, v41
	v_add_f32_e32 v42, v42, v43
	v_add_f32_e32 v44, v44, v45
	v_add_f32_e32 v46, v46, v47
	v_add_f32_e32 v48, v48, v49
	v_add_f32_e32 v50, v50, v51
	v_add_f32_e32 v52, v52, v53
	v_add_f32_e32 v54, v54, v55
	v_add_f32_e32 v56, v56, v57
	v_add_f32_e32 v58, v58, v59
	v_add_f32_e32 v60, v60, v61
	v_add_f32_e32 v62, v62, v63
	v_add_f32_e32 v64, v64, v65
	s_nop 1
	v_add_f32_dpp v18, v36, v36 quad_perm:[1,0,3,2] row_mask:0xf bank_mask:0xf bound_ctrl:1
	s_nop 0
	v_add_f32_dpp v16, v16, v16 quad_perm:[1,0,3,2] row_mask:0xf bank_mask:0xf bound_ctrl:1
	v_add_f32_dpp v36, v62, v62 quad_perm:[1,0,3,2] row_mask:0xf bank_mask:0xf bound_ctrl:1
	v_add_f32_dpp v18, v18, v18 quad_perm:[2,3,0,1] row_mask:0xf bank_mask:0xf bound_ctrl:1
	v_add_f32_dpp v16, v16, v16 quad_perm:[2,3,0,1] row_mask:0xf bank_mask:0xf bound_ctrl:1
	v_add_f32_dpp v36, v36, v36 quad_perm:[2,3,0,1] row_mask:0xf bank_mask:0xf bound_ctrl:1
	v_add_f32_dpp v18, v18, v18 row_ror:4 row_mask:0xf bank_mask:0xf bound_ctrl:1
	v_add_f32_dpp v16, v16, v16 row_ror:4 row_mask:0xf bank_mask:0xf bound_ctrl:1
	v_add_f32_dpp v36, v36, v36 row_ror:4 row_mask:0xf bank_mask:0xf bound_ctrl:1
	v_add_f32_dpp v18, v18, v18 row_ror:8 row_mask:0xf bank_mask:0xf bound_ctrl:1
	v_mov_b32_e32 v19, v18
	s_nop 1
	v_permlane16_swap_b32_e32 v18, v19
	v_add_f32_e32 v18, v18, v19
	v_mov_b32_e32 v19, v18
	s_nop 1
	s_nop 0
	v_mov_b32_e32 v18, v18
	s_nop 0
; #define WS_STEP(ctrl) v += __int_as_float(__builtin_amdgcn_update_dpp(0, __float_as_int(v), (ctrl), 0xf, 0xf, true))
; __device__ __forceinline__ float wave_sum(float v) {
;     ...
;     WS_STEP(0xB1); WS_STEP(0x4E); WS_STEP(0x124); WS_STEP(0x128);
;     ...
;     const auto r16 = __builtin_amdgcn_permlane16_swap(__float_as_uint(v), __float_as_uint(v), false, false);
;     v = __uint_as_float(r16[0]) + __uint_as_float(r16[1]);
;     const auto rr = __builtin_amdgcn_permlane32_swap(__float_as_uint(v), __float_as_uint(v), false, false);
;     return __uint_as_float(rr[0]) + __uint_as_float(rr[1]);
; }
; __device__ __forceinline__ float sigmoidf_(float x) { return __builtin_amdgcn_rcpf(1.f + __expf(-x)); }
	v_add_f32_dpp v19, v38, v38 quad_perm:[1,0,3,2] row_mask:0xf bank_mask:0xf bound_ctrl:1
	v_mul_f32_e32 v18, 0xbfb8aa3b, v18
	v_exp_f32_e32 v18, v18
	v_add_f32_dpp v19, v19, v19 quad_perm:[2,3,0,1] row_mask:0xf bank_mask:0xf bound_ctrl:1
	v_add_f32_dpp v16, v16, v16 row_ror:8 row_mask:0xf bank_mask:0xf bound_ctrl:1
	v_add_f32_dpp v36, v36, v36 row_ror:8 row_mask:0xf bank_mask:0xf bound_ctrl:1
	v_add_f32_dpp v19, v19, v19 row_ror:4 row_mask:0xf bank_mask:0xf bound_ctrl:1
	v_add_f32_e32 v18, 1.0, v18
	v_rcp_f32_e32 v18, v18
	v_add_f32_dpp v19, v19, v19 row_ror:8 row_mask:0xf bank_mask:0xf bound_ctrl:1
	v_mov_b32_e32 v20, v19
	s_nop 1
	v_permlane16_swap_b32_e32 v19, v20
	v_add_f32_e32 v19, v19, v20
	v_mov_b32_e32 v20, v19
	s_nop 1
	s_nop 0
	v_mov_b32_e32 v19, v19
	s_nop 0
	v_add_f32_dpp v20, v40, v40 quad_perm:[1,0,3,2] row_mask:0xf bank_mask:0xf bound_ctrl:1
	v_mul_f32_e32 v19, 0xbfb8aa3b, v19
	v_exp_f32_e32 v19, v19
	v_add_f32_dpp v20, v20, v20 quad_perm:[2,3,0,1] row_mask:0xf bank_mask:0xf bound_ctrl:1
	v_add_f32_dpp v40, v64, v64 quad_perm:[1,0,3,2] row_mask:0xf bank_mask:0xf bound_ctrl:1
	v_mov_b32_e32 v38, v36
	v_add_f32_dpp v20, v20, v20 row_ror:4 row_mask:0xf bank_mask:0xf bound_ctrl:1
	v_add_f32_e32 v19, 1.0, v19
	v_rcp_f32_e32 v19, v19
	v_add_f32_dpp v20, v20, v20 row_ror:8 row_mask:0xf bank_mask:0xf bound_ctrl:1
	v_mov_b32_e32 v21, v20
	s_nop 1
	v_permlane16_swap_b32_e32 v20, v21
	v_add_f32_e32 v20, v20, v21
	v_mov_b32_e32 v21, v20
	s_nop 1
	s_nop 0
	v_mov_b32_e32 v20, v20
	s_nop 0
	v_add_f32_dpp v21, v44, v44 quad_perm:[1,0,3,2] row_mask:0xf bank_mask:0xf bound_ctrl:1
	v_mul_f32_e32 v20, 0xbfb8aa3b, v20
	v_exp_f32_e32 v20, v20
	v_add_f32_dpp v21, v21, v21 quad_perm:[2,3,0,1] row_mask:0xf bank_mask:0xf bound_ctrl:1
	v_mov_b32_e32 v44, v16
	s_nop 1
	v_permlane16_swap_b32_e32 v16, v44
	v_add_f32_dpp v21, v21, v21 row_ror:4 row_mask:0xf bank_mask:0xf bound_ctrl:1
	v_add_f32_e32 v20, 1.0, v20
	v_rcp_f32_e32 v70, v20
	v_add_f32_dpp v21, v21, v21 row_ror:8 row_mask:0xf bank_mask:0xf bound_ctrl:1
	v_mov_b32_e32 v22, v21
	s_nop 1
	v_permlane16_swap_b32_e32 v21, v22
	v_add_f32_e32 v21, v21, v22
	v_mov_b32_e32 v22, v21
	s_nop 1
	s_nop 0
	v_mov_b32_e32 v21, v21
	s_nop 0
	v_add_f32_dpp v22, v42, v42 quad_perm:[1,0,3,2] row_mask:0xf bank_mask:0xf bound_ctrl:1
	v_mul_f32_e32 v21, 0xbfb8aa3b, v21
	v_exp_f32_e32 v21, v21
	v_add_f32_dpp v22, v22, v22 quad_perm:[2,3,0,1] row_mask:0xf bank_mask:0xf bound_ctrl:1
	v_add_f32_e32 v79, v14, v70
	v_add_f32_e32 v44, v16, v44
	v_add_f32_dpp v22, v22, v22 row_ror:4 row_mask:0xf bank_mask:0xf bound_ctrl:1
	v_add_f32_e32 v20, 1.0, v21
	v_rcp_f32_e32 v72, v20
	v_add_f32_dpp v22, v22, v22 row_ror:8 row_mask:0xf bank_mask:0xf bound_ctrl:1
	v_mov_b32_e32 v23, v22
	s_nop 1
	v_permlane16_swap_b32_e32 v22, v23
	v_add_f32_e32 v69, v22, v23
	s_nop 0
	v_add_f32_dpp v22, v46, v46 quad_perm:[1,0,3,2] row_mask:0xf bank_mask:0xf bound_ctrl:1
	v_pk_add_f32 v[20:21], v[12:13], v[18:19]
	v_add_f32_e32 v80, v15, v72
	v_add_f32_dpp v22, v22, v22 quad_perm:[2,3,0,1] row_mask:0xf bank_mask:0xf bound_ctrl:1
	v_cmp_gt_f32_e32 vcc, v21, v20
	v_add_f32_dpp v40, v40, v40 quad_perm:[2,3,0,1] row_mask:0xf bank_mask:0xf bound_ctrl:1
	v_add_f32_dpp v22, v22, v22 row_ror:4 row_mask:0xf bank_mask:0xf bound_ctrl:1
	v_cndmask_b32_e32 v16, v20, v21, vcc
	v_cmp_gt_f32_e64 s[6:7], v79, v16
	v_add_f32_dpp v22, v22, v22 row_ror:8 row_mask:0xf bank_mask:0xf bound_ctrl:1
	v_mov_b32_e32 v23, v22
	s_nop 1
	v_permlane16_swap_b32_e32 v22, v23
	v_add_f32_e32 v73, v22, v23
	s_nop 0
	v_add_f32_dpp v22, v48, v48 quad_perm:[1,0,3,2] row_mask:0xf bank_mask:0xf bound_ctrl:1
	v_cndmask_b32_e64 v48, 0, 1, vcc
	v_cndmask_b32_e64 v16, v16, v79, s[6:7]
	v_add_f32_dpp v22, v22, v22 quad_perm:[2,3,0,1] row_mask:0xf bank_mask:0xf bound_ctrl:1
	v_cndmask_b32_e64 v48, v48, 2, s[6:7]
	v_cmp_ngt_f32_e64 s[8:9], v80, v16
	v_add_f32_dpp v22, v22, v22 row_ror:4 row_mask:0xf bank_mask:0xf bound_ctrl:1
	v_add_f32_dpp v40, v40, v40 row_ror:4 row_mask:0xf bank_mask:0xf bound_ctrl:1
	v_permlane16_swap_b32_e32 v36, v38
	v_add_f32_dpp v22, v22, v22 row_ror:8 row_mask:0xf bank_mask:0xf bound_ctrl:1
	v_mov_b32_e32 v23, v22
	s_nop 1
	v_permlane16_swap_b32_e32 v22, v23
	v_add_f32_e32 v75, v22, v23
	s_nop 0
	v_add_f32_dpp v22, v50, v50 quad_perm:[1,0,3,2] row_mask:0xf bank_mask:0xf bound_ctrl:1
	v_add_f32_dpp v40, v40, v40 row_ror:8 row_mask:0xf bank_mask:0xf bound_ctrl:1
	v_mov_b32_e32 v42, v40
	v_add_f32_dpp v22, v22, v22 quad_perm:[2,3,0,1] row_mask:0xf bank_mask:0xf bound_ctrl:1
	s_nop 0
	v_permlane16_swap_b32_e32 v40, v42
	v_add_f32_dpp v22, v22, v22 row_ror:4 row_mask:0xf bank_mask:0xf bound_ctrl:1
	v_add_f32_e32 v36, v36, v38
	v_add_f32_e32 v40, v40, v42
	v_add_f32_dpp v22, v22, v22 row_ror:8 row_mask:0xf bank_mask:0xf bound_ctrl:1
	v_mov_b32_e32 v23, v22
	s_nop 1
	v_permlane16_swap_b32_e32 v22, v23
	v_add_f32_e32 v77, v22, v23
	s_nop 0
	v_add_f32_dpp v22, v52, v52 quad_perm:[1,0,3,2] row_mask:0xf bank_mask:0xf bound_ctrl:1
	v_cndmask_b32_e64 v62, v80, v16, s[8:9]
	v_mov_b32_e32 v71, v69
	v_add_f32_dpp v22, v22, v22 quad_perm:[2,3,0,1] row_mask:0xf bank_mask:0xf bound_ctrl:1
	v_mov_b32_e32 v74, v73
	v_mov_b32_e32 v76, v75
	v_add_f32_dpp v22, v22, v22 row_ror:4 row_mask:0xf bank_mask:0xf bound_ctrl:1
	v_mov_b32_e32 v78, v77
	v_mov_b32_e32 v38, v36
	v_add_f32_dpp v22, v22, v22 row_ror:8 row_mask:0xf bank_mask:0xf bound_ctrl:1
	v_mov_b32_e32 v23, v22
	s_nop 1
	v_permlane16_swap_b32_e32 v22, v23
	v_add_f32_e32 v50, v22, v23
	s_nop 0
	v_add_f32_dpp v22, v54, v54 quad_perm:[1,0,3,2] row_mask:0xf bank_mask:0xf bound_ctrl:1
	v_mov_b32_e32 v52, v50
	v_mov_b32_e32 v42, v40
	v_add_f32_dpp v22, v22, v22 quad_perm:[2,3,0,1] row_mask:0xf bank_mask:0xf bound_ctrl:1
	v_mov_b32_e32 v46, v44
	s_nop 0
	v_add_f32_dpp v22, v22, v22 row_ror:4 row_mask:0xf bank_mask:0xf bound_ctrl:1
	s_nop 0
	s_nop 0
	v_add_f32_dpp v22, v22, v22 row_ror:8 row_mask:0xf bank_mask:0xf bound_ctrl:1
	v_mov_b32_e32 v23, v22
	s_nop 1
	v_permlane16_swap_b32_e32 v22, v23
	v_add_f32_e32 v54, v22, v23
	s_nop 0
	v_add_f32_dpp v22, v56, v56 quad_perm:[1,0,3,2] row_mask:0xf bank_mask:0xf bound_ctrl:1
	v_mov_b32_e32 v66, v54
	s_nop 0
	v_add_f32_dpp v22, v22, v22 quad_perm:[2,3,0,1] row_mask:0xf bank_mask:0xf bound_ctrl:1
	s_nop 0
	s_nop 0
	v_add_f32_dpp v22, v22, v22 row_ror:4 row_mask:0xf bank_mask:0xf bound_ctrl:1
	s_nop 0
	s_nop 0
	v_add_f32_dpp v22, v22, v22 row_ror:8 row_mask:0xf bank_mask:0xf bound_ctrl:1
	v_mov_b32_e32 v23, v22
	s_nop 1
	v_permlane16_swap_b32_e32 v22, v23
	v_add_f32_e32 v56, v22, v23
	s_nop 0
	v_add_f32_dpp v22, v58, v58 quad_perm:[1,0,3,2] row_mask:0xf bank_mask:0xf bound_ctrl:1
	v_mov_b32_e32 v67, v56
	s_nop 0
	v_add_f32_dpp v22, v22, v22 quad_perm:[2,3,0,1] row_mask:0xf bank_mask:0xf bound_ctrl:1
	s_nop 0
	s_nop 0
	v_add_f32_dpp v22, v22, v22 row_ror:4 row_mask:0xf bank_mask:0xf bound_ctrl:1
	s_nop 0
	s_nop 0
	v_add_f32_dpp v22, v22, v22 row_ror:8 row_mask:0xf bank_mask:0xf bound_ctrl:1
	v_mov_b32_e32 v23, v22
	s_nop 1
	v_permlane16_swap_b32_e32 v22, v23
	v_add_f32_e32 v58, v22, v23
	s_nop 0
	v_add_f32_dpp v22, v60, v60 quad_perm:[1,0,3,2] row_mask:0xf bank_mask:0xf bound_ctrl:1
	v_cndmask_b32_e64 v60, 3, v48, s[8:9]
	v_mov_b32_e32 v48, 0xff800000
	v_cmp_eq_u32_e64 s[10:11], 0, v60
	v_cmp_nlg_f32_e64 s[12:13], v20, v48
	s_or_b64 s[10:11], s[10:11], s[12:13]
	v_cndmask_b32_e64 v20, v20, v48, s[10:11]
	v_cmp_ne_u32_e64 s[12:13], 1, v60
	v_cmp_gt_f32_e64 s[14:15], v21, v20
	s_and_b64 s[12:13], s[12:13], s[14:15]
	v_cndmask_b32_e64 v20, v20, v21, s[12:13]
	v_add_f32_dpp v22, v22, v22 quad_perm:[2,3,0,1] row_mask:0xf bank_mask:0xf bound_ctrl:1
	v_cmp_ne_u32_e64 s[14:15], 2, v60
	v_cmp_gt_f32_e64 s[16:17], v79, v20
	v_add_f32_dpp v22, v22, v22 row_ror:4 row_mask:0xf bank_mask:0xf bound_ctrl:1
	s_and_b64 s[14:15], s[14:15], s[16:17]
	v_cndmask_b32_e64 v20, v20, v79, s[14:15]
	v_add_f32_dpp v22, v22, v22 row_ror:8 row_mask:0xf bank_mask:0xf bound_ctrl:1
	v_mov_b32_e32 v23, v22
	v_cmp_gt_f32_e64 s[16:17], v80, v20
	s_nop 0
	v_permlane16_swap_b32_e32 v22, v23
	s_and_b64 s[16:17], s[8:9], s[16:17]
	v_add_f32_e32 v22, v22, v23
	v_cndmask_b32_e64 v20, v20, v80, s[16:17]
	v_mov_b32_e32 v68, v58
	v_mov_b32_e32 v23, v22
	v_add_f32_e32 v62, v62, v20
	s_nop 0
	s_nop 0
	s_nop 0
	s_nop 0
	v_mov_b32_e32 v16, 1
	v_cmp_lg_f32_e64 s[18:19], v62, v48
	v_mov_b32_e32 v21, 0
	v_mov_b32_e32 v20, 0
	s_and_saveexec_b64 s[38:39], s[18:19]
	s_cbranch_execz .LBB0_911
	v_cndmask_b32_e64 v20, v18, 0, s[10:11]
	v_cndmask_b32_e64 v16, 0, 1, s[12:13]
	v_cndmask_b32_e64 v20, v20, v19, s[12:13]
	v_cndmask_b32_e32 v18, v18, v19, vcc
	v_cndmask_b32_e64 v16, v16, 2, s[14:15]
	v_cndmask_b32_e64 v20, v20, v70, s[14:15]
	v_cndmask_b32_e64 v18, v18, v70, s[6:7]
	v_cndmask_b32_e64 v16, v16, 3, s[16:17]
	v_cndmask_b32_e64 v35, v20, v72, s[16:17]
	v_cndmask_b32_e64 v21, v72, v18, s[8:9]
	v_mov_b32_e32 v20, v60
	v_mov_b32_e32 v48, v62
